# nt hints on the prologue's (P0) f32->bf16 weight conversion loads and stores (read-once f32 sources; bf16 weights first read behind the grid barrier)
# speedup vs baseline: 1.0087x; 1.0011x over previous
.LBB0_35:
	s_sext_i32_i16 s31, s5
	v_mov_b32_e32 v184, 0
	v_mov_b32_e32 v185, 0
	v_mov_b32_e32 v186, 0
	v_mov_b32_e32 v187, 0
	v_mov_b32_e32 v188, 0
	v_mov_b32_e32 v189, 0
	v_mov_b32_e32 v190, 0
	v_mov_b32_e32 v191, 0
	v_mov_b32_e32 v176, 0
	v_mov_b32_e32 v177, 0
	v_mov_b32_e32 v178, 0
	v_mov_b32_e32 v179, 0
	v_mov_b32_e32 v180, 0
	v_mov_b32_e32 v181, 0
	v_mov_b32_e32 v182, 0
	v_mov_b32_e32 v183, 0
	v_mov_b32_e32 v168, 0
	v_mov_b32_e32 v169, 0
	v_mov_b32_e32 v170, 0
	v_mov_b32_e32 v171, 0
	v_mov_b32_e32 v172, 0
	v_mov_b32_e32 v173, 0
	v_mov_b32_e32 v174, 0
	v_mov_b32_e32 v175, 0
	v_mov_b32_e32 v152, 0
	v_mov_b32_e32 v153, 0
	v_mov_b32_e32 v154, 0
	v_mov_b32_e32 v155, 0
	v_mov_b32_e32 v160, 0
	v_mov_b32_e32 v161, 0
	v_mov_b32_e32 v162, 0
	v_mov_b32_e32 v163, 0
	v_mov_b32_e32 v156, 0
	v_mov_b32_e32 v157, 0
	v_mov_b32_e32 v158, 0
	v_mov_b32_e32 v159, 0
	v_mov_b32_e32 v164, 0
	v_mov_b32_e32 v165, 0
	v_mov_b32_e32 v166, 0
	v_mov_b32_e32 v167, 0
	v_mov_b32_e32 v144, 0
	v_mov_b32_e32 v145, 0
	v_mov_b32_e32 v146, 0
	v_mov_b32_e32 v147, 0
	v_mov_b32_e32 v148, 0
	v_mov_b32_e32 v149, 0
	v_mov_b32_e32 v150, 0
	v_mov_b32_e32 v151, 0
	v_mov_b32_e32 v136, 0
	v_mov_b32_e32 v137, 0
	v_mov_b32_e32 v138, 0
	v_mov_b32_e32 v139, 0
	v_mov_b32_e32 v140, 0
	v_mov_b32_e32 v141, 0
	v_mov_b32_e32 v142, 0
	v_mov_b32_e32 v143, 0
	v_mov_b32_e32 v128, 0
	v_mov_b32_e32 v129, 0
	v_mov_b32_e32 v130, 0
	v_mov_b32_e32 v131, 0
	v_mov_b32_e32 v132, 0
	v_mov_b32_e32 v133, 0
	v_mov_b32_e32 v134, 0
	v_mov_b32_e32 v135, 0
	s_and_saveexec_b64 s[2:3], s[14:15]
	s_cbranch_execz .LBB0_37
	v_readlane_b32 s40, v252, 4
	v_readlane_b32 s44, v252, 8
	v_readlane_b32 s45, v252, 9
	v_lshl_add_u32 v130, s31, 6, v193
	s_ashr_i32 s5, s4, 31
	v_mov_b64_e32 v[128:129], s[44:45]
	v_mad_i64_i32 v[128:129], s[14:15], v130, s25, v[128:129]
	v_lshl_add_u64 v[128:129], s[4:5], 2, v[128:129]
	v_lshlrev_b32_e32 v130, 2, v196
	v_mov_b32_e32 v131, v195
	v_lshl_add_u64 v[184:185], v[128:129], 0, v[130:131]
	v_add_co_u32_e32 v128, vcc, 0x7000, v184
	v_readlane_b32 s41, v252, 5
	s_nop 0
	v_addc_co_u32_e32 v129, vcc, 0, v185, vcc
	v_add_co_u32_e32 v136, vcc, 0xe000, v184
	global_load_dwordx4 v[132:135], v[184:185], off nt
	s_nop 0
	global_load_dwordx4 v[128:131], v[128:129], off offset:1120 nt
	v_addc_co_u32_e32 v137, vcc, 0, v185, vcc
	v_add_co_u32_e32 v138, vcc, 0x15000, v184
	v_readlane_b32 s42, v252, 6
	s_nop 0
	v_addc_co_u32_e32 v139, vcc, 0, v185, vcc
	v_add_co_u32_e32 v144, vcc, 0x1d000, v184
	global_load_dwordx4 v[140:143], v[136:137], off offset:2240 nt
	s_nop 0
	global_load_dwordx4 v[136:139], v[138:139], off offset:3360 nt
	v_addc_co_u32_e32 v145, vcc, 0, v185, vcc
	v_add_co_u32_e32 v146, vcc, 0x24000, v184
	v_readlane_b32 s43, v252, 7
	s_nop 0
	v_addc_co_u32_e32 v147, vcc, 0, v185, vcc
	v_add_co_u32_e32 v152, vcc, 0x2b000, v184
	global_load_dwordx4 v[148:151], v[144:145], off offset:384 nt
	s_nop 0
	global_load_dwordx4 v[144:147], v[146:147], off offset:1504 nt
	v_addc_co_u32_e32 v153, vcc, 0, v185, vcc
	v_add_co_u32_e32 v154, vcc, 0x32000, v184
	v_readlane_b32 s46, v252, 10
	s_nop 0
	v_addc_co_u32_e32 v155, vcc, 0, v185, vcc
	global_load_dwordx4 v[164:167], v[152:153], off offset:2624 nt
	global_load_dwordx4 v[156:159], v[154:155], off offset:3744 nt
	v_add_co_u32_e32 v152, vcc, 0x3a000, v184
	v_readlane_b32 s47, v252, 11
	s_nop 0
	v_addc_co_u32_e32 v153, vcc, 0, v185, vcc
	v_add_co_u32_e32 v154, vcc, 0x41000, v184
	v_readlane_b32 s48, v252, 12
	s_nop 0
	v_addc_co_u32_e32 v155, vcc, 0, v185, vcc
	v_add_co_u32_e32 v168, vcc, 0x48000, v184
	global_load_dwordx4 v[160:163], v[152:153], off offset:768 nt
	s_nop 0
	global_load_dwordx4 v[152:155], v[154:155], off offset:1888 nt
	v_addc_co_u32_e32 v169, vcc, 0, v185, vcc
	v_add_co_u32_e32 v170, vcc, 0x50000, v184
	v_readlane_b32 s49, v252, 13
	s_nop 0
	v_addc_co_u32_e32 v171, vcc, 0, v185, vcc
	v_add_co_u32_e32 v176, vcc, 0x57000, v184
	global_load_dwordx4 v[172:175], v[168:169], off offset:3008 nt
	s_nop 0
	global_load_dwordx4 v[168:171], v[170:171], off offset:32 nt
	v_addc_co_u32_e32 v177, vcc, 0, v185, vcc
	v_add_co_u32_e32 v178, vcc, 0x5e000, v184
	v_readlane_b32 s50, v252, 14
	s_nop 0
	v_addc_co_u32_e32 v179, vcc, 0, v185, vcc
	v_add_co_u32_e32 v186, vcc, 0x65000, v184
	global_load_dwordx4 v[180:183], v[176:177], off offset:1152 nt
	s_nop 0
	global_load_dwordx4 v[176:179], v[178:179], off offset:2272 nt
	v_addc_co_u32_e32 v187, vcc, 0, v185, vcc
	v_add_co_u32_e32 v184, vcc, 0x6d000, v184
	v_readlane_b32 s51, v252, 15
	s_nop 0
	v_addc_co_u32_e32 v185, vcc, 0, v185, vcc
	global_load_dwordx4 v[188:191], v[186:187], off offset:3392 nt
	s_nop 0
	global_load_dwordx4 v[184:187], v[184:185], off offset:416 nt
	v_readlane_b32 s52, v252, 16
	v_readlane_b32 s53, v252, 17
	v_readlane_b32 s54, v252, 18
	v_readlane_b32 s55, v252, 19

.LBB0_60:
	v_mov_b32_e32 v3, 0
	v_mov_b32_e32 v2, 0
	v_mov_b32_e32 v1, 0
	v_mov_b32_e32 v0, 0
	v_mov_b32_e32 v7, 0
	v_mov_b32_e32 v6, 0
	v_mov_b32_e32 v5, 0
	v_mov_b32_e32 v4, 0
	v_mov_b32_e32 v11, 0
	v_mov_b32_e32 v10, 0
	v_mov_b32_e32 v9, 0
	v_mov_b32_e32 v8, 0
	v_mov_b32_e32 v15, 0
	v_mov_b32_e32 v14, 0
	v_mov_b32_e32 v13, 0
	v_mov_b32_e32 v12, 0
	v_mov_b32_e32 v19, 0
	v_mov_b32_e32 v18, 0
	v_mov_b32_e32 v17, 0
	v_mov_b32_e32 v16, 0
	v_mov_b32_e32 v23, 0
	v_mov_b32_e32 v22, 0
	v_mov_b32_e32 v21, 0
	v_mov_b32_e32 v20, 0
	v_mov_b32_e32 v27, 0
	v_mov_b32_e32 v26, 0
	v_mov_b32_e32 v25, 0
	v_mov_b32_e32 v24, 0
	v_mov_b32_e32 v31, 0
	v_mov_b32_e32 v30, 0
	v_mov_b32_e32 v29, 0
	v_mov_b32_e32 v28, 0
	v_mov_b32_e32 v35, 0
	v_mov_b32_e32 v34, 0
	v_mov_b32_e32 v33, 0
	v_mov_b32_e32 v32, 0
	v_mov_b32_e32 v39, 0
	v_mov_b32_e32 v38, 0
	v_mov_b32_e32 v37, 0
	v_mov_b32_e32 v36, 0
	v_mov_b32_e32 v47, 0
	v_mov_b32_e32 v46, 0
	v_mov_b32_e32 v45, 0
	v_mov_b32_e32 v44, 0
	v_mov_b32_e32 v51, 0
	v_mov_b32_e32 v50, 0
	v_mov_b32_e32 v49, 0
	v_mov_b32_e32 v48, 0
	v_mov_b32_e32 v59, 0
	v_mov_b32_e32 v58, 0
	v_mov_b32_e32 v57, 0
	v_mov_b32_e32 v56, 0
	v_mov_b32_e32 v67, 0
	v_mov_b32_e32 v66, 0
	v_mov_b32_e32 v65, 0
	v_mov_b32_e32 v64, 0
	v_mov_b32_e32 v75, 0
	v_mov_b32_e32 v74, 0
	v_mov_b32_e32 v73, 0
	v_mov_b32_e32 v72, 0
	v_mov_b32_e32 v79, 0
	v_mov_b32_e32 v78, 0
	v_mov_b32_e32 v77, 0
	v_mov_b32_e32 v76, 0
	s_and_saveexec_b64 s[2:3], s[16:17]
	s_cbranch_execz .LBB0_62
	v_readlane_b32 s40, v252, 4
	s_sext_i32_i16 s15, s15
	v_readlane_b32 s44, v252, 8
	v_readlane_b32 s45, v252, 9
	v_lshl_add_u32 v2, s15, 6, v193
	s_ashr_i32 s15, s14, 31
	v_mov_b64_e32 v[0:1], s[44:45]
	v_mad_i64_i32 v[0:1], s[16:17], v2, s25, v[0:1]
	v_lshl_add_u64 v[0:1], s[14:15], 2, v[0:1]
	v_lshlrev_b32_e32 v2, 2, v196
	v_mov_b32_e32 v3, v195
	v_lshl_add_u64 v[72:73], v[0:1], 0, v[2:3]
	v_add_co_u32_e32 v4, vcc, 0x7000, v72
	v_readlane_b32 s41, v252, 5
	s_nop 0
	v_addc_co_u32_e32 v5, vcc, 0, v73, vcc
	v_add_co_u32_e32 v8, vcc, 0xe000, v72
	global_load_dwordx4 v[0:3], v[72:73], off nt
	s_nop 0
	global_load_dwordx4 v[4:7], v[4:5], off offset:1120 nt
	v_addc_co_u32_e32 v9, vcc, 0, v73, vcc
	v_add_co_u32_e32 v12, vcc, 0x15000, v72
	v_readlane_b32 s42, v252, 6
	s_nop 0
	v_addc_co_u32_e32 v13, vcc, 0, v73, vcc
	v_add_co_u32_e32 v16, vcc, 0x1d000, v72
	global_load_dwordx4 v[8:11], v[8:9], off offset:2240 nt
	s_nop 0
	global_load_dwordx4 v[12:15], v[12:13], off offset:3360 nt
	v_addc_co_u32_e32 v17, vcc, 0, v73, vcc
	v_add_co_u32_e32 v20, vcc, 0x24000, v72
	v_readlane_b32 s43, v252, 7
	s_nop 0
	v_addc_co_u32_e32 v21, vcc, 0, v73, vcc
	v_add_co_u32_e32 v24, vcc, 0x2b000, v72
	global_load_dwordx4 v[16:19], v[16:17], off offset:384 nt
	s_nop 0
	global_load_dwordx4 v[20:23], v[20:21], off offset:1504 nt
	v_addc_co_u32_e32 v25, vcc, 0, v73, vcc
	v_add_co_u32_e32 v28, vcc, 0x32000, v72
	v_readlane_b32 s46, v252, 10
	s_nop 0
	v_addc_co_u32_e32 v29, vcc, 0, v73, vcc
	v_add_co_u32_e32 v32, vcc, 0x3a000, v72
	global_load_dwordx4 v[24:27], v[24:25], off offset:2624 nt
	s_nop 0
	global_load_dwordx4 v[28:31], v[28:29], off offset:3744 nt
	v_addc_co_u32_e32 v33, vcc, 0, v73, vcc
	v_add_co_u32_e32 v36, vcc, 0x41000, v72
	v_readlane_b32 s47, v252, 11
	s_nop 0
	v_addc_co_u32_e32 v37, vcc, 0, v73, vcc
	v_add_co_u32_e32 v44, vcc, 0x48000, v72
	global_load_dwordx4 v[32:35], v[32:33], off offset:768 nt
	s_nop 0
	global_load_dwordx4 v[36:39], v[36:37], off offset:1888 nt
	v_addc_co_u32_e32 v45, vcc, 0, v73, vcc
	v_add_co_u32_e32 v48, vcc, 0x50000, v72
	v_readlane_b32 s48, v252, 12
	s_nop 0
	v_addc_co_u32_e32 v49, vcc, 0, v73, vcc
	v_add_co_u32_e32 v56, vcc, 0x57000, v72
	global_load_dwordx4 v[44:47], v[44:45], off offset:3008 nt
	s_nop 0
	global_load_dwordx4 v[48:51], v[48:49], off offset:32 nt
	v_addc_co_u32_e32 v57, vcc, 0, v73, vcc
	v_add_co_u32_e32 v64, vcc, 0x5e000, v72
	v_readlane_b32 s49, v252, 13
	s_nop 0
	v_addc_co_u32_e32 v65, vcc, 0, v73, vcc
	v_add_co_u32_e32 v74, vcc, 0x65000, v72
	global_load_dwordx4 v[56:59], v[56:57], off offset:1152 nt
	s_nop 0
	global_load_dwordx4 v[64:67], v[64:65], off offset:2272 nt
	v_addc_co_u32_e32 v75, vcc, 0, v73, vcc
	v_add_co_u32_e32 v76, vcc, 0x6d000, v72
	v_readlane_b32 s50, v252, 14
	s_nop 0
	v_addc_co_u32_e32 v77, vcc, 0, v73, vcc
	global_load_dwordx4 v[72:75], v[74:75], off offset:3392 nt
	s_nop 0
	global_load_dwordx4 v[76:79], v[76:77], off offset:416 nt
	v_readlane_b32 s51, v252, 15
	v_readlane_b32 s52, v252, 16
	v_readlane_b32 s53, v252, 17
	v_readlane_b32 s54, v252, 18
	v_readlane_b32 s55, v252, 19

.LBB0_86:
	v_mov_b32_e32 v43, 0
	v_mov_b32_e32 v42, 0
	v_mov_b32_e32 v41, 0
	v_mov_b32_e32 v40, 0
	v_mov_b32_e32 v55, 0
	v_mov_b32_e32 v54, 0
	v_mov_b32_e32 v53, 0
	v_mov_b32_e32 v52, 0
	v_mov_b32_e32 v63, 0
	v_mov_b32_e32 v62, 0
	v_mov_b32_e32 v61, 0
	v_mov_b32_e32 v60, 0
	v_mov_b32_e32 v71, 0
	v_mov_b32_e32 v70, 0
	v_mov_b32_e32 v69, 0
	v_mov_b32_e32 v68, 0
	v_mov_b32_e32 v83, 0
	v_mov_b32_e32 v82, 0
	v_mov_b32_e32 v81, 0
	v_mov_b32_e32 v80, 0
	v_mov_b32_e32 v87, 0
	v_mov_b32_e32 v86, 0
	v_mov_b32_e32 v85, 0
	v_mov_b32_e32 v84, 0
	v_mov_b32_e32 v91, 0
	v_mov_b32_e32 v90, 0
	v_mov_b32_e32 v89, 0
	v_mov_b32_e32 v88, 0
	v_mov_b32_e32 v95, 0
	v_mov_b32_e32 v94, 0
	v_mov_b32_e32 v93, 0
	v_mov_b32_e32 v92, 0
	v_mov_b32_e32 v99, 0
	v_mov_b32_e32 v98, 0
	v_mov_b32_e32 v97, 0
	v_mov_b32_e32 v96, 0
	v_mov_b32_e32 v103, 0
	v_mov_b32_e32 v102, 0
	v_mov_b32_e32 v101, 0
	v_mov_b32_e32 v100, 0
	v_mov_b32_e32 v107, 0
	v_mov_b32_e32 v106, 0
	v_mov_b32_e32 v105, 0
	v_mov_b32_e32 v104, 0
	v_mov_b32_e32 v111, 0
	v_mov_b32_e32 v110, 0
	v_mov_b32_e32 v109, 0
	v_mov_b32_e32 v108, 0
	v_mov_b32_e32 v115, 0
	v_mov_b32_e32 v114, 0
	v_mov_b32_e32 v113, 0
	v_mov_b32_e32 v112, 0
	v_mov_b32_e32 v119, 0
	v_mov_b32_e32 v118, 0
	v_mov_b32_e32 v117, 0
	v_mov_b32_e32 v116, 0
	v_mov_b32_e32 v123, 0
	v_mov_b32_e32 v122, 0
	v_mov_b32_e32 v121, 0
	v_mov_b32_e32 v120, 0
	v_mov_b32_e32 v127, 0
	v_mov_b32_e32 v126, 0
	v_mov_b32_e32 v125, 0
	v_mov_b32_e32 v124, 0
	s_and_saveexec_b64 s[14:15], s[18:19]
	s_cbranch_execz .LBB0_88
	v_readlane_b32 s44, v252, 4
	s_sext_i32_i16 s17, s17
	v_readlane_b32 s48, v252, 8
	v_readlane_b32 s49, v252, 9
	v_lshl_add_u32 v42, s17, 6, v193
	s_ashr_i32 s17, s16, 31
	v_mov_b64_e32 v[40:41], s[48:49]
	v_mad_i64_i32 v[40:41], s[18:19], v42, s25, v[40:41]
	v_lshl_add_u64 v[40:41], s[16:17], 2, v[40:41]
	v_lshlrev_b32_e32 v42, 2, v196
	v_mov_b32_e32 v43, v195
	v_lshl_add_u64 v[120:121], v[40:41], 0, v[42:43]
	v_add_co_u32_e32 v52, vcc, 0x7000, v120
	v_readlane_b32 s45, v252, 5
	s_nop 0
	v_addc_co_u32_e32 v53, vcc, 0, v121, vcc
	v_add_co_u32_e32 v60, vcc, 0xe000, v120
	global_load_dwordx4 v[40:43], v[120:121], off nt
	s_nop 0
	global_load_dwordx4 v[52:55], v[52:53], off offset:1120 nt
	v_addc_co_u32_e32 v61, vcc, 0, v121, vcc
	v_add_co_u32_e32 v68, vcc, 0x15000, v120
	v_readlane_b32 s46, v252, 6
	s_nop 0
	v_addc_co_u32_e32 v69, vcc, 0, v121, vcc
	v_add_co_u32_e32 v80, vcc, 0x1d000, v120
	global_load_dwordx4 v[60:63], v[60:61], off offset:2240 nt
	s_nop 0
	global_load_dwordx4 v[68:71], v[68:69], off offset:3360 nt
	v_addc_co_u32_e32 v81, vcc, 0, v121, vcc
	v_add_co_u32_e32 v84, vcc, 0x24000, v120
	v_readlane_b32 s47, v252, 7
	s_nop 0
	v_addc_co_u32_e32 v85, vcc, 0, v121, vcc
	v_add_co_u32_e32 v88, vcc, 0x2b000, v120
	global_load_dwordx4 v[80:83], v[80:81], off offset:384 nt
	s_nop 0
	global_load_dwordx4 v[84:87], v[84:85], off offset:1504 nt
	v_addc_co_u32_e32 v89, vcc, 0, v121, vcc
	v_add_co_u32_e32 v92, vcc, 0x32000, v120
	v_readlane_b32 s50, v252, 10
	s_nop 0
	v_addc_co_u32_e32 v93, vcc, 0, v121, vcc
	v_add_co_u32_e32 v96, vcc, 0x3a000, v120
	global_load_dwordx4 v[88:91], v[88:89], off offset:2624 nt
	s_nop 0
	global_load_dwordx4 v[92:95], v[92:93], off offset:3744 nt
	v_addc_co_u32_e32 v97, vcc, 0, v121, vcc
	v_add_co_u32_e32 v100, vcc, 0x41000, v120
	v_readlane_b32 s51, v252, 11
	s_nop 0
	v_addc_co_u32_e32 v101, vcc, 0, v121, vcc
	v_add_co_u32_e32 v104, vcc, 0x48000, v120
	global_load_dwordx4 v[96:99], v[96:97], off offset:768 nt
	s_nop 0
	global_load_dwordx4 v[100:103], v[100:101], off offset:1888 nt
	v_addc_co_u32_e32 v105, vcc, 0, v121, vcc
	v_add_co_u32_e32 v108, vcc, 0x50000, v120
	v_readlane_b32 s52, v252, 12
	s_nop 0
	v_addc_co_u32_e32 v109, vcc, 0, v121, vcc
	v_add_co_u32_e32 v112, vcc, 0x57000, v120
	global_load_dwordx4 v[104:107], v[104:105], off offset:3008 nt
	s_nop 0
	global_load_dwordx4 v[108:111], v[108:109], off offset:32 nt
	v_addc_co_u32_e32 v113, vcc, 0, v121, vcc
	v_add_co_u32_e32 v116, vcc, 0x5e000, v120
	v_readlane_b32 s53, v252, 13
	s_nop 0
	v_addc_co_u32_e32 v117, vcc, 0, v121, vcc
	v_add_co_u32_e32 v122, vcc, 0x65000, v120
	global_load_dwordx4 v[112:115], v[112:113], off offset:1152 nt
	s_nop 0
	global_load_dwordx4 v[116:119], v[116:117], off offset:2272 nt
	v_addc_co_u32_e32 v123, vcc, 0, v121, vcc
	v_add_co_u32_e32 v124, vcc, 0x6d000, v120
	v_readlane_b32 s54, v252, 14
	s_nop 0
	v_addc_co_u32_e32 v125, vcc, 0, v121, vcc
	global_load_dwordx4 v[120:123], v[122:123], off offset:3392 nt
	s_nop 0
	global_load_dwordx4 v[124:127], v[124:125], off offset:416 nt
	v_readlane_b32 s55, v252, 15
	v_readlane_b32 s56, v252, 16
	v_readlane_b32 s57, v252, 17
	v_readlane_b32 s58, v252, 18
	v_readlane_b32 s59, v252, 19

.LBB0_89:
	s_waitcnt vmcnt(14)
	v_cvt_pk_bf16_f32 v218, v132, v128
	s_waitcnt vmcnt(12)
	v_cvt_pk_bf16_f32 v219, v140, v136
	s_waitcnt vmcnt(10)
	v_cvt_pk_bf16_f32 v220, v148, v144
	s_waitcnt vmcnt(8)
	v_cvt_pk_bf16_f32 v221, v164, v156
	ds_write_b128 v202, v[218:221]
	s_waitcnt vmcnt(6)
	v_cvt_pk_bf16_f32 v218, v160, v152
	s_waitcnt vmcnt(4)
	v_cvt_pk_bf16_f32 v219, v172, v168
	s_waitcnt vmcnt(2)
	v_cvt_pk_bf16_f32 v220, v180, v176
	s_waitcnt vmcnt(0)
	v_cvt_pk_bf16_f32 v221, v188, v184
	ds_write_b128 v203, v[218:221]
	v_cvt_pk_bf16_f32 v218, v133, v129
	v_cvt_pk_bf16_f32 v219, v141, v137
	v_cvt_pk_bf16_f32 v220, v149, v145
	v_cvt_pk_bf16_f32 v221, v165, v157
	ds_write_b128 v202, v[218:221] offset:128
	v_cvt_pk_bf16_f32 v218, v161, v153
	v_cvt_pk_bf16_f32 v219, v173, v169
	v_cvt_pk_bf16_f32 v220, v181, v177
	v_cvt_pk_bf16_f32 v221, v189, v185
	ds_write_b128 v203, v[218:221] offset:128
	v_cvt_pk_bf16_f32 v218, v134, v130
	v_cvt_pk_bf16_f32 v219, v142, v138
	v_cvt_pk_bf16_f32 v220, v150, v146
	v_cvt_pk_bf16_f32 v221, v166, v158
	ds_write_b128 v202, v[218:221] offset:256
	v_cvt_pk_bf16_f32 v218, v162, v154
	v_cvt_pk_bf16_f32 v219, v174, v170
	v_cvt_pk_bf16_f32 v220, v182, v178
	v_cvt_pk_bf16_f32 v221, v190, v186
	ds_write_b128 v203, v[218:221] offset:256
	v_cvt_pk_bf16_f32 v128, v135, v131
	v_cvt_pk_bf16_f32 v129, v143, v139
	v_cvt_pk_bf16_f32 v130, v151, v147
	v_cvt_pk_bf16_f32 v131, v167, v159
	ds_write_b128 v202, v[128:131] offset:384
	v_cvt_pk_bf16_f32 v128, v163, v155
	v_cvt_pk_bf16_f32 v129, v175, v171
	v_cvt_pk_bf16_f32 v130, v183, v179
	v_cvt_pk_bf16_f32 v131, v191, v187
	ds_write_b128 v203, v[128:131] offset:384
	v_add_u32_e32 v128, s30, v201
	v_ashrrev_i32_e32 v129, 31, v128
	v_lshlrev_b64 v[128:129], 11, v[128:129]
	v_lshl_add_u64 v[134:135], s[12:13], 0, v[128:129]
	v_add_u32_e32 v128, v204, v205
	ds_read_b128 v[130:133], v128
	s_lshl_b32 s14, s31, 6
	s_ashr_i32 s15, s14, 31
	v_add_u32_e32 v129, v206, v207
	v_lshl_add_u64 v[134:135], s[14:15], 1, v[134:135]
	ds_read_b128 v[138:141], v129
	v_lshl_add_u64 v[146:147], v[134:135], 0, v[194:195]
	ds_read_b128 v[134:137], v128 offset:4096
	s_waitcnt lgkmcnt(2)
	global_store_dwordx4 v[146:147], v[130:133], off nt
	s_mov_b32 s14, 0x14000
	s_nop 0
	v_add_u32_e32 v130, v208, v209
	v_add_co_u32_e32 v132, vcc, s26, v146
	ds_read_b128 v[142:145], v130
	s_nop 0
	v_addc_co_u32_e32 v133, vcc, 0, v147, vcc
	v_add_u32_e32 v131, v210, v211
	s_waitcnt lgkmcnt(2)
	global_store_dwordx4 v[132:133], v[138:141], off nt
	ds_read_b128 v[138:141], v131
	v_add_co_u32_e32 v132, vcc, s27, v146
	s_nop 1
	v_addc_co_u32_e32 v133, vcc, 0, v147, vcc
	s_waitcnt lgkmcnt(1)
	global_store_dwordx4 v[132:133], v[142:145], off nt
	v_add_co_u32_e32 v148, vcc, s28, v146
	v_add_u32_e32 v132, v212, v213
	s_nop 0
	v_addc_co_u32_e32 v149, vcc, 0, v147, vcc
	ds_read_b128 v[142:145], v132
	s_waitcnt lgkmcnt(1)
	global_store_dwordx4 v[148:149], v[138:141], off nt
	v_add_u32_e32 v133, v214, v215
	s_nop 0
	v_add_co_u32_e32 v138, vcc, s29, v146
	s_nop 1
	v_addc_co_u32_e32 v139, vcc, 0, v147, vcc
	global_store_dwordx4 v[138:139], v[134:137], off nt
	ds_read_b128 v[136:139], v133
	s_nop 0
	v_add_co_u32_e32 v134, vcc, s14, v146
	s_nop 1
	v_addc_co_u32_e32 v135, vcc, 0, v147, vcc
	s_waitcnt lgkmcnt(1)
	global_store_dwordx4 v[134:135], v[142:145], off nt
	v_add_u32_e32 v134, v216, v217
	ds_read_b128 v[140:143], v134
	v_add_co_u32_e32 v144, vcc, 0x18000, v146
	s_nop 1
	v_addc_co_u32_e32 v145, vcc, 0, v147, vcc
	s_waitcnt lgkmcnt(1)
	global_store_dwordx4 v[144:145], v[136:139], off nt
	s_nop 1
	v_add_co_u32_e32 v136, vcc, 0x1c000, v146
	s_nop 1
	v_addc_co_u32_e32 v137, vcc, 0, v147, vcc
	s_andn2_b64 vcc, exec, s[4:5]
	s_waitcnt lgkmcnt(0)
	global_store_dwordx4 v[136:137], v[140:143], off nt
	s_cbranch_vccz .LBB0_91
	s_andn2_b64 vcc, exec, s[2:3]
	s_cbranch_vccnz .LBB0_13
	s_branch .LBB0_92
.LBB0_91:
	s_add_i32 s39, s39, s35
	s_lshr_b32 s4, s39, 31
	s_ashr_i32 s5, s39, 10
	s_add_i32 s4, s5, s4
	s_mulk_i32 s4, 0x780
	s_sub_i32 s4, s35, s4
	s_sext_i32_i16 s5, s4
	s_mulk_i32 s5, 0x8889
	s_lshr_b32 s5, s5, 16
	v_cvt_pk_bf16_f32 v136, v0, v4
	s_add_i32 s5, s5, s4
	v_cvt_pk_bf16_f32 v137, v8, v12
	v_cvt_pk_bf16_f32 v138, v16, v20
	v_cvt_pk_bf16_f32 v139, v24, v28
	ds_write_b128 v202, v[136:139]
	v_cvt_pk_bf16_f32 v136, v32, v36
	s_sext_i32_i16 s14, s5
	v_cvt_pk_bf16_f32 v137, v44, v48
	v_cvt_pk_bf16_f32 v138, v56, v64
	v_cvt_pk_bf16_f32 v139, v72, v76
	ds_write_b128 v203, v[136:139]
	v_cvt_pk_bf16_f32 v136, v1, v5
	s_ashr_i32 s14, s14, 6
	s_bfe_u32 s5, s5, 0x1000f
	v_cvt_pk_bf16_f32 v137, v9, v13
	v_cvt_pk_bf16_f32 v138, v17, v21
	v_cvt_pk_bf16_f32 v139, v25, v29
	ds_write_b128 v202, v[136:139] offset:128
	v_cvt_pk_bf16_f32 v136, v33, v37
	s_add_i32 s5, s14, s5
	v_cvt_pk_bf16_f32 v137, v45, v49
	v_cvt_pk_bf16_f32 v138, v57, v65
	v_cvt_pk_bf16_f32 v139, v73, v77
	ds_write_b128 v203, v[136:139] offset:128
	v_cvt_pk_bf16_f32 v136, v2, v6
	s_mul_i32 s14, s5, 0x78
	v_cvt_pk_bf16_f32 v137, v10, v14
	v_cvt_pk_bf16_f32 v138, v18, v22
	v_cvt_pk_bf16_f32 v139, v26, v30
	ds_write_b128 v202, v[136:139] offset:256
	v_cvt_pk_bf16_f32 v136, v34, v38
	s_sub_i32 s4, s4, s14
	v_cvt_pk_bf16_f32 v137, v46, v50
	v_cvt_pk_bf16_f32 v138, v58, v66
	v_cvt_pk_bf16_f32 v139, v74, v78
	ds_write_b128 v203, v[136:139] offset:256
	v_cvt_pk_bf16_f32 v136, v3, v7
	v_cvt_pk_bf16_f32 v137, v11, v15
	v_cvt_pk_bf16_f32 v138, v19, v23
	v_cvt_pk_bf16_f32 v139, v27, v31
	ds_write_b128 v202, v[136:139] offset:384
	v_cvt_pk_bf16_f32 v136, v35, v39
	s_sext_i32_i16 s4, s4
	v_cvt_pk_bf16_f32 v137, v47, v51
	v_cvt_pk_bf16_f32 v138, v59, v67
	v_cvt_pk_bf16_f32 v139, v75, v79
	ds_write_b128 v203, v[136:139] offset:384
	v_lshl_add_u32 v136, s4, 6, v201
	v_ashrrev_i32_e32 v137, 31, v136
	v_lshlrev_b64 v[136:137], 11, v[136:137]
	s_sext_i32_i16 s5, s5
	v_lshl_add_u64 v[140:141], s[12:13], 0, v[136:137]
	ds_read_b128 v[136:139], v128
	s_lshl_b32 s4, s5, 6
	s_ashr_i32 s5, s4, 31
	v_lshl_add_u64 v[140:141], s[4:5], 1, v[140:141]
	v_lshl_add_u64 v[148:149], v[140:141], 0, v[194:195]
	ds_read_b128 v[140:143], v128 offset:4096
	s_waitcnt lgkmcnt(1)
	global_store_dwordx4 v[148:149], v[136:139], off nt
	ds_read_b128 v[136:139], v129
	ds_read_b128 v[144:147], v130
	v_add_co_u32_e32 v150, vcc, s26, v148
	s_nop 1
	v_addc_co_u32_e32 v151, vcc, 0, v149, vcc
	s_waitcnt lgkmcnt(1)
	global_store_dwordx4 v[150:151], v[136:139], off nt
	s_nop 1
	v_add_co_u32_e32 v136, vcc, s27, v148
	s_nop 1
	v_addc_co_u32_e32 v137, vcc, 0, v149, vcc
	s_waitcnt lgkmcnt(0)
	global_store_dwordx4 v[136:137], v[144:147], off nt
	ds_read_b128 v[136:139], v131
	ds_read_b128 v[144:147], v132
	v_add_co_u32_e32 v150, vcc, s28, v148
	s_nop 1
	v_addc_co_u32_e32 v151, vcc, 0, v149, vcc
	s_waitcnt lgkmcnt(1)
	global_store_dwordx4 v[150:151], v[136:139], off nt
	s_nop 1
	v_add_co_u32_e32 v136, vcc, s29, v148
	s_nop 1
	v_addc_co_u32_e32 v137, vcc, 0, v149, vcc
	global_store_dwordx4 v[136:137], v[140:143], off nt
	v_add_co_u32_e32 v136, vcc, 0x14000, v148
	ds_read_b128 v[140:143], v134
	s_nop 0
	v_addc_co_u32_e32 v137, vcc, 0, v149, vcc
	s_waitcnt lgkmcnt(1)
	global_store_dwordx4 v[136:137], v[144:147], off nt
	ds_read_b128 v[136:139], v133
	s_nop 0
	v_add_co_u32_e32 v144, vcc, 0x18000, v148
	s_nop 1
	v_addc_co_u32_e32 v145, vcc, 0, v149, vcc
	s_waitcnt lgkmcnt(0)
	global_store_dwordx4 v[144:145], v[136:139], off nt
	s_nop 1
	v_add_co_u32_e32 v136, vcc, 0x1c000, v148
	s_nop 1
	v_addc_co_u32_e32 v137, vcc, 0, v149, vcc
	global_store_dwordx4 v[136:137], v[140:143], off nt
	s_andn2_b64 vcc, exec, s[2:3]
	s_cbranch_vccnz .LBB0_13
.LBB0_92:
	s_add_i32 s41, s41, s40
	s_lshr_b32 s2, s41, 31
	s_ashr_i32 s3, s41, 10
	s_add_i32 s2, s3, s2
	s_mulk_i32 s2, 0x780
	s_sub_i32 s2, s40, s2
	s_sext_i32_i16 s3, s2
	s_mulk_i32 s3, 0x8889
	s_lshr_b32 s3, s3, 16
	v_cvt_pk_bf16_f32 v136, v40, v52
	s_add_i32 s3, s3, s2
	v_cvt_pk_bf16_f32 v137, v60, v68
	v_cvt_pk_bf16_f32 v138, v80, v84
	v_cvt_pk_bf16_f32 v139, v88, v92
	ds_write_b128 v202, v[136:139]
	v_cvt_pk_bf16_f32 v136, v96, v100
	s_sext_i32_i16 s4, s3
	v_cvt_pk_bf16_f32 v137, v104, v108
	v_cvt_pk_bf16_f32 v138, v112, v116
	v_cvt_pk_bf16_f32 v139, v120, v124
	ds_write_b128 v203, v[136:139]
	v_cvt_pk_bf16_f32 v136, v41, v53
	s_ashr_i32 s4, s4, 6
	s_bfe_u32 s3, s3, 0x1000f
	v_cvt_pk_bf16_f32 v137, v61, v69
	v_cvt_pk_bf16_f32 v138, v81, v85
	v_cvt_pk_bf16_f32 v139, v89, v93
	ds_write_b128 v202, v[136:139] offset:128
	v_cvt_pk_bf16_f32 v136, v97, v101
	s_add_i32 s3, s4, s3
	v_cvt_pk_bf16_f32 v137, v105, v109
	v_cvt_pk_bf16_f32 v138, v113, v117
	v_cvt_pk_bf16_f32 v139, v121, v125
	ds_write_b128 v203, v[136:139] offset:128
	v_cvt_pk_bf16_f32 v136, v42, v54
	s_mul_i32 s4, s3, 0x78
	v_cvt_pk_bf16_f32 v137, v62, v70
	v_cvt_pk_bf16_f32 v138, v82, v86
	v_cvt_pk_bf16_f32 v139, v90, v94
	ds_write_b128 v202, v[136:139] offset:256
	v_cvt_pk_bf16_f32 v136, v98, v102
	s_sub_i32 s2, s2, s4
	v_cvt_pk_bf16_f32 v137, v106, v110
	v_cvt_pk_bf16_f32 v138, v114, v118
	v_cvt_pk_bf16_f32 v139, v122, v126
	ds_write_b128 v203, v[136:139] offset:256
	v_cvt_pk_bf16_f32 v136, v43, v55
	v_cvt_pk_bf16_f32 v137, v63, v71
	v_cvt_pk_bf16_f32 v138, v83, v87
	v_cvt_pk_bf16_f32 v139, v91, v95
	ds_write_b128 v202, v[136:139] offset:384
	v_cvt_pk_bf16_f32 v136, v99, v103
	s_sext_i32_i16 s2, s2
	v_cvt_pk_bf16_f32 v137, v107, v111
	v_cvt_pk_bf16_f32 v138, v115, v119
	v_cvt_pk_bf16_f32 v139, v123, v127
	ds_write_b128 v203, v[136:139] offset:384
	v_lshl_add_u32 v136, s2, 6, v201
	v_ashrrev_i32_e32 v137, 31, v136
	v_lshlrev_b64 v[136:137], 11, v[136:137]
	s_sext_i32_i16 s3, s3
	v_lshl_add_u64 v[140:141], s[12:13], 0, v[136:137]
	ds_read_b128 v[136:139], v128
	s_lshl_b32 s2, s3, 6
	s_ashr_i32 s3, s2, 31
	v_lshl_add_u64 v[140:141], s[2:3], 1, v[140:141]
	v_lshl_add_u64 v[148:149], v[140:141], 0, v[194:195]
	ds_read_b128 v[140:143], v128 offset:4096
	s_waitcnt lgkmcnt(1)
	global_store_dwordx4 v[148:149], v[136:139], off nt
	ds_read_b128 v[136:139], v129
	ds_read_b128 v[144:147], v130
	v_add_co_u32_e32 v128, vcc, s26, v148
	s_nop 1
	v_addc_co_u32_e32 v129, vcc, 0, v149, vcc
	s_waitcnt lgkmcnt(1)
	global_store_dwordx4 v[128:129], v[136:139], off nt
	v_add_co_u32_e32 v128, vcc, s27, v148
	ds_read_b128 v[136:139], v132
	s_nop 0
	v_addc_co_u32_e32 v129, vcc, 0, v149, vcc
	s_waitcnt lgkmcnt(1)
	global_store_dwordx4 v[128:129], v[144:147], off nt
	ds_read_b128 v[128:131], v131
	s_nop 0
	v_add_co_u32_e32 v144, vcc, s28, v148
	s_nop 1
	v_addc_co_u32_e32 v145, vcc, 0, v149, vcc
	s_waitcnt lgkmcnt(0)
	global_store_dwordx4 v[144:145], v[128:131], off nt
	s_nop 1
	v_add_co_u32_e32 v128, vcc, s29, v148
	s_nop 1
	v_addc_co_u32_e32 v129, vcc, 0, v149, vcc
	global_store_dwordx4 v[128:129], v[140:143], off nt
	v_add_co_u32_e32 v128, vcc, 0x14000, v148
	s_nop 1
	v_addc_co_u32_e32 v129, vcc, 0, v149, vcc
	global_store_dwordx4 v[128:129], v[136:139], off nt
	ds_read_b128 v[128:131], v133
	ds_read_b128 v[132:135], v134
	v_add_co_u32_e32 v136, vcc, 0x18000, v148
	s_nop 1
	v_addc_co_u32_e32 v137, vcc, 0, v149, vcc
	s_waitcnt lgkmcnt(1)
	global_store_dwordx4 v[136:137], v[128:131], off nt
	s_nop 1
	v_add_co_u32_e32 v128, vcc, 0x1c000, v148
	s_nop 1
	v_addc_co_u32_e32 v129, vcc, 0, v149, vcc
	s_waitcnt lgkmcnt(0)
	global_store_dwordx4 v[128:129], v[132:135], off nt
	s_branch .LBB0_13

.LBB0_96:
	s_add_i32 s35, s8, s23
	s_cmpk_lt_i32 s35, 0x100
	s_cselect_b64 s[2:3], -1, 0
	s_ashr_i32 s0, s23, 31
	s_lshr_b32 s0, s0, 25
	s_add_i32 s0, s23, s0
	s_ashr_i32 s16, s0, 7
	s_and_b32 s0, s0, 0xff80
	s_sub_i32 s0, s23, s0
	s_bfe_i32 s1, s0, 0x80000
	s_bfe_u32 s1, s1, 0x2000d
	s_add_i32 s1, s0, s1
	s_bfe_i32 s4, s1, 0x80000
	s_and_b32 s1, s1, 0xfc
	s_sub_i32 s0, s0, s1
	s_sext_i32_i8 s0, s0
	s_ashr_i32 s17, s16, 31
	v_readlane_b32 s40, v252, 4
	s_lshl_b32 s14, s0, 6
	s_lshl_b64 s[0:1], s[16:17], 21
	v_readlane_b32 s48, v252, 12
	s_sext_i32_i16 s4, s4
	v_readlane_b32 s49, v252, 13
	s_add_u32 s0, s48, s0
	s_addc_u32 s1, s49, s1
	s_lshl_b32 s4, s4, 4
	s_andn2_b32 s4, s4, 63
	v_add_u32_e32 v128, s4, v193
	v_ashrrev_i32_e32 v129, 31, v128
	v_lshlrev_b64 v[128:129], 10, v[128:129]
	s_ashr_i32 s15, s14, 31
	v_lshl_add_u64 v[128:129], s[0:1], 0, v[128:129]
	v_lshl_add_u64 v[128:129], s[14:15], 2, v[128:129]
	v_lshl_add_u64 v[172:173], v[128:129], 0, v[198:199]
	v_add_co_u32_e32 v140, vcc, s27, v172
	global_load_dwordx4 v[132:135], v[172:173], off nt
	global_load_dwordx4 v[144:147], v[172:173], off offset:1024 nt
	global_load_dwordx4 v[128:131], v[172:173], off offset:2048 nt
	global_load_dwordx4 v[136:139], v[172:173], off offset:3072 nt
	v_addc_co_u32_e32 v141, vcc, 0, v173, vcc
	v_add_co_u32_e32 v152, vcc, 0x2000, v172
	global_load_dwordx4 v[164:167], v[140:141], off nt
	global_load_dwordx4 v[176:179], v[140:141], off offset:1024 nt
	global_load_dwordx4 v[156:159], v[140:141], off offset:2048 nt
	global_load_dwordx4 v[168:171], v[140:141], off offset:3072 nt
	v_addc_co_u32_e32 v153, vcc, 0, v173, vcc
	v_add_co_u32_e32 v184, vcc, 0x3000, v172
	global_load_dwordx4 v[148:151], v[152:153], off nt
	global_load_dwordx4 v[160:163], v[152:153], off offset:1024 nt
	global_load_dwordx4 v[140:143], v[152:153], off offset:2048 nt
	s_nop 0
	global_load_dwordx4 v[152:155], v[152:153], off offset:3072 nt
	v_addc_co_u32_e32 v185, vcc, 0, v173, vcc
	global_load_dwordx4 v[180:183], v[184:185], off nt
	global_load_dwordx4 v[188:191], v[184:185], off offset:1024 nt
	global_load_dwordx4 v[172:175], v[184:185], off offset:2048 nt
	s_nop 0
	global_load_dwordx4 v[184:187], v[184:185], off offset:3072 nt
	s_cmpk_gt_i32 s35, 0xff
	v_readlane_b32 s41, v252, 5
	v_readlane_b32 s42, v252, 6
	v_readlane_b32 s43, v252, 7
	v_readlane_b32 s44, v252, 8
	v_readlane_b32 s45, v252, 9
	v_readlane_b32 s46, v252, 10
	v_readlane_b32 s47, v252, 11
	v_readlane_b32 s50, v252, 14
	v_readlane_b32 s51, v252, 15
	v_readlane_b32 s52, v252, 16
	v_readlane_b32 s53, v252, 17
	v_readlane_b32 s54, v252, 18
	v_readlane_b32 s55, v252, 19
	s_cbranch_scc1 .LBB0_98
	s_ashr_i32 s0, s35, 31
	s_lshr_b32 s0, s0, 25
	s_add_i32 s1, s35, s0
	s_and_b32 s0, s1, 0x80
	s_sub_i32 s0, s35, s0
	s_bfe_i32 s5, s0, 0x80000
	s_bfe_u32 s5, s5, 0x2000d
	s_add_i32 s5, s0, s5
	s_bfe_i32 s15, s5, 0x80000
	s_and_b32 s5, s5, 0xfc
	s_sub_i32 s0, s0, s5
	s_ashr_i32 s40, s1, 7
	s_sext_i32_i8 s0, s0
	s_ashr_i32 s41, s40, 31
	v_readlane_b32 s44, v252, 4
	s_lshl_b32 s0, s0, 6
	s_lshl_b64 s[40:41], s[40:41], 21
	v_readlane_b32 s52, v252, 12
	s_sext_i32_i16 s15, s15
	v_readlane_b32 s53, v252, 13
	s_add_u32 s40, s52, s40
	s_addc_u32 s41, s53, s41
	s_lshl_b32 s1, s15, 4
	s_andn2_b32 s1, s1, 63
	v_add_u32_e32 v0, s1, v193
	v_ashrrev_i32_e32 v1, 31, v0
	v_lshlrev_b64 v[0:1], 10, v[0:1]
	v_lshl_add_u64 v[0:1], s[40:41], 0, v[0:1]
	s_ashr_i32 s1, s0, 31
	v_lshl_add_u64 v[0:1], s[0:1], 2, v[0:1]
	v_mov_b32_e32 v197, v195
	v_lshl_add_u64 v[48:49], v[0:1], 0, v[196:197]
	v_add_co_u32_e32 v16, vcc, s27, v48
	global_load_dwordx4 v[12:15], v[48:49], off nt
	global_load_dwordx4 v[8:11], v[48:49], off offset:1024 nt
	global_load_dwordx4 v[4:7], v[48:49], off offset:2048 nt
	global_load_dwordx4 v[0:3], v[48:49], off offset:3072 nt
	v_addc_co_u32_e32 v17, vcc, 0, v49, vcc
	v_add_co_u32_e32 v32, vcc, 0x2000, v48
	global_load_dwordx4 v[28:31], v[16:17], off nt
	global_load_dwordx4 v[24:27], v[16:17], off offset:1024 nt
	global_load_dwordx4 v[20:23], v[16:17], off offset:2048 nt
	s_nop 0
	global_load_dwordx4 v[16:19], v[16:17], off offset:3072 nt
	v_addc_co_u32_e32 v33, vcc, 0, v49, vcc
	v_add_co_u32_e32 v48, vcc, 0x3000, v48
	global_load_dwordx4 v[44:47], v[32:33], off nt
	global_load_dwordx4 v[40:43], v[32:33], off offset:1024 nt
	global_load_dwordx4 v[36:39], v[32:33], off offset:2048 nt
	s_nop 0
	global_load_dwordx4 v[32:35], v[32:33], off offset:3072 nt
	v_addc_co_u32_e32 v49, vcc, 0, v49, vcc
	global_load_dwordx4 v[60:63], v[48:49], off nt
	global_load_dwordx4 v[56:59], v[48:49], off offset:1024 nt
	global_load_dwordx4 v[52:55], v[48:49], off offset:2048 nt
	s_nop 0
	global_load_dwordx4 v[48:51], v[48:49], off offset:3072 nt
	v_readlane_b32 s45, v252, 5
	v_readlane_b32 s46, v252, 6
	v_readlane_b32 s47, v252, 7
	v_readlane_b32 s48, v252, 8
	v_readlane_b32 s49, v252, 9
	v_readlane_b32 s50, v252, 10
	v_readlane_b32 s51, v252, 11
	v_readlane_b32 s54, v252, 14
	v_readlane_b32 s55, v252, 15
	v_readlane_b32 s56, v252, 16
	v_readlane_b32 s57, v252, 17
	v_readlane_b32 s58, v252, 18
	v_readlane_b32 s59, v252, 19
.LBB0_98:
	s_add_i32 s15, s26, s23
	s_cmpk_lt_i32 s15, 0x100
	s_cselect_b64 s[0:1], -1, 0
	s_cmpk_gt_i32 s15, 0xff
	s_cbranch_scc1 .LBB0_100
	s_ashr_i32 s5, s15, 31
	s_lshr_b32 s5, s5, 25
	s_add_i32 s5, s15, s5
	s_and_b32 s39, s5, 0x80
	s_sub_i32 s39, s15, s39
	s_bfe_i32 s40, s39, 0x80000
	s_bfe_u32 s40, s40, 0x2000d
	s_add_i32 s40, s39, s40
	s_bfe_i32 s41, s40, 0x80000
	s_and_b32 s40, s40, 0xfc
	s_sub_i32 s39, s39, s40
	s_ashr_i32 s42, s5, 7
	s_sext_i32_i8 s39, s39
	s_ashr_i32 s43, s42, 31
	v_readlane_b32 s44, v252, 4
	s_lshl_b32 s40, s39, 6
	s_lshl_b64 s[42:43], s[42:43], 21
	v_readlane_b32 s52, v252, 12
	s_sext_i32_i16 s41, s41
	v_readlane_b32 s53, v252, 13
	s_add_u32 s42, s52, s42
	s_addc_u32 s43, s53, s43
	s_lshl_b32 s5, s41, 4
	s_andn2_b32 s5, s5, 63
	v_add_u32_e32 v64, s5, v193
	v_ashrrev_i32_e32 v65, 31, v64
	v_lshlrev_b64 v[64:65], 10, v[64:65]
	v_lshl_add_u64 v[64:65], s[42:43], 0, v[64:65]
	s_ashr_i32 s41, s40, 31
	v_lshl_add_u64 v[64:65], s[40:41], 2, v[64:65]
	v_mov_b32_e32 v197, v195
	v_lshl_add_u64 v[112:113], v[64:65], 0, v[196:197]
	v_add_co_u32_e32 v80, vcc, s27, v112
	global_load_dwordx4 v[76:79], v[112:113], off nt
	global_load_dwordx4 v[72:75], v[112:113], off offset:1024 nt
	global_load_dwordx4 v[68:71], v[112:113], off offset:2048 nt
	global_load_dwordx4 v[64:67], v[112:113], off offset:3072 nt
	v_addc_co_u32_e32 v81, vcc, 0, v113, vcc
	v_add_co_u32_e32 v96, vcc, 0x2000, v112
	global_load_dwordx4 v[92:95], v[80:81], off nt
	global_load_dwordx4 v[88:91], v[80:81], off offset:1024 nt
	global_load_dwordx4 v[84:87], v[80:81], off offset:2048 nt
	s_nop 0
	global_load_dwordx4 v[80:83], v[80:81], off offset:3072 nt
	v_addc_co_u32_e32 v97, vcc, 0, v113, vcc
	v_add_co_u32_e32 v112, vcc, 0x3000, v112
	global_load_dwordx4 v[108:111], v[96:97], off nt
	global_load_dwordx4 v[104:107], v[96:97], off offset:1024 nt
	global_load_dwordx4 v[100:103], v[96:97], off offset:2048 nt
	s_nop 0
	global_load_dwordx4 v[96:99], v[96:97], off offset:3072 nt
	v_addc_co_u32_e32 v113, vcc, 0, v113, vcc
	global_load_dwordx4 v[124:127], v[112:113], off nt
	global_load_dwordx4 v[120:123], v[112:113], off offset:1024 nt
	global_load_dwordx4 v[116:119], v[112:113], off offset:2048 nt
	s_nop 0
	global_load_dwordx4 v[112:115], v[112:113], off offset:3072 nt
	v_readlane_b32 s45, v252, 5
	v_readlane_b32 s46, v252, 6
	v_readlane_b32 s47, v252, 7
	v_readlane_b32 s48, v252, 8
	v_readlane_b32 s49, v252, 9
	v_readlane_b32 s50, v252, 10
	v_readlane_b32 s51, v252, 11
	v_readlane_b32 s54, v252, 14
	v_readlane_b32 s55, v252, 15
	v_readlane_b32 s56, v252, 16
	v_readlane_b32 s57, v252, 17
	v_readlane_b32 s58, v252, 18
	v_readlane_b32 s59, v252, 19
.LBB0_100:
	s_waitcnt vmcnt(14)
	v_cvt_pk_bf16_f32 v218, v132, v144
	s_waitcnt vmcnt(12)
	v_cvt_pk_bf16_f32 v219, v128, v136
	s_waitcnt vmcnt(10)
	v_cvt_pk_bf16_f32 v220, v164, v176
	s_waitcnt vmcnt(8)
	v_cvt_pk_bf16_f32 v221, v156, v168
	ds_write_b128 v202, v[218:221]
	s_waitcnt vmcnt(6)
	v_cvt_pk_bf16_f32 v218, v148, v160
	s_waitcnt vmcnt(4)
	v_cvt_pk_bf16_f32 v219, v140, v152
	s_waitcnt vmcnt(2)
	v_cvt_pk_bf16_f32 v220, v180, v188
	s_waitcnt vmcnt(0)
	v_cvt_pk_bf16_f32 v221, v172, v184
	ds_write_b128 v203, v[218:221]
	v_cvt_pk_bf16_f32 v218, v133, v145
	v_cvt_pk_bf16_f32 v219, v129, v137
	v_cvt_pk_bf16_f32 v220, v165, v177
	v_cvt_pk_bf16_f32 v221, v157, v169
	ds_write_b128 v202, v[218:221] offset:128
	v_cvt_pk_bf16_f32 v218, v149, v161
	v_cvt_pk_bf16_f32 v219, v141, v153
	v_cvt_pk_bf16_f32 v220, v181, v189
	v_cvt_pk_bf16_f32 v221, v173, v185
	ds_write_b128 v203, v[218:221] offset:128
	v_cvt_pk_bf16_f32 v218, v134, v146
	v_cvt_pk_bf16_f32 v219, v130, v138
	v_cvt_pk_bf16_f32 v220, v166, v178
	v_cvt_pk_bf16_f32 v221, v158, v170
	ds_write_b128 v202, v[218:221] offset:256
	v_cvt_pk_bf16_f32 v218, v150, v162
	v_cvt_pk_bf16_f32 v219, v142, v154
	v_cvt_pk_bf16_f32 v220, v182, v190
	v_cvt_pk_bf16_f32 v221, v174, v186
	ds_write_b128 v203, v[218:221] offset:256
	v_cvt_pk_bf16_f32 v128, v135, v147
	s_lshl_b64 s[16:17], s[16:17], 19
	v_cvt_pk_bf16_f32 v129, v131, v139
	v_cvt_pk_bf16_f32 v130, v167, v179
	v_cvt_pk_bf16_f32 v131, v159, v171
	ds_write_b128 v202, v[128:131] offset:384
	v_cvt_pk_bf16_f32 v128, v151, v163
	v_cvt_pk_bf16_f32 v129, v143, v155
	v_cvt_pk_bf16_f32 v130, v183, v191
	v_cvt_pk_bf16_f32 v131, v175, v187
	ds_write_b128 v203, v[128:131] offset:384
	s_lshl_b64 s[16:17], s[16:17], 1
	v_add_u32_e32 v128, s14, v201
	s_add_u32 s16, s24, s16
	v_ashrrev_i32_e32 v129, 31, v128
	s_addc_u32 s17, s25, s17
	v_lshlrev_b64 v[128:129], 12, v[128:129]
	v_lshl_add_u64 v[134:135], s[16:17], 0, v[128:129]
	v_add_u32_e32 v128, v204, v205
	ds_read_b128 v[130:133], v128
	s_ashr_i32 s5, s4, 31
	v_add_u32_e32 v129, v206, v207
	v_lshl_add_u64 v[134:135], s[4:5], 1, v[134:135]
	ds_read_b128 v[138:141], v129
	v_lshl_add_u64 v[146:147], v[134:135], 0, v[194:195]
	ds_read_b128 v[134:137], v128 offset:4096
	s_waitcnt lgkmcnt(2)
	global_store_dwordx4 v[146:147], v[130:133], off nt
	s_mov_b32 s4, 0x28000
	s_nop 0
	v_add_u32_e32 v130, v208, v209
	v_add_co_u32_e32 v132, vcc, s28, v146
	ds_read_b128 v[142:145], v130
	s_nop 0
	v_addc_co_u32_e32 v133, vcc, 0, v147, vcc
	v_add_u32_e32 v131, v210, v211
	s_waitcnt lgkmcnt(2)
	global_store_dwordx4 v[132:133], v[138:141], off nt
	ds_read_b128 v[138:141], v131
	v_add_co_u32_e32 v132, vcc, s29, v146
	s_nop 1
	v_addc_co_u32_e32 v133, vcc, 0, v147, vcc
	s_waitcnt lgkmcnt(1)
	global_store_dwordx4 v[132:133], v[142:145], off nt
	v_add_co_u32_e32 v148, vcc, s30, v146
	v_add_u32_e32 v132, v212, v213
	s_nop 0
	v_addc_co_u32_e32 v149, vcc, 0, v147, vcc
	ds_read_b128 v[142:145], v132
	s_waitcnt lgkmcnt(1)
	global_store_dwordx4 v[148:149], v[138:141], off nt
	v_add_u32_e32 v133, v214, v215
	s_nop 0
	v_add_co_u32_e32 v138, vcc, s31, v146
	s_nop 1
	v_addc_co_u32_e32 v139, vcc, 0, v147, vcc
	global_store_dwordx4 v[138:139], v[134:137], off nt
	ds_read_b128 v[136:139], v133
	s_nop 0
	v_add_co_u32_e32 v134, vcc, s4, v146
	s_nop 1
	v_addc_co_u32_e32 v135, vcc, 0, v147, vcc
	s_waitcnt lgkmcnt(1)
	global_store_dwordx4 v[134:135], v[142:145], off nt
	v_add_u32_e32 v134, v216, v217
	ds_read_b128 v[140:143], v134
	v_add_co_u32_e32 v144, vcc, 0x30000, v146
	s_nop 1
	v_addc_co_u32_e32 v145, vcc, 0, v147, vcc
	s_waitcnt lgkmcnt(1)
	global_store_dwordx4 v[144:145], v[136:139], off nt
	s_nop 1
	v_add_co_u32_e32 v136, vcc, 0x38000, v146
	s_nop 1
	v_addc_co_u32_e32 v137, vcc, 0, v147, vcc
	s_andn2_b64 vcc, exec, s[2:3]
	s_waitcnt lgkmcnt(0)
	global_store_dwordx4 v[136:137], v[140:143], off nt
	s_cbranch_vccz .LBB0_102
	s_andn2_b64 vcc, exec, s[0:1]
	s_cbranch_vccnz .LBB0_95
	s_branch .LBB0_103
.LBB0_102:
	s_ashr_i32 s2, s35, 31
	s_lshr_b32 s2, s2, 25
	s_add_i32 s3, s35, s2
	s_ashr_i32 s2, s3, 7
	s_and_b32 s3, s3, 0xff80
	v_cvt_pk_bf16_f32 v136, v12, v8
	s_sub_i32 s3, s35, s3
	v_cvt_pk_bf16_f32 v137, v4, v0
	v_cvt_pk_bf16_f32 v138, v28, v24
	v_cvt_pk_bf16_f32 v139, v20, v16
	ds_write_b128 v202, v[136:139]
	v_cvt_pk_bf16_f32 v136, v44, v40
	s_bfe_i32 s4, s3, 0x80000
	v_cvt_pk_bf16_f32 v137, v36, v32
	v_cvt_pk_bf16_f32 v138, v60, v56
	v_cvt_pk_bf16_f32 v139, v52, v48
	ds_write_b128 v203, v[136:139]
	v_cvt_pk_bf16_f32 v136, v13, v9
	s_bfe_u32 s4, s4, 0x2000d
	v_cvt_pk_bf16_f32 v137, v5, v1
	v_cvt_pk_bf16_f32 v138, v29, v25
	v_cvt_pk_bf16_f32 v139, v21, v17
	ds_write_b128 v202, v[136:139] offset:128
	v_cvt_pk_bf16_f32 v136, v45, v41
	s_add_i32 s4, s3, s4
	v_cvt_pk_bf16_f32 v137, v37, v33
	v_cvt_pk_bf16_f32 v138, v61, v57
	v_cvt_pk_bf16_f32 v139, v53, v49
	ds_write_b128 v203, v[136:139] offset:128
	v_cvt_pk_bf16_f32 v136, v14, v10
	s_bfe_i32 s5, s4, 0x80000
	v_cvt_pk_bf16_f32 v137, v6, v2
	v_cvt_pk_bf16_f32 v138, v30, v26
	v_cvt_pk_bf16_f32 v139, v22, v18
	ds_write_b128 v202, v[136:139] offset:256
	v_cvt_pk_bf16_f32 v136, v46, v42
	s_and_b32 s4, s4, 0xfc
	v_cvt_pk_bf16_f32 v137, v38, v34
	v_cvt_pk_bf16_f32 v138, v62, v58
	v_cvt_pk_bf16_f32 v139, v54, v50
	ds_write_b128 v203, v[136:139] offset:256
	v_cvt_pk_bf16_f32 v136, v15, v11
	s_sub_i32 s3, s3, s4
	v_cvt_pk_bf16_f32 v137, v7, v3
	v_cvt_pk_bf16_f32 v138, v31, v27
	v_cvt_pk_bf16_f32 v139, v23, v19
	ds_write_b128 v202, v[136:139] offset:384
	v_cvt_pk_bf16_f32 v136, v47, v43
	s_sext_i32_i8 s4, s3
	s_ashr_i32 s3, s2, 31
	v_cvt_pk_bf16_f32 v137, v39, v35
	v_cvt_pk_bf16_f32 v138, v63, v59
	v_cvt_pk_bf16_f32 v139, v55, v51
	ds_write_b128 v203, v[136:139] offset:384
	s_lshl_b64 s[2:3], s[2:3], 20
	v_lshl_add_u32 v136, s4, 6, v201
	s_add_u32 s2, s24, s2
	v_ashrrev_i32_e32 v137, 31, v136
	s_sext_i32_i16 s5, s5
	s_addc_u32 s3, s25, s3
	v_lshlrev_b64 v[136:137], 12, v[136:137]
	v_lshl_add_u64 v[140:141], s[2:3], 0, v[136:137]
	s_lshl_b32 s2, s5, 4
	ds_read_b128 v[136:139], v128
	s_andn2_b32 s2, s2, 63
	s_ashr_i32 s3, s2, 31
	v_lshl_add_u64 v[140:141], s[2:3], 1, v[140:141]
	v_lshl_add_u64 v[148:149], v[140:141], 0, v[194:195]
	ds_read_b128 v[140:143], v128 offset:4096
	s_waitcnt lgkmcnt(1)
	global_store_dwordx4 v[148:149], v[136:139], off nt
	ds_read_b128 v[136:139], v129
	ds_read_b128 v[144:147], v130
	v_add_co_u32_e32 v150, vcc, s28, v148
	s_nop 1
	v_addc_co_u32_e32 v151, vcc, 0, v149, vcc
	s_waitcnt lgkmcnt(1)
	global_store_dwordx4 v[150:151], v[136:139], off nt
	s_nop 1
	v_add_co_u32_e32 v136, vcc, s29, v148
	s_nop 1
	v_addc_co_u32_e32 v137, vcc, 0, v149, vcc
	s_waitcnt lgkmcnt(0)
	global_store_dwordx4 v[136:137], v[144:147], off nt
	ds_read_b128 v[136:139], v131
	ds_read_b128 v[144:147], v132
	v_add_co_u32_e32 v150, vcc, s30, v148
	s_nop 1
	v_addc_co_u32_e32 v151, vcc, 0, v149, vcc
	s_waitcnt lgkmcnt(1)
	global_store_dwordx4 v[150:151], v[136:139], off nt
	s_nop 1
	v_add_co_u32_e32 v136, vcc, s31, v148
	s_nop 1
	v_addc_co_u32_e32 v137, vcc, 0, v149, vcc
	global_store_dwordx4 v[136:137], v[140:143], off nt
	v_add_co_u32_e32 v136, vcc, 0x28000, v148
	ds_read_b128 v[140:143], v134
	s_nop 0
	v_addc_co_u32_e32 v137, vcc, 0, v149, vcc
	s_waitcnt lgkmcnt(1)
	global_store_dwordx4 v[136:137], v[144:147], off nt
	ds_read_b128 v[136:139], v133
	s_nop 0
	v_add_co_u32_e32 v144, vcc, 0x30000, v148
	s_nop 1
	v_addc_co_u32_e32 v145, vcc, 0, v149, vcc
	s_waitcnt lgkmcnt(0)
	global_store_dwordx4 v[144:145], v[136:139], off nt
	s_nop 1
	v_add_co_u32_e32 v136, vcc, 0x38000, v148
	s_nop 1
	v_addc_co_u32_e32 v137, vcc, 0, v149, vcc
	global_store_dwordx4 v[136:137], v[140:143], off nt
	s_andn2_b64 vcc, exec, s[0:1]
	s_cbranch_vccnz .LBB0_95
.LBB0_103:
	s_ashr_i32 s0, s15, 31
	s_lshr_b32 s0, s0, 25
	s_add_i32 s1, s15, s0
	s_ashr_i32 s0, s1, 7
	s_and_b32 s1, s1, 0xff80
	v_cvt_pk_bf16_f32 v136, v76, v72
	s_sub_i32 s1, s15, s1
	v_cvt_pk_bf16_f32 v137, v68, v64
	v_cvt_pk_bf16_f32 v138, v92, v88
	v_cvt_pk_bf16_f32 v139, v84, v80
	ds_write_b128 v202, v[136:139]
	v_cvt_pk_bf16_f32 v136, v108, v104
	s_bfe_i32 s2, s1, 0x80000
	v_cvt_pk_bf16_f32 v137, v100, v96
	v_cvt_pk_bf16_f32 v138, v124, v120
	v_cvt_pk_bf16_f32 v139, v116, v112
	ds_write_b128 v203, v[136:139]
	v_cvt_pk_bf16_f32 v136, v77, v73
	s_bfe_u32 s2, s2, 0x2000d
	v_cvt_pk_bf16_f32 v137, v69, v65
	v_cvt_pk_bf16_f32 v138, v93, v89
	v_cvt_pk_bf16_f32 v139, v85, v81
	ds_write_b128 v202, v[136:139] offset:128
	v_cvt_pk_bf16_f32 v136, v109, v105
	s_add_i32 s2, s1, s2
	v_cvt_pk_bf16_f32 v137, v101, v97
	v_cvt_pk_bf16_f32 v138, v125, v121
	v_cvt_pk_bf16_f32 v139, v117, v113
	ds_write_b128 v203, v[136:139] offset:128
	v_cvt_pk_bf16_f32 v136, v78, v74
	s_bfe_i32 s3, s2, 0x80000
	v_cvt_pk_bf16_f32 v137, v70, v66
	v_cvt_pk_bf16_f32 v138, v94, v90
	v_cvt_pk_bf16_f32 v139, v86, v82
	ds_write_b128 v202, v[136:139] offset:256
	v_cvt_pk_bf16_f32 v136, v110, v106
	s_and_b32 s2, s2, 0xfc
	v_cvt_pk_bf16_f32 v137, v102, v98
	v_cvt_pk_bf16_f32 v138, v126, v122
	v_cvt_pk_bf16_f32 v139, v118, v114
	ds_write_b128 v203, v[136:139] offset:256
	v_cvt_pk_bf16_f32 v136, v79, v75
	s_sub_i32 s1, s1, s2
	v_cvt_pk_bf16_f32 v137, v71, v67
	v_cvt_pk_bf16_f32 v138, v95, v91
	v_cvt_pk_bf16_f32 v139, v87, v83
	ds_write_b128 v202, v[136:139] offset:384
	v_cvt_pk_bf16_f32 v136, v111, v107
	s_sext_i32_i8 s2, s1
	s_ashr_i32 s1, s0, 31
	v_cvt_pk_bf16_f32 v137, v103, v99
	v_cvt_pk_bf16_f32 v138, v127, v123
	v_cvt_pk_bf16_f32 v139, v119, v115
	ds_write_b128 v203, v[136:139] offset:384
	s_lshl_b64 s[0:1], s[0:1], 20
	v_lshl_add_u32 v136, s2, 6, v201
	s_add_u32 s0, s24, s0
	v_ashrrev_i32_e32 v137, 31, v136
	s_sext_i32_i16 s3, s3
	s_addc_u32 s1, s25, s1
	v_lshlrev_b64 v[136:137], 12, v[136:137]
	v_lshl_add_u64 v[140:141], s[0:1], 0, v[136:137]
	s_lshl_b32 s0, s3, 4
	ds_read_b128 v[136:139], v128
	s_andn2_b32 s0, s0, 63
	s_ashr_i32 s1, s0, 31
	v_lshl_add_u64 v[140:141], s[0:1], 1, v[140:141]
	v_lshl_add_u64 v[148:149], v[140:141], 0, v[194:195]
	ds_read_b128 v[140:143], v128 offset:4096
	s_waitcnt lgkmcnt(1)
	global_store_dwordx4 v[148:149], v[136:139], off nt
	ds_read_b128 v[136:139], v129
	ds_read_b128 v[144:147], v130
	v_add_co_u32_e32 v128, vcc, s28, v148
	s_nop 1
	v_addc_co_u32_e32 v129, vcc, 0, v149, vcc
	s_waitcnt lgkmcnt(1)
	global_store_dwordx4 v[128:129], v[136:139], off nt
	v_add_co_u32_e32 v128, vcc, s29, v148
	ds_read_b128 v[136:139], v132
	s_nop 0
	v_addc_co_u32_e32 v129, vcc, 0, v149, vcc
	s_waitcnt lgkmcnt(1)
	global_store_dwordx4 v[128:129], v[144:147], off nt
	ds_read_b128 v[128:131], v131
	s_nop 0
	v_add_co_u32_e32 v144, vcc, s30, v148
	s_nop 1
	v_addc_co_u32_e32 v145, vcc, 0, v149, vcc
	s_waitcnt lgkmcnt(0)
	global_store_dwordx4 v[144:145], v[128:131], off nt
	s_nop 1
	v_add_co_u32_e32 v128, vcc, s31, v148
	s_nop 1
	v_addc_co_u32_e32 v129, vcc, 0, v149, vcc
	global_store_dwordx4 v[128:129], v[140:143], off nt
	v_add_co_u32_e32 v128, vcc, 0x28000, v148
	s_nop 1
	v_addc_co_u32_e32 v129, vcc, 0, v149, vcc
	global_store_dwordx4 v[128:129], v[136:139], off nt
	ds_read_b128 v[128:131], v133
	ds_read_b128 v[132:135], v134
	v_add_co_u32_e32 v136, vcc, 0x30000, v148
	s_nop 1
	v_addc_co_u32_e32 v137, vcc, 0, v149, vcc
	s_waitcnt lgkmcnt(1)
	global_store_dwordx4 v[136:137], v[128:131], off nt
	s_nop 1
	v_add_co_u32_e32 v128, vcc, 0x38000, v148
	s_nop 1
	v_addc_co_u32_e32 v129, vcc, 0, v149, vcc
	s_waitcnt lgkmcnt(0)
	global_store_dwordx4 v[128:129], v[132:135], off nt
	s_branch .LBB0_95

.LBB0_107:
	s_ashr_i32 s0, s16, 31
	s_lshr_b32 s0, s0, 28
	s_add_i32 s1, s16, s0
	s_ashr_i32 s0, s1, 4
	s_and_b32 s1, s1, 0xfff0
	s_sub_i32 s1, s16, s1
	s_bfe_i32 s2, s1, 0x80000
	s_bfe_u32 s2, s2, 0x2000d
	s_add_i32 s2, s1, s2
	s_bfe_i32 s3, s2, 0x80000
	s_and_b32 s2, s2, 0xfffc
	s_sext_i32_i16 s3, s3
	s_sub_i32 s1, s1, s2
	s_ashr_i32 s28, s3, 2
	s_bfe_i32 s3, s1, 0x80000
	s_sext_i32_i8 s1, s1
	s_lshl_b32 s2, s1, 6
	s_sext_i32_i16 s1, s3
	s_cmp_gt_i32 s1, 0
	v_mov_b32_e32 v128, 0
	v_mov_b32_e32 v129, 0
	v_mov_b32_e32 v130, 0
	v_mov_b32_e32 v131, 0
	v_mov_b32_e32 v132, 0
	v_mov_b32_e32 v133, 0
	v_mov_b32_e32 v134, 0
	v_mov_b32_e32 v135, 0
	v_mov_b32_e32 v136, 0
	v_mov_b32_e32 v137, 0
	v_mov_b32_e32 v138, 0
	v_mov_b32_e32 v139, 0
	v_mov_b32_e32 v140, 0
	v_mov_b32_e32 v141, 0
	v_mov_b32_e32 v142, 0
	v_mov_b32_e32 v143, 0
	v_mov_b32_e32 v144, 0
	v_mov_b32_e32 v145, 0
	v_mov_b32_e32 v146, 0
	v_mov_b32_e32 v147, 0
	v_mov_b32_e32 v148, 0
	v_mov_b32_e32 v149, 0
	v_mov_b32_e32 v150, 0
	v_mov_b32_e32 v151, 0
	v_mov_b32_e32 v152, 0
	v_mov_b32_e32 v153, 0
	v_mov_b32_e32 v154, 0
	v_mov_b32_e32 v155, 0
	v_mov_b32_e32 v156, 0
	v_mov_b32_e32 v157, 0
	v_mov_b32_e32 v158, 0
	v_mov_b32_e32 v159, 0
	v_mov_b32_e32 v160, 0
	v_mov_b32_e32 v161, 0
	v_mov_b32_e32 v162, 0
	v_mov_b32_e32 v163, 0
	v_mov_b32_e32 v164, 0
	v_mov_b32_e32 v165, 0
	v_mov_b32_e32 v166, 0
	v_mov_b32_e32 v167, 0
	v_mov_b32_e32 v168, 0
	v_mov_b32_e32 v169, 0
	v_mov_b32_e32 v170, 0
	v_mov_b32_e32 v171, 0
	v_mov_b32_e32 v172, 0
	v_mov_b32_e32 v173, 0
	v_mov_b32_e32 v174, 0
	v_mov_b32_e32 v175, 0
	v_mov_b32_e32 v176, 0
	v_mov_b32_e32 v177, 0
	v_mov_b32_e32 v178, 0
	v_mov_b32_e32 v179, 0
	v_mov_b32_e32 v180, 0
	v_mov_b32_e32 v181, 0
	v_mov_b32_e32 v182, 0
	v_mov_b32_e32 v183, 0
	v_mov_b32_e32 v184, 0
	v_mov_b32_e32 v185, 0
	v_mov_b32_e32 v186, 0
	v_mov_b32_e32 v187, 0
	v_mov_b32_e32 v188, 0
	v_mov_b32_e32 v189, 0
	v_mov_b32_e32 v190, 0
	v_mov_b32_e32 v191, 0
	s_cbranch_scc1 .LBB0_109
	s_ashr_i32 s1, s0, 31
	v_readlane_b32 s40, v252, 4
	s_lshl_b64 s[4:5], s[0:1], 16
	v_readlane_b32 s50, v252, 14
	v_lshl_add_u32 v128, s28, 6, v193
	v_readlane_b32 s51, v252, 15
	s_add_u32 s4, s50, s4
	v_ashrrev_i32_e32 v129, 31, v128
	s_addc_u32 s5, s51, s5
	v_lshlrev_b64 v[128:129], 8, v[128:129]
	v_lshl_add_u64 v[128:129], s[4:5], 0, v[128:129]
	s_ashr_i32 s3, s2, 31
	v_lshl_add_u64 v[128:129], s[2:3], 2, v[128:129]
	v_mov_b32_e32 v197, v195
	v_lshl_add_u64 v[128:129], v[128:129], 0, v[196:197]
	global_load_dwordx4 v[188:191], v[128:129], off nt
	global_load_dwordx4 v[184:187], v[128:129], off offset:256 nt
	global_load_dwordx4 v[180:183], v[128:129], off offset:512 nt
	global_load_dwordx4 v[176:179], v[128:129], off offset:768 nt
	global_load_dwordx4 v[172:175], v[128:129], off offset:1024 nt
	global_load_dwordx4 v[168:171], v[128:129], off offset:1280 nt
	global_load_dwordx4 v[164:167], v[128:129], off offset:1536 nt
	global_load_dwordx4 v[160:163], v[128:129], off offset:1792 nt
	global_load_dwordx4 v[156:159], v[128:129], off offset:2048 nt
	global_load_dwordx4 v[152:155], v[128:129], off offset:2304 nt
	global_load_dwordx4 v[148:151], v[128:129], off offset:2560 nt
	global_load_dwordx4 v[144:147], v[128:129], off offset:2816 nt
	global_load_dwordx4 v[140:143], v[128:129], off offset:3072 nt
	global_load_dwordx4 v[136:139], v[128:129], off offset:3328 nt
	global_load_dwordx4 v[132:135], v[128:129], off offset:3584 nt
	s_nop 0
	global_load_dwordx4 v[128:131], v[128:129], off offset:3840 nt
	v_readlane_b32 s41, v252, 5
	v_readlane_b32 s42, v252, 6
	v_readlane_b32 s43, v252, 7
	v_readlane_b32 s44, v252, 8
	v_readlane_b32 s45, v252, 9
	v_readlane_b32 s46, v252, 10
	v_readlane_b32 s47, v252, 11
	v_readlane_b32 s48, v252, 12
	v_readlane_b32 s49, v252, 13
	v_readlane_b32 s52, v252, 16
	v_readlane_b32 s53, v252, 17
	v_readlane_b32 s54, v252, 18
	v_readlane_b32 s55, v252, 19
.LBB0_109:
	s_add_i32 s3, s8, s16
	s_cmp_lt_i32 s3, 32
	s_cselect_b64 s[4:5], -1, 0
	s_cmp_gt_i32 s3, 31
	s_cbranch_scc1 .LBB0_112
	s_ashr_i32 s1, s3, 31
	s_lshr_b32 s1, s1, 28
	s_add_i32 s1, s3, s1
	s_and_b32 s14, s1, 0xfff0
	s_sub_i32 s15, s3, s14
	s_bfe_i32 s14, s15, 0x80000
	s_bfe_u32 s14, s14, 0x2000d
	s_add_i32 s14, s15, s14
	s_and_b32 s29, s14, 0xfc
	s_sub_i32 s15, s15, s29
	s_bfe_i32 s15, s15, 0x80000
	s_sext_i32_i16 s15, s15
	v_mov_b32_e32 v3, 0
	s_cmp_gt_i32 s15, 0
	v_mov_b32_e32 v2, 0
	v_mov_b32_e32 v1, 0
	v_mov_b32_e32 v0, 0
	v_mov_b32_e32 v7, 0
	v_mov_b32_e32 v6, 0
	v_mov_b32_e32 v5, 0
	v_mov_b32_e32 v4, 0
	v_mov_b32_e32 v11, 0
	v_mov_b32_e32 v10, 0
	v_mov_b32_e32 v9, 0
	v_mov_b32_e32 v8, 0
	v_mov_b32_e32 v15, 0
	v_mov_b32_e32 v14, 0
	v_mov_b32_e32 v13, 0
	v_mov_b32_e32 v12, 0
	v_mov_b32_e32 v19, 0
	v_mov_b32_e32 v18, 0
	v_mov_b32_e32 v17, 0
	v_mov_b32_e32 v16, 0
	v_mov_b32_e32 v23, 0
	v_mov_b32_e32 v22, 0
	v_mov_b32_e32 v21, 0
	v_mov_b32_e32 v20, 0
	v_mov_b32_e32 v27, 0
	v_mov_b32_e32 v26, 0
	v_mov_b32_e32 v25, 0
	v_mov_b32_e32 v24, 0
	v_mov_b32_e32 v31, 0
	v_mov_b32_e32 v30, 0
	v_mov_b32_e32 v29, 0
	v_mov_b32_e32 v28, 0
	v_mov_b32_e32 v35, 0
	v_mov_b32_e32 v34, 0
	v_mov_b32_e32 v33, 0
	v_mov_b32_e32 v32, 0
	v_mov_b32_e32 v39, 0
	v_mov_b32_e32 v38, 0
	v_mov_b32_e32 v37, 0
	v_mov_b32_e32 v36, 0
	v_mov_b32_e32 v43, 0
	v_mov_b32_e32 v42, 0
	v_mov_b32_e32 v41, 0
	v_mov_b32_e32 v40, 0
	v_mov_b32_e32 v47, 0
	v_mov_b32_e32 v46, 0
	v_mov_b32_e32 v45, 0
	v_mov_b32_e32 v44, 0
	v_mov_b32_e32 v51, 0
	v_mov_b32_e32 v50, 0
	v_mov_b32_e32 v49, 0
	v_mov_b32_e32 v48, 0
	v_mov_b32_e32 v55, 0
	v_mov_b32_e32 v54, 0
	v_mov_b32_e32 v53, 0
	v_mov_b32_e32 v52, 0
	v_mov_b32_e32 v59, 0
	v_mov_b32_e32 v58, 0
	v_mov_b32_e32 v57, 0
	v_mov_b32_e32 v56, 0
	v_mov_b32_e32 v63, 0
	v_mov_b32_e32 v62, 0
	v_mov_b32_e32 v61, 0
	v_mov_b32_e32 v60, 0
	s_cbranch_scc1 .LBB0_112
	s_bfe_i32 s14, s14, 0x80000
	s_sext_i32_i16 s14, s14
	s_lshr_b32 s29, s14, 2
	s_ashr_i32 s30, s1, 4
	s_lshl_b32 s14, s15, 6
	s_sext_i32_i8 s15, s29
	s_ashr_i32 s31, s30, 31
	v_readlane_b32 s40, v252, 4
	s_lshl_b64 s[30:31], s[30:31], 16
	v_readlane_b32 s50, v252, 14
	v_lshl_add_u32 v0, s15, 6, v193
	v_readlane_b32 s51, v252, 15
	s_add_u32 s30, s50, s30
	v_ashrrev_i32_e32 v1, 31, v0
	s_addc_u32 s31, s51, s31
	v_lshlrev_b64 v[0:1], 8, v[0:1]
	v_lshl_add_u64 v[0:1], s[30:31], 0, v[0:1]
	s_ashr_i32 s15, s14, 31
	v_lshl_add_u64 v[0:1], s[14:15], 2, v[0:1]
	v_mov_b32_e32 v197, v195
	v_lshl_add_u64 v[60:61], v[0:1], 0, v[196:197]
	global_load_dwordx4 v[0:3], v[60:61], off nt
	global_load_dwordx4 v[4:7], v[60:61], off offset:256 nt
	global_load_dwordx4 v[8:11], v[60:61], off offset:512 nt
	global_load_dwordx4 v[12:15], v[60:61], off offset:768 nt
	global_load_dwordx4 v[16:19], v[60:61], off offset:1024 nt
	global_load_dwordx4 v[20:23], v[60:61], off offset:1280 nt
	global_load_dwordx4 v[24:27], v[60:61], off offset:1536 nt
	global_load_dwordx4 v[28:31], v[60:61], off offset:1792 nt
	global_load_dwordx4 v[32:35], v[60:61], off offset:2048 nt
	global_load_dwordx4 v[36:39], v[60:61], off offset:2304 nt
	global_load_dwordx4 v[40:43], v[60:61], off offset:2560 nt
	global_load_dwordx4 v[44:47], v[60:61], off offset:2816 nt
	global_load_dwordx4 v[48:51], v[60:61], off offset:3072 nt
	global_load_dwordx4 v[52:55], v[60:61], off offset:3328 nt
	global_load_dwordx4 v[56:59], v[60:61], off offset:3584 nt
	s_nop 0
	global_load_dwordx4 v[60:63], v[60:61], off offset:3840 nt
	v_readlane_b32 s41, v252, 5
	v_readlane_b32 s42, v252, 6
	v_readlane_b32 s43, v252, 7
	v_readlane_b32 s44, v252, 8
	v_readlane_b32 s45, v252, 9
	v_readlane_b32 s46, v252, 10
	v_readlane_b32 s47, v252, 11
	v_readlane_b32 s48, v252, 12
	v_readlane_b32 s49, v252, 13
	v_readlane_b32 s52, v252, 16
	v_readlane_b32 s53, v252, 17
	v_readlane_b32 s54, v252, 18
	v_readlane_b32 s55, v252, 19
.LBB0_112:
	s_add_i32 s29, s24, s16
	s_cmp_lt_i32 s29, 32
	s_cselect_b64 s[14:15], -1, 0
	s_cmp_gt_i32 s29, 31
	s_cbranch_scc1 .LBB0_115
	s_ashr_i32 s1, s29, 31
	s_lshr_b32 s1, s1, 28
	s_add_i32 s1, s29, s1
	s_and_b32 s30, s1, 0xfff0
	s_sub_i32 s31, s29, s30
	s_bfe_i32 s30, s31, 0x80000
	s_bfe_u32 s30, s30, 0x2000d
	s_add_i32 s30, s31, s30
	s_and_b32 s35, s30, 0xfc
	s_sub_i32 s31, s31, s35
	s_bfe_i32 s31, s31, 0x80000
	s_sext_i32_i16 s31, s31
	v_mov_b32_e32 v67, 0
	s_cmp_gt_i32 s31, 0
	v_mov_b32_e32 v66, 0
	v_mov_b32_e32 v65, 0
	v_mov_b32_e32 v64, 0
	v_mov_b32_e32 v71, 0
	v_mov_b32_e32 v70, 0
	v_mov_b32_e32 v69, 0
	v_mov_b32_e32 v68, 0
	v_mov_b32_e32 v75, 0
	v_mov_b32_e32 v74, 0
	v_mov_b32_e32 v73, 0
	v_mov_b32_e32 v72, 0
	v_mov_b32_e32 v79, 0
	v_mov_b32_e32 v78, 0
	v_mov_b32_e32 v77, 0
	v_mov_b32_e32 v76, 0
	v_mov_b32_e32 v83, 0
	v_mov_b32_e32 v82, 0
	v_mov_b32_e32 v81, 0
	v_mov_b32_e32 v80, 0
	v_mov_b32_e32 v87, 0
	v_mov_b32_e32 v86, 0
	v_mov_b32_e32 v85, 0
	v_mov_b32_e32 v84, 0
	v_mov_b32_e32 v91, 0
	v_mov_b32_e32 v90, 0
	v_mov_b32_e32 v89, 0
	v_mov_b32_e32 v88, 0
	v_mov_b32_e32 v95, 0
	v_mov_b32_e32 v94, 0
	v_mov_b32_e32 v93, 0
	v_mov_b32_e32 v92, 0
	v_mov_b32_e32 v99, 0
	v_mov_b32_e32 v98, 0
	v_mov_b32_e32 v97, 0
	v_mov_b32_e32 v96, 0
	v_mov_b32_e32 v103, 0
	v_mov_b32_e32 v102, 0
	v_mov_b32_e32 v101, 0
	v_mov_b32_e32 v100, 0
	v_mov_b32_e32 v107, 0
	v_mov_b32_e32 v106, 0
	v_mov_b32_e32 v105, 0
	v_mov_b32_e32 v104, 0
	v_mov_b32_e32 v111, 0
	v_mov_b32_e32 v110, 0
	v_mov_b32_e32 v109, 0
	v_mov_b32_e32 v108, 0
	v_mov_b32_e32 v115, 0
	v_mov_b32_e32 v114, 0
	v_mov_b32_e32 v113, 0
	v_mov_b32_e32 v112, 0
	v_mov_b32_e32 v119, 0
	v_mov_b32_e32 v118, 0
	v_mov_b32_e32 v117, 0
	v_mov_b32_e32 v116, 0
	v_mov_b32_e32 v123, 0
	v_mov_b32_e32 v122, 0
	v_mov_b32_e32 v121, 0
	v_mov_b32_e32 v120, 0
	v_mov_b32_e32 v127, 0
	v_mov_b32_e32 v126, 0
	v_mov_b32_e32 v125, 0
	v_mov_b32_e32 v124, 0
	s_cbranch_scc1 .LBB0_115
	s_bfe_i32 s30, s30, 0x80000
	s_sext_i32_i16 s30, s30
	s_lshr_b32 s35, s30, 2
	s_ashr_i32 s40, s1, 4
	s_lshl_b32 s30, s31, 6
	s_sext_i32_i8 s31, s35
	s_ashr_i32 s41, s40, 31
	v_readlane_b32 s44, v252, 4
	s_lshl_b64 s[40:41], s[40:41], 16
	v_readlane_b32 s54, v252, 14
	v_lshl_add_u32 v64, s31, 6, v193
	v_readlane_b32 s55, v252, 15
	s_add_u32 s40, s54, s40
	v_ashrrev_i32_e32 v65, 31, v64
	s_addc_u32 s41, s55, s41
	v_lshlrev_b64 v[64:65], 8, v[64:65]
	v_lshl_add_u64 v[64:65], s[40:41], 0, v[64:65]
	s_ashr_i32 s31, s30, 31
	v_lshl_add_u64 v[64:65], s[30:31], 2, v[64:65]
	v_mov_b32_e32 v197, v195
	v_lshl_add_u64 v[124:125], v[64:65], 0, v[196:197]
	global_load_dwordx4 v[64:67], v[124:125], off nt
	global_load_dwordx4 v[68:71], v[124:125], off offset:256 nt
	global_load_dwordx4 v[72:75], v[124:125], off offset:512 nt
	global_load_dwordx4 v[76:79], v[124:125], off offset:768 nt
	global_load_dwordx4 v[80:83], v[124:125], off offset:1024 nt
	global_load_dwordx4 v[84:87], v[124:125], off offset:1280 nt
	global_load_dwordx4 v[88:91], v[124:125], off offset:1536 nt
	global_load_dwordx4 v[92:95], v[124:125], off offset:1792 nt
	global_load_dwordx4 v[96:99], v[124:125], off offset:2048 nt
	global_load_dwordx4 v[100:103], v[124:125], off offset:2304 nt
	global_load_dwordx4 v[104:107], v[124:125], off offset:2560 nt
	global_load_dwordx4 v[108:111], v[124:125], off offset:2816 nt
	global_load_dwordx4 v[112:115], v[124:125], off offset:3072 nt
	global_load_dwordx4 v[116:119], v[124:125], off offset:3328 nt
	global_load_dwordx4 v[120:123], v[124:125], off offset:3584 nt
	s_nop 0
	global_load_dwordx4 v[124:127], v[124:125], off offset:3840 nt
	v_readlane_b32 s45, v252, 5
	v_readlane_b32 s46, v252, 6
	v_readlane_b32 s47, v252, 7
	v_readlane_b32 s48, v252, 8
	v_readlane_b32 s49, v252, 9
	v_readlane_b32 s50, v252, 10
	v_readlane_b32 s51, v252, 11
	v_readlane_b32 s52, v252, 12
	v_readlane_b32 s53, v252, 13
	v_readlane_b32 s56, v252, 16
	v_readlane_b32 s57, v252, 17
	v_readlane_b32 s58, v252, 18
	v_readlane_b32 s59, v252, 19
.LBB0_115:
	s_waitcnt vmcnt(14)
	v_cvt_pk_bf16_f32 v218, v188, v184
	s_waitcnt vmcnt(12)
	v_cvt_pk_bf16_f32 v219, v180, v176
	s_waitcnt vmcnt(10)
	v_cvt_pk_bf16_f32 v220, v172, v168
	s_waitcnt vmcnt(8)
	v_cvt_pk_bf16_f32 v221, v164, v160
	ds_write_b128 v202, v[218:221]
	s_waitcnt vmcnt(6)
	v_cvt_pk_bf16_f32 v218, v156, v152
	s_waitcnt vmcnt(4)
	v_cvt_pk_bf16_f32 v219, v148, v144
	s_waitcnt vmcnt(2)
	v_cvt_pk_bf16_f32 v220, v140, v136
	s_waitcnt vmcnt(0)
	v_cvt_pk_bf16_f32 v221, v132, v128
	ds_write_b128 v203, v[218:221]
	v_cvt_pk_bf16_f32 v218, v189, v185
	v_cvt_pk_bf16_f32 v219, v181, v177
	v_cvt_pk_bf16_f32 v220, v173, v169
	v_cvt_pk_bf16_f32 v221, v165, v161
	ds_write_b128 v202, v[218:221] offset:128
	v_cvt_pk_bf16_f32 v218, v157, v153
	v_cvt_pk_bf16_f32 v219, v149, v145
	v_cvt_pk_bf16_f32 v220, v141, v137
	v_cvt_pk_bf16_f32 v221, v133, v129
	ds_write_b128 v203, v[218:221] offset:128
	v_cvt_pk_bf16_f32 v218, v190, v186
	v_cvt_pk_bf16_f32 v219, v182, v178
	v_cvt_pk_bf16_f32 v220, v174, v170
	v_cvt_pk_bf16_f32 v221, v166, v162
	ds_write_b128 v202, v[218:221] offset:256
	v_cvt_pk_bf16_f32 v218, v158, v154
	v_cvt_pk_bf16_f32 v219, v150, v146
	v_cvt_pk_bf16_f32 v220, v142, v138
	v_cvt_pk_bf16_f32 v221, v134, v130
	ds_write_b128 v203, v[218:221] offset:256
	v_cvt_pk_bf16_f32 v160, v191, v187
	v_cvt_pk_bf16_f32 v161, v183, v179
	v_cvt_pk_bf16_f32 v162, v175, v171
	v_cvt_pk_bf16_f32 v163, v167, v163
	ds_write_b128 v202, v[160:163] offset:384
	v_cvt_pk_bf16_f32 v128, v159, v155
	s_ashr_i32 s1, s0, 31
	v_cvt_pk_bf16_f32 v129, v151, v147
	v_cvt_pk_bf16_f32 v130, v143, v139
	v_cvt_pk_bf16_f32 v131, v135, v131
	ds_write_b128 v203, v[128:131] offset:384
	s_lshl_b64 s[0:1], s[0:1], 17
	v_add_u32_e32 v128, s2, v201
	s_add_u32 s0, s17, s0
	v_ashrrev_i32_e32 v129, 31, v128
	s_addc_u32 s1, s23, s1
	v_lshlrev_b64 v[128:129], 9, v[128:129]
	v_lshl_add_u64 v[134:135], s[0:1], 0, v[128:129]
	v_add_u32_e32 v128, v204, v205
	ds_read_b128 v[130:133], v128
	s_lshl_b32 s0, s28, 6
	s_ashr_i32 s1, s0, 31
	v_lshl_add_u64 v[134:135], s[0:1], 1, v[134:135]
	v_lshl_add_u64 v[146:147], v[134:135], 0, v[194:195]
	ds_read_b128 v[134:137], v128 offset:4096
	s_waitcnt lgkmcnt(1)
	global_store_dwordx4 v[146:147], v[130:133], off nt
	v_add_u32_e32 v129, v206, v207
	s_nop 0
	v_add_u32_e32 v130, v208, v209
	ds_read_b128 v[138:141], v129
	ds_read_b128 v[142:145], v130
	v_add_co_u32_e32 v132, vcc, s25, v146
	v_add_u32_e32 v131, v210, v211
	s_nop 0
	v_addc_co_u32_e32 v133, vcc, 0, v147, vcc
	s_waitcnt lgkmcnt(1)
	global_store_dwordx4 v[132:133], v[138:141], off offset:-4096 nt
	s_waitcnt lgkmcnt(0)
	global_store_dwordx4 v[132:133], v[142:145], off nt
	ds_read_b128 v[138:141], v131
	v_add_u32_e32 v132, v212, v213
	v_add_co_u32_e32 v148, vcc, s26, v146
	ds_read_b128 v[142:145], v132
	s_nop 0
	v_addc_co_u32_e32 v149, vcc, 0, v147, vcc
	s_waitcnt lgkmcnt(1)
	global_store_dwordx4 v[148:149], v[138:141], off offset:-4096 nt
	global_store_dwordx4 v[148:149], v[134:137], off nt
	v_add_u32_e32 v133, v214, v215
	ds_read_b128 v[136:139], v133
	v_add_co_u32_e32 v134, vcc, s27, v146
	s_nop 1
	v_addc_co_u32_e32 v135, vcc, 0, v147, vcc
	s_waitcnt lgkmcnt(1)
	global_store_dwordx4 v[134:135], v[142:145], off nt
	v_add_u32_e32 v134, v216, v217
	ds_read_b128 v[140:143], v134
	v_add_co_u32_e32 v144, vcc, 0x6000, v146
	s_nop 1
	v_addc_co_u32_e32 v145, vcc, 0, v147, vcc
	s_waitcnt lgkmcnt(1)
	global_store_dwordx4 v[144:145], v[136:139], off nt
	s_nop 1
	v_add_co_u32_e32 v136, vcc, 0x7000, v146
	s_nop 1
	v_addc_co_u32_e32 v137, vcc, 0, v147, vcc
	s_andn2_b64 vcc, exec, s[4:5]
	s_waitcnt lgkmcnt(0)
	global_store_dwordx4 v[136:137], v[140:143], off nt
	s_cbranch_vccz .LBB0_117
	s_andn2_b64 vcc, exec, s[14:15]
	s_cbranch_vccnz .LBB0_106
	s_branch .LBB0_118
.LBB0_117:
	s_ashr_i32 s0, s3, 31
	s_lshr_b32 s0, s0, 28
	s_add_i32 s1, s3, s0
	s_ashr_i32 s0, s1, 4
	s_and_b32 s1, s1, 0xfff0
	v_cvt_pk_bf16_f32 v136, v0, v4
	s_sub_i32 s1, s3, s1
	v_cvt_pk_bf16_f32 v137, v8, v12
	v_cvt_pk_bf16_f32 v138, v16, v20
	v_cvt_pk_bf16_f32 v139, v24, v28
	ds_write_b128 v202, v[136:139]
	v_cvt_pk_bf16_f32 v136, v32, v36
	s_bfe_i32 s2, s1, 0x80000
	v_cvt_pk_bf16_f32 v137, v40, v44
	v_cvt_pk_bf16_f32 v138, v48, v52
	v_cvt_pk_bf16_f32 v139, v56, v60
	ds_write_b128 v203, v[136:139]
	v_cvt_pk_bf16_f32 v136, v1, v5
	s_bfe_u32 s2, s2, 0x2000d
	v_cvt_pk_bf16_f32 v137, v9, v13
	v_cvt_pk_bf16_f32 v138, v17, v21
	v_cvt_pk_bf16_f32 v139, v25, v29
	ds_write_b128 v202, v[136:139] offset:128
	v_cvt_pk_bf16_f32 v136, v33, v37
	s_add_i32 s2, s1, s2
	v_cvt_pk_bf16_f32 v137, v41, v45
	v_cvt_pk_bf16_f32 v138, v49, v53
	v_cvt_pk_bf16_f32 v139, v57, v61
	ds_write_b128 v203, v[136:139] offset:128
	v_cvt_pk_bf16_f32 v136, v2, v6
	s_bfe_i32 s3, s2, 0x80000
	s_and_b32 s2, s2, 0xfc
	v_cvt_pk_bf16_f32 v137, v10, v14
	v_cvt_pk_bf16_f32 v138, v18, v22
	v_cvt_pk_bf16_f32 v139, v26, v30
	ds_write_b128 v202, v[136:139] offset:256
	v_cvt_pk_bf16_f32 v136, v34, v38
	s_sub_i32 s1, s1, s2
	v_cvt_pk_bf16_f32 v137, v42, v46
	v_cvt_pk_bf16_f32 v138, v50, v54
	v_cvt_pk_bf16_f32 v139, v58, v62
	ds_write_b128 v203, v[136:139] offset:256
	v_cvt_pk_bf16_f32 v136, v3, v7
	v_cvt_pk_bf16_f32 v137, v11, v15
	v_cvt_pk_bf16_f32 v138, v19, v23
	v_cvt_pk_bf16_f32 v139, v27, v31
	ds_write_b128 v202, v[136:139] offset:384
	v_cvt_pk_bf16_f32 v136, v35, v39
	s_sext_i32_i8 s2, s1
	s_ashr_i32 s1, s0, 31
	v_cvt_pk_bf16_f32 v137, v43, v47
	v_cvt_pk_bf16_f32 v138, v51, v55
	v_cvt_pk_bf16_f32 v139, v59, v63
	ds_write_b128 v203, v[136:139] offset:384
	s_lshl_b64 s[0:1], s[0:1], 17
	v_lshl_add_u32 v136, s2, 6, v201
	s_add_u32 s0, s17, s0
	v_ashrrev_i32_e32 v137, 31, v136
	s_sext_i32_i16 s3, s3
	s_addc_u32 s1, s23, s1
	v_lshlrev_b64 v[136:137], 9, v[136:137]
	v_lshl_add_u64 v[140:141], s[0:1], 0, v[136:137]
	s_lshl_b32 s0, s3, 4
	ds_read_b128 v[136:139], v128
	s_andn2_b32 s0, s0, 63
	s_ashr_i32 s1, s0, 31
	v_lshl_add_u64 v[140:141], s[0:1], 1, v[140:141]
	v_lshl_add_u64 v[148:149], v[140:141], 0, v[194:195]
	ds_read_b128 v[140:143], v128 offset:4096
	s_waitcnt lgkmcnt(1)
	global_store_dwordx4 v[148:149], v[136:139], off nt
	ds_read_b128 v[136:139], v129
	ds_read_b128 v[144:147], v130
	v_add_co_u32_e32 v150, vcc, s25, v148
	s_nop 1
	v_addc_co_u32_e32 v151, vcc, 0, v149, vcc
	s_waitcnt lgkmcnt(1)
	global_store_dwordx4 v[150:151], v[136:139], off offset:-4096 nt
	s_waitcnt lgkmcnt(0)
	global_store_dwordx4 v[150:151], v[144:147], off nt
	ds_read_b128 v[136:139], v131
	ds_read_b128 v[144:147], v132
	v_add_co_u32_e32 v150, vcc, s26, v148
	s_nop 1
	v_addc_co_u32_e32 v151, vcc, 0, v149, vcc
	s_waitcnt lgkmcnt(1)
	global_store_dwordx4 v[150:151], v[136:139], off offset:-4096 nt
	global_store_dwordx4 v[150:151], v[140:143], off nt
	ds_read_b128 v[140:143], v134
	v_add_co_u32_e32 v136, vcc, 0x5000, v148
	s_nop 1
	v_addc_co_u32_e32 v137, vcc, 0, v149, vcc
	s_waitcnt lgkmcnt(1)
	global_store_dwordx4 v[136:137], v[144:147], off nt
	ds_read_b128 v[136:139], v133
	s_nop 0
	v_add_co_u32_e32 v144, vcc, 0x6000, v148
	s_nop 1
	v_addc_co_u32_e32 v145, vcc, 0, v149, vcc
	s_waitcnt lgkmcnt(0)
	global_store_dwordx4 v[144:145], v[136:139], off nt
	s_nop 1
	v_add_co_u32_e32 v136, vcc, 0x7000, v148
	s_nop 1
	v_addc_co_u32_e32 v137, vcc, 0, v149, vcc
	global_store_dwordx4 v[136:137], v[140:143], off nt
	s_andn2_b64 vcc, exec, s[14:15]
	s_cbranch_vccnz .LBB0_106
.LBB0_118:
	s_ashr_i32 s0, s29, 31
	s_lshr_b32 s0, s0, 28
	s_add_i32 s1, s29, s0
	s_ashr_i32 s0, s1, 4
	s_and_b32 s1, s1, 0xfff0
	v_cvt_pk_bf16_f32 v136, v64, v68
	s_sub_i32 s1, s29, s1
	v_cvt_pk_bf16_f32 v137, v72, v76
	v_cvt_pk_bf16_f32 v138, v80, v84
	v_cvt_pk_bf16_f32 v139, v88, v92
	ds_write_b128 v202, v[136:139]
	v_cvt_pk_bf16_f32 v136, v96, v100
	s_bfe_i32 s2, s1, 0x80000
	v_cvt_pk_bf16_f32 v137, v104, v108
	v_cvt_pk_bf16_f32 v138, v112, v116
	v_cvt_pk_bf16_f32 v139, v120, v124
	ds_write_b128 v203, v[136:139]
	v_cvt_pk_bf16_f32 v136, v65, v69
	s_bfe_u32 s2, s2, 0x2000d
	v_cvt_pk_bf16_f32 v137, v73, v77
	v_cvt_pk_bf16_f32 v138, v81, v85
	v_cvt_pk_bf16_f32 v139, v89, v93
	ds_write_b128 v202, v[136:139] offset:128
	v_cvt_pk_bf16_f32 v136, v97, v101
	s_add_i32 s2, s1, s2
	v_cvt_pk_bf16_f32 v137, v105, v109
	v_cvt_pk_bf16_f32 v138, v113, v117
	v_cvt_pk_bf16_f32 v139, v121, v125
	ds_write_b128 v203, v[136:139] offset:128
	v_cvt_pk_bf16_f32 v136, v66, v70
	s_bfe_i32 s3, s2, 0x80000
	s_and_b32 s2, s2, 0xfc
	v_cvt_pk_bf16_f32 v137, v74, v78
	v_cvt_pk_bf16_f32 v138, v82, v86
	v_cvt_pk_bf16_f32 v139, v90, v94
	ds_write_b128 v202, v[136:139] offset:256
	v_cvt_pk_bf16_f32 v136, v98, v102
	s_sub_i32 s1, s1, s2
	v_cvt_pk_bf16_f32 v137, v106, v110
	v_cvt_pk_bf16_f32 v138, v114, v118
	v_cvt_pk_bf16_f32 v139, v122, v126
	ds_write_b128 v203, v[136:139] offset:256
	v_cvt_pk_bf16_f32 v136, v67, v71
	v_cvt_pk_bf16_f32 v137, v75, v79
	v_cvt_pk_bf16_f32 v138, v83, v87
	v_cvt_pk_bf16_f32 v139, v91, v95
	ds_write_b128 v202, v[136:139] offset:384
	v_cvt_pk_bf16_f32 v136, v99, v103
	s_sext_i32_i8 s2, s1
	s_ashr_i32 s1, s0, 31
	v_cvt_pk_bf16_f32 v137, v107, v111
	v_cvt_pk_bf16_f32 v138, v115, v119
	v_cvt_pk_bf16_f32 v139, v123, v127
	ds_write_b128 v203, v[136:139] offset:384
	s_lshl_b64 s[0:1], s[0:1], 17
	v_lshl_add_u32 v136, s2, 6, v201
	s_add_u32 s0, s17, s0
	v_ashrrev_i32_e32 v137, 31, v136
	s_sext_i32_i16 s3, s3
	s_addc_u32 s1, s23, s1
	v_lshlrev_b64 v[136:137], 9, v[136:137]
	v_lshl_add_u64 v[140:141], s[0:1], 0, v[136:137]
	s_lshl_b32 s0, s3, 4
	ds_read_b128 v[136:139], v128
	s_andn2_b32 s0, s0, 63
	s_ashr_i32 s1, s0, 31
	v_lshl_add_u64 v[140:141], s[0:1], 1, v[140:141]
	v_lshl_add_u64 v[148:149], v[140:141], 0, v[194:195]
	ds_read_b128 v[140:143], v128 offset:4096
	s_waitcnt lgkmcnt(1)
	global_store_dwordx4 v[148:149], v[136:139], off nt
	ds_read_b128 v[136:139], v129
	ds_read_b128 v[144:147], v130
	v_add_co_u32_e32 v128, vcc, s25, v148
	s_nop 1
	v_addc_co_u32_e32 v129, vcc, 0, v149, vcc
	s_waitcnt lgkmcnt(1)
	global_store_dwordx4 v[128:129], v[136:139], off offset:-4096 nt
	s_waitcnt lgkmcnt(0)
	global_store_dwordx4 v[128:129], v[144:147], off nt
	ds_read_b128 v[128:131], v131
	ds_read_b128 v[136:139], v132
	v_add_co_u32_e32 v144, vcc, s26, v148
	s_nop 1
	v_addc_co_u32_e32 v145, vcc, 0, v149, vcc
	s_waitcnt lgkmcnt(1)
	global_store_dwordx4 v[144:145], v[128:131], off offset:-4096 nt
	global_store_dwordx4 v[144:145], v[140:143], off nt
	s_nop 0
	v_add_co_u32_e32 v128, vcc, 0x5000, v148
	s_nop 1
	v_addc_co_u32_e32 v129, vcc, 0, v149, vcc
	s_waitcnt lgkmcnt(0)
	global_store_dwordx4 v[128:129], v[136:139], off nt
	ds_read_b128 v[128:131], v133
	ds_read_b128 v[132:135], v134
	v_add_co_u32_e32 v136, vcc, 0x6000, v148
	s_nop 1
	v_addc_co_u32_e32 v137, vcc, 0, v149, vcc
	s_waitcnt lgkmcnt(1)
	global_store_dwordx4 v[136:137], v[128:131], off nt
	s_nop 1
	v_add_co_u32_e32 v128, vcc, 0x7000, v148
	s_nop 1
	v_addc_co_u32_e32 v129, vcc, 0, v149, vcc
	s_waitcnt lgkmcnt(0)
	global_store_dwordx4 v[128:129], v[132:135], off nt
	s_branch .LBB0_106

.LBB0_122:
	s_add_i32 s43, s8, s23
	s_cmpk_lt_i32 s43, 0x180
	s_cselect_b64 s[2:3], -1, 0
	s_ashr_i32 s0, s23, 31
	s_lshr_b32 s0, s0, 25
	s_add_i32 s0, s23, s0
	s_ashr_i32 s4, s0, 7
	s_and_b32 s0, s0, 0xff80
	s_sub_i32 s0, s23, s0
	s_bfe_i32 s1, s0, 0x80000
	s_bfe_u32 s1, s1, 0x4000b
	s_add_i32 s1, s0, s1
	s_bfe_i32 s5, s1, 0x80000
	s_and_b32 s1, s1, 0xf0
	s_sub_i32 s0, s0, s1
	s_sext_i32_i16 s14, s5
	s_sext_i32_i8 s0, s0
	s_ashr_i32 s5, s4, 31
	v_readlane_b32 s44, v252, 4
	s_lshl_b32 s16, s0, 6
	s_lshl_b64 s[0:1], s[4:5], 21
	v_readlane_b32 s58, v252, 18
	v_readlane_b32 s59, v252, 19
	s_add_u32 s0, s58, s0
	s_addc_u32 s1, s59, s1
	s_lshl_b32 s14, s14, 2
	s_andn2_b32 s14, s14, 63
	v_add_u32_e32 v128, s14, v193
	v_ashrrev_i32_e32 v129, 31, v128
	v_lshlrev_b64 v[128:129], 12, v[128:129]
	s_ashr_i32 s17, s16, 31
	v_lshl_add_u64 v[128:129], s[0:1], 0, v[128:129]
	v_lshl_add_u64 v[128:129], s[16:17], 2, v[128:129]
	v_lshl_add_u64 v[180:181], v[128:129], 0, v[198:199]
	v_add_co_u32_e32 v128, vcc, s27, v180
	s_cmpk_gt_i32 s43, 0x17f
	s_nop 0
	v_addc_co_u32_e32 v129, vcc, 0, v181, vcc
	v_add_co_u32_e32 v136, vcc, s28, v180
	global_load_dwordx4 v[132:135], v[128:129], off offset:-4096 nt
	s_nop 0
	global_load_dwordx4 v[128:131], v[128:129], off nt
	v_addc_co_u32_e32 v137, vcc, 0, v181, vcc
	v_add_co_u32_e32 v140, vcc, s29, v180
	global_load_dwordx4 v[144:147], v[136:137], off offset:-4096 nt
	s_nop 0
	global_load_dwordx4 v[136:139], v[136:137], off nt
	v_addc_co_u32_e32 v141, vcc, 0, v181, vcc
	global_load_dwordx4 v[152:155], v[140:141], off offset:-4096 nt
	global_load_dwordx4 v[148:151], v[140:141], off nt
	v_add_co_u32_e32 v140, vcc, s30, v180
	v_readlane_b32 s45, v252, 5
	s_nop 0
	v_addc_co_u32_e32 v141, vcc, 0, v181, vcc
	v_add_co_u32_e32 v156, vcc, s31, v180
	global_load_dwordx4 v[160:163], v[140:141], off offset:-4096 nt
	s_nop 0
	global_load_dwordx4 v[140:143], v[140:141], off nt
	v_addc_co_u32_e32 v157, vcc, 0, v181, vcc
	v_add_co_u32_e32 v168, vcc, s39, v180
	global_load_dwordx4 v[164:167], v[156:157], off offset:-4096 nt
	s_nop 0
	global_load_dwordx4 v[156:159], v[156:157], off nt
	v_addc_co_u32_e32 v169, vcc, 0, v181, vcc
	v_add_co_u32_e32 v176, vcc, 0xd000, v180
	global_load_dwordx4 v[172:175], v[168:169], off offset:-4096 nt
	s_nop 0
	global_load_dwordx4 v[168:171], v[168:169], off nt
	v_addc_co_u32_e32 v177, vcc, 0, v181, vcc
	v_add_co_u32_e32 v182, vcc, 0xe000, v180
	global_load_dwordx4 v[188:191], v[180:181], off nt
	s_nop 0
	global_load_dwordx4 v[176:179], v[176:177], off nt
	v_addc_co_u32_e32 v183, vcc, 0, v181, vcc
	v_add_co_u32_e32 v184, vcc, 0xf000, v180
	v_readlane_b32 s46, v252, 6
	s_nop 0
	v_addc_co_u32_e32 v185, vcc, 0, v181, vcc
	global_load_dwordx4 v[180:183], v[182:183], off nt
	s_nop 0
	global_load_dwordx4 v[184:187], v[184:185], off nt
	v_readlane_b32 s47, v252, 7
	v_readlane_b32 s48, v252, 8
	v_readlane_b32 s49, v252, 9
	v_readlane_b32 s50, v252, 10
	v_readlane_b32 s51, v252, 11
	v_readlane_b32 s52, v252, 12
	v_readlane_b32 s53, v252, 13
	v_readlane_b32 s54, v252, 14
	v_readlane_b32 s55, v252, 15
	v_readlane_b32 s56, v252, 16
	v_readlane_b32 s57, v252, 17
	s_cbranch_scc1 .LBB0_124
	s_ashr_i32 s0, s43, 31
	s_lshr_b32 s0, s0, 25
	s_add_i32 s1, s43, s0
	s_and_b32 s0, s1, 0x80
	s_sub_i32 s0, s43, s0
	s_bfe_i32 s15, s0, 0x80000
	s_bfe_u32 s15, s15, 0x4000b
	s_add_i32 s15, s0, s15
	s_bfe_i32 s17, s15, 0x80000
	s_and_b32 s15, s15, 0xf0
	s_sub_i32 s0, s0, s15
	s_ashr_i32 s44, s1, 7
	s_sext_i32_i8 s0, s0
	s_ashr_i32 s45, s44, 31
	v_readlane_b32 s48, v252, 4
	s_lshl_b32 s0, s0, 6
	s_lshl_b64 s[44:45], s[44:45], 21
	v_readlane_b32 s62, v252, 18
	s_sext_i32_i16 s17, s17
	v_readlane_b32 s63, v252, 19
	s_add_u32 s44, s62, s44
	s_addc_u32 s45, s63, s45
	s_lshl_b32 s1, s17, 2
	s_andn2_b32 s1, s1, 63
	v_add_u32_e32 v0, s1, v193
	v_ashrrev_i32_e32 v1, 31, v0
	v_lshlrev_b64 v[0:1], 12, v[0:1]
	v_lshl_add_u64 v[0:1], s[44:45], 0, v[0:1]
	s_ashr_i32 s1, s0, 31
	v_lshl_add_u64 v[0:1], s[0:1], 2, v[0:1]
	v_mov_b32_e32 v197, v195
	v_lshl_add_u64 v[100:101], v[0:1], 0, v[196:197]
	v_add_co_u32_e32 v0, vcc, s27, v100
	v_readlane_b32 s49, v252, 5
	s_nop 0
	v_addc_co_u32_e32 v1, vcc, 0, v101, vcc
	v_add_co_u32_e32 v8, vcc, s28, v100
	global_load_dwordx4 v[4:7], v[0:1], off offset:-4096 nt
	s_nop 0
	global_load_dwordx4 v[0:3], v[0:1], off nt
	v_addc_co_u32_e32 v9, vcc, 0, v101, vcc
	v_add_co_u32_e32 v16, vcc, s29, v100
	global_load_dwordx4 v[12:15], v[8:9], off offset:-4096 nt
	s_nop 0
	global_load_dwordx4 v[8:11], v[8:9], off nt
	v_addc_co_u32_e32 v17, vcc, 0, v101, vcc
	v_add_co_u32_e32 v24, vcc, s30, v100
	global_load_dwordx4 v[20:23], v[16:17], off offset:-4096 nt
	s_nop 0
	global_load_dwordx4 v[16:19], v[16:17], off nt
	v_addc_co_u32_e32 v25, vcc, 0, v101, vcc
	v_add_co_u32_e32 v40, vcc, s31, v100
	global_load_dwordx4 v[28:31], v[24:25], off offset:-4096 nt
	s_nop 0
	global_load_dwordx4 v[24:27], v[24:25], off nt
	v_addc_co_u32_e32 v41, vcc, 0, v101, vcc
	v_add_co_u32_e32 v64, vcc, s35, v100
	global_load_dwordx4 v[44:47], v[40:41], off offset:-4096 nt
	s_nop 0
	global_load_dwordx4 v[40:43], v[40:41], off nt
	v_addc_co_u32_e32 v65, vcc, 0, v101, vcc
	v_add_co_u32_e32 v88, vcc, 0xc000, v100
	global_load_dwordx4 v[76:79], v[100:101], off nt
	s_nop 0
	global_load_dwordx4 v[64:67], v[64:65], off nt
	v_addc_co_u32_e32 v89, vcc, 0, v101, vcc
	v_add_co_u32_e32 v92, vcc, 0xd000, v100
	v_readlane_b32 s50, v252, 6
	s_nop 0
	v_addc_co_u32_e32 v93, vcc, 0, v101, vcc
	v_add_co_u32_e32 v102, vcc, 0xe000, v100
	global_load_dwordx4 v[88:91], v[88:89], off nt
	s_nop 0
	global_load_dwordx4 v[92:95], v[92:93], off nt
	v_addc_co_u32_e32 v103, vcc, 0, v101, vcc
	v_add_co_u32_e32 v108, vcc, 0xf000, v100
	v_readlane_b32 s51, v252, 7
	s_nop 0
	v_addc_co_u32_e32 v109, vcc, 0, v101, vcc
	global_load_dwordx4 v[100:103], v[102:103], off nt
	s_nop 0
	global_load_dwordx4 v[108:111], v[108:109], off nt
	v_readlane_b32 s52, v252, 8
	v_readlane_b32 s53, v252, 9
	v_readlane_b32 s54, v252, 10
	v_readlane_b32 s55, v252, 11
	v_readlane_b32 s56, v252, 12
	v_readlane_b32 s57, v252, 13
	v_readlane_b32 s58, v252, 14
	v_readlane_b32 s59, v252, 15
	v_readlane_b32 s60, v252, 16
	v_readlane_b32 s61, v252, 17
.LBB0_124:
	s_add_i32 s17, s26, s23
	s_cmpk_lt_i32 s17, 0x180
	s_cselect_b64 s[0:1], -1, 0
	s_cmpk_gt_i32 s17, 0x17f
	s_cbranch_scc1 .LBB0_126
	s_ashr_i32 s15, s17, 31
	s_lshr_b32 s15, s15, 25
	s_add_i32 s15, s17, s15
	s_and_b32 s44, s15, 0x80
	s_sub_i32 s44, s17, s44
	s_bfe_i32 s45, s44, 0x80000
	s_bfe_u32 s45, s45, 0x4000b
	s_add_i32 s45, s44, s45
	s_bfe_i32 s46, s45, 0x80000
	s_and_b32 s45, s45, 0xf0
	s_sext_i32_i16 s48, s46
	s_sub_i32 s44, s44, s45
	s_ashr_i32 s46, s15, 7
	s_sext_i32_i8 s44, s44
	s_ashr_i32 s47, s46, 31
	v_readlane_b32 s52, v252, 4
	s_lshl_b32 s44, s44, 6
	s_lshl_b64 s[46:47], s[46:47], 21
	v_readlane_b32 s66, v252, 18
	v_readlane_b32 s67, v252, 19
	s_add_u32 s46, s66, s46
	s_addc_u32 s47, s67, s47
	s_lshl_b32 s15, s48, 2
	s_andn2_b32 s15, s15, 63
	v_add_u32_e32 v32, s15, v193
	v_ashrrev_i32_e32 v33, 31, v32
	v_lshlrev_b64 v[32:33], 12, v[32:33]
	v_lshl_add_u64 v[32:33], s[46:47], 0, v[32:33]
	s_ashr_i32 s45, s44, 31
	v_lshl_add_u64 v[32:33], s[44:45], 2, v[32:33]
	v_mov_b32_e32 v197, v195
	v_lshl_add_u64 v[120:121], v[32:33], 0, v[196:197]
	v_add_co_u32_e32 v32, vcc, s27, v120
	v_readlane_b32 s53, v252, 5
	s_nop 0
	v_addc_co_u32_e32 v33, vcc, 0, v121, vcc
	v_add_co_u32_e32 v48, vcc, s28, v120
	global_load_dwordx4 v[36:39], v[32:33], off offset:-4096 nt
	s_nop 0
	global_load_dwordx4 v[32:35], v[32:33], off nt
	v_addc_co_u32_e32 v49, vcc, 0, v121, vcc
	v_add_co_u32_e32 v56, vcc, s29, v120
	global_load_dwordx4 v[52:55], v[48:49], off offset:-4096 nt
	s_nop 0
	global_load_dwordx4 v[48:51], v[48:49], off nt
	v_addc_co_u32_e32 v57, vcc, 0, v121, vcc
	v_add_co_u32_e32 v68, vcc, s30, v120
	global_load_dwordx4 v[60:63], v[56:57], off offset:-4096 nt
	s_nop 0
	global_load_dwordx4 v[56:59], v[56:57], off nt
	v_addc_co_u32_e32 v69, vcc, 0, v121, vcc
	v_add_co_u32_e32 v80, vcc, s31, v120
	global_load_dwordx4 v[72:75], v[68:69], off offset:-4096 nt
	s_nop 0
	global_load_dwordx4 v[68:71], v[68:69], off nt
	v_addc_co_u32_e32 v81, vcc, 0, v121, vcc
	v_add_co_u32_e32 v96, vcc, s35, v120
	global_load_dwordx4 v[84:87], v[80:81], off offset:-4096 nt
	s_nop 0
	global_load_dwordx4 v[80:83], v[80:81], off nt
	v_addc_co_u32_e32 v97, vcc, 0, v121, vcc
	v_add_co_u32_e32 v112, vcc, 0xc000, v120
	global_load_dwordx4 v[104:107], v[120:121], off nt
	s_nop 0
	global_load_dwordx4 v[96:99], v[96:97], off nt
	v_addc_co_u32_e32 v113, vcc, 0, v121, vcc
	v_add_co_u32_e32 v116, vcc, 0xd000, v120
	v_readlane_b32 s54, v252, 6
	s_nop 0
	v_addc_co_u32_e32 v117, vcc, 0, v121, vcc
	v_add_co_u32_e32 v122, vcc, 0xe000, v120
	global_load_dwordx4 v[112:115], v[112:113], off nt
	s_nop 0
	global_load_dwordx4 v[116:119], v[116:117], off nt
	v_addc_co_u32_e32 v123, vcc, 0, v121, vcc
	v_add_co_u32_e32 v124, vcc, 0xf000, v120
	v_readlane_b32 s55, v252, 7
	s_nop 0
	v_addc_co_u32_e32 v125, vcc, 0, v121, vcc
	global_load_dwordx4 v[120:123], v[122:123], off nt
	s_nop 0
	global_load_dwordx4 v[124:127], v[124:125], off nt
	v_readlane_b32 s56, v252, 8
	v_readlane_b32 s57, v252, 9
	v_readlane_b32 s58, v252, 10
	v_readlane_b32 s59, v252, 11
	v_readlane_b32 s60, v252, 12
	v_readlane_b32 s61, v252, 13
	v_readlane_b32 s62, v252, 14
	v_readlane_b32 s63, v252, 15
	v_readlane_b32 s64, v252, 16
	v_readlane_b32 s65, v252, 17
.LBB0_126:
	s_waitcnt vmcnt(3)
	v_cvt_pk_bf16_f32 v218, v188, v132
	v_cvt_pk_bf16_f32 v219, v128, v144
	v_cvt_pk_bf16_f32 v220, v136, v152
	v_cvt_pk_bf16_f32 v221, v148, v160
	ds_write_b128 v202, v[218:221]
	v_cvt_pk_bf16_f32 v218, v140, v164
	v_cvt_pk_bf16_f32 v219, v156, v172
	s_waitcnt vmcnt(2)
	v_cvt_pk_bf16_f32 v220, v168, v176
	s_waitcnt vmcnt(0)
	v_cvt_pk_bf16_f32 v221, v180, v184
	ds_write_b128 v203, v[218:221]
	v_cvt_pk_bf16_f32 v218, v189, v133
	v_cvt_pk_bf16_f32 v219, v129, v145
	v_cvt_pk_bf16_f32 v220, v137, v153
	v_cvt_pk_bf16_f32 v221, v149, v161
	ds_write_b128 v202, v[218:221] offset:128
	v_cvt_pk_bf16_f32 v218, v141, v165
	v_cvt_pk_bf16_f32 v219, v157, v173
	v_cvt_pk_bf16_f32 v220, v169, v177
	v_cvt_pk_bf16_f32 v221, v181, v185
	ds_write_b128 v203, v[218:221] offset:128
	v_cvt_pk_bf16_f32 v218, v190, v134
	v_cvt_pk_bf16_f32 v219, v130, v146
	v_cvt_pk_bf16_f32 v220, v138, v154
	v_cvt_pk_bf16_f32 v221, v150, v162
	s_lshl_b64 s[4:5], s[4:5], 10
	ds_write_b128 v202, v[218:221] offset:256
	v_cvt_pk_bf16_f32 v218, v142, v166
	v_cvt_pk_bf16_f32 v219, v158, v174
	v_cvt_pk_bf16_f32 v220, v170, v178
	v_cvt_pk_bf16_f32 v221, v182, v186
	ds_write_b128 v203, v[218:221] offset:256
	v_cvt_pk_bf16_f32 v128, v191, v135
	v_cvt_pk_bf16_f32 v129, v131, v147
	v_cvt_pk_bf16_f32 v130, v139, v155
	s_add_u32 s4, s24, s4
	v_cvt_pk_bf16_f32 v131, v151, v163
	ds_write_b128 v202, v[128:131] offset:384
	v_cvt_pk_bf16_f32 v128, v143, v167
	v_cvt_pk_bf16_f32 v129, v159, v175
	v_cvt_pk_bf16_f32 v130, v171, v179
	s_addc_u32 s5, s25, s5
	v_cvt_pk_bf16_f32 v131, v183, v187
	ds_write_b128 v203, v[128:131] offset:384
	v_add_u32_e32 v130, s16, v201
	v_mov_b64_e32 v[128:129], s[4:5]
	v_mad_i64_i32 v[134:135], s[4:5], v130, s40, v[128:129]
	v_add_u32_e32 v128, v204, v205
	ds_read_b128 v[130:133], v128
	s_ashr_i32 s15, s14, 31
	v_add_u32_e32 v129, v206, v207
	v_lshl_add_u64 v[134:135], s[14:15], 1, v[134:135]
	ds_read_b128 v[138:141], v129
	v_lshl_add_u64 v[146:147], v[134:135], 0, v[194:195]
	ds_read_b128 v[134:137], v128 offset:4096
	s_waitcnt lgkmcnt(2)
	global_store_dwordx4 v[146:147], v[130:133], off nt
	s_mov_b32 s4, 0x1e000
	s_nop 0
	v_add_u32_e32 v130, v208, v209
	v_add_co_u32_e32 v132, vcc, s29, v146
	ds_read_b128 v[142:145], v130
	s_nop 0
	v_addc_co_u32_e32 v133, vcc, 0, v147, vcc
	v_add_u32_e32 v131, v210, v211
	s_waitcnt lgkmcnt(2)
	global_store_dwordx4 v[132:133], v[138:141], off nt
	ds_read_b128 v[138:141], v131
	v_add_co_u32_e32 v132, vcc, s39, v146
	s_nop 1
	v_addc_co_u32_e32 v133, vcc, 0, v147, vcc
	s_waitcnt lgkmcnt(1)
	global_store_dwordx4 v[132:133], v[142:145], off nt
	v_add_co_u32_e32 v148, vcc, s41, v146
	v_add_u32_e32 v132, v212, v213
	s_nop 0
	v_addc_co_u32_e32 v149, vcc, 0, v147, vcc
	ds_read_b128 v[142:145], v132
	s_waitcnt lgkmcnt(1)
	global_store_dwordx4 v[148:149], v[138:141], off nt
	v_add_u32_e32 v133, v214, v215
	s_nop 0
	v_add_co_u32_e32 v138, vcc, s42, v146
	s_nop 1
	v_addc_co_u32_e32 v139, vcc, 0, v147, vcc
	global_store_dwordx4 v[138:139], v[134:137], off nt
	ds_read_b128 v[136:139], v133
	s_nop 0
	v_add_co_u32_e32 v134, vcc, s4, v146
	s_nop 1
	v_addc_co_u32_e32 v135, vcc, 0, v147, vcc
	s_waitcnt lgkmcnt(1)
	global_store_dwordx4 v[134:135], v[142:145], off nt
	v_add_u32_e32 v134, v216, v217
	ds_read_b128 v[140:143], v134
	v_add_co_u32_e32 v144, vcc, 0x24000, v146
	s_nop 1
	v_addc_co_u32_e32 v145, vcc, 0, v147, vcc
	s_waitcnt lgkmcnt(1)
	global_store_dwordx4 v[144:145], v[136:139], off nt
	s_nop 1
	v_add_co_u32_e32 v136, vcc, 0x2a000, v146
	s_nop 1
	v_addc_co_u32_e32 v137, vcc, 0, v147, vcc
	s_andn2_b64 vcc, exec, s[2:3]
	s_waitcnt lgkmcnt(0)
	global_store_dwordx4 v[136:137], v[140:143], off nt
	s_cbranch_vccz .LBB0_128
	s_andn2_b64 vcc, exec, s[0:1]
	s_cbranch_vccnz .LBB0_121
	s_branch .LBB0_129
.LBB0_128:
	s_ashr_i32 s2, s43, 31
	s_lshr_b32 s2, s2, 25
	s_add_i32 s3, s43, s2
	s_ashr_i32 s2, s3, 7
	s_and_b32 s3, s3, 0xff80
	s_sub_i32 s3, s43, s3
	s_bfe_i32 s4, s3, 0x80000
	s_bfe_u32 s4, s4, 0x4000b
	v_cvt_pk_bf16_f32 v136, v76, v4
	v_cvt_pk_bf16_f32 v137, v0, v12
	s_add_i32 s4, s3, s4
	v_cvt_pk_bf16_f32 v138, v8, v20
	v_cvt_pk_bf16_f32 v139, v16, v28
	ds_write_b128 v202, v[136:139]
	v_cvt_pk_bf16_f32 v136, v24, v44
	v_cvt_pk_bf16_f32 v137, v40, v64
	s_bfe_i32 s5, s4, 0x80000
	v_cvt_pk_bf16_f32 v138, v88, v92
	v_cvt_pk_bf16_f32 v139, v100, v108
	ds_write_b128 v203, v[136:139]
	v_cvt_pk_bf16_f32 v136, v77, v5
	v_cvt_pk_bf16_f32 v137, v1, v13
	s_and_b32 s4, s4, 0xf0
	v_cvt_pk_bf16_f32 v138, v9, v21
	v_cvt_pk_bf16_f32 v139, v17, v29
	ds_write_b128 v202, v[136:139] offset:128
	v_cvt_pk_bf16_f32 v136, v25, v45
	v_cvt_pk_bf16_f32 v137, v41, v65
	s_sub_i32 s3, s3, s4
	v_cvt_pk_bf16_f32 v138, v89, v93
	v_cvt_pk_bf16_f32 v139, v101, v109
	ds_write_b128 v203, v[136:139] offset:128
	v_cvt_pk_bf16_f32 v136, v78, v6
	v_cvt_pk_bf16_f32 v137, v2, v14
	s_sext_i32_i8 s4, s3
	s_ashr_i32 s3, s2, 31
	v_cvt_pk_bf16_f32 v138, v10, v22
	v_cvt_pk_bf16_f32 v139, v18, v30
	ds_write_b128 v202, v[136:139] offset:256
	v_cvt_pk_bf16_f32 v136, v26, v46
	v_cvt_pk_bf16_f32 v137, v42, v66
	s_lshl_b64 s[2:3], s[2:3], 10
	v_cvt_pk_bf16_f32 v138, v90, v94
	v_cvt_pk_bf16_f32 v139, v102, v110
	ds_write_b128 v203, v[136:139] offset:256
	v_cvt_pk_bf16_f32 v136, v79, v7
	v_cvt_pk_bf16_f32 v137, v3, v15
	s_add_u32 s2, s24, s2
	v_cvt_pk_bf16_f32 v138, v11, v23
	v_cvt_pk_bf16_f32 v139, v19, v31
	ds_write_b128 v202, v[136:139] offset:384
	v_cvt_pk_bf16_f32 v136, v27, v47
	v_cvt_pk_bf16_f32 v137, v43, v67
	s_addc_u32 s3, s25, s3
	v_cvt_pk_bf16_f32 v138, v91, v95
	v_cvt_pk_bf16_f32 v139, v103, v111
	ds_write_b128 v203, v[136:139] offset:384
	v_lshl_add_u32 v135, s4, 6, v201
	v_mov_b64_e32 v[136:137], s[2:3]
	s_sext_i32_i16 s5, s5
	v_mad_i64_i32 v[136:137], s[2:3], v135, s40, v[136:137]
	s_lshl_b32 s2, s5, 2
	s_andn2_b32 s2, s2, 63
	s_ashr_i32 s3, s2, 31
	v_lshl_add_u64 v[136:137], s[2:3], 1, v[136:137]
	v_lshl_add_u64 v[140:141], v[136:137], 0, v[194:195]
	ds_read_b128 v[136:139], v128
	v_add_co_u32_e32 v142, vcc, s29, v140
	s_waitcnt lgkmcnt(0)
	global_store_dwordx4 v[140:141], v[136:139], off nt
	ds_read_b128 v[136:139], v129
	v_addc_co_u32_e32 v143, vcc, 0, v141, vcc
	s_waitcnt lgkmcnt(0)
	global_store_dwordx4 v[142:143], v[136:139], off nt
	ds_read_b128 v[136:139], v130
	v_add_co_u32_e32 v142, vcc, s39, v140
	s_nop 1
	v_addc_co_u32_e32 v143, vcc, 0, v141, vcc
	s_waitcnt lgkmcnt(0)
	global_store_dwordx4 v[142:143], v[136:139], off nt
	ds_read_b128 v[136:139], v131
	v_add_co_u32_e32 v142, vcc, s41, v140
	s_nop 1
	v_addc_co_u32_e32 v143, vcc, 0, v141, vcc
	s_waitcnt lgkmcnt(0)
	global_store_dwordx4 v[142:143], v[136:139], off nt
	ds_read_b128 v[136:139], v128 offset:4096
	v_add_co_u32_e32 v142, vcc, s42, v140
	s_nop 1
	v_addc_co_u32_e32 v143, vcc, 0, v141, vcc
	s_waitcnt lgkmcnt(0)
	global_store_dwordx4 v[142:143], v[136:139], off nt
	ds_read_b128 v[136:139], v132
	v_add_co_u32_e32 v142, vcc, 0x1e000, v140
	s_nop 1
	v_addc_co_u32_e32 v143, vcc, 0, v141, vcc
	s_waitcnt lgkmcnt(0)
	global_store_dwordx4 v[142:143], v[136:139], off nt
	ds_read_b128 v[136:139], v133
	v_add_co_u32_e32 v142, vcc, 0x24000, v140
	s_nop 1
	v_addc_co_u32_e32 v143, vcc, 0, v141, vcc
	s_waitcnt lgkmcnt(0)
	global_store_dwordx4 v[142:143], v[136:139], off nt
	ds_read_b128 v[136:139], v134
	v_add_co_u32_e32 v140, vcc, 0x2a000, v140
	s_nop 1
	v_addc_co_u32_e32 v141, vcc, 0, v141, vcc
	s_waitcnt lgkmcnt(0)
	global_store_dwordx4 v[140:141], v[136:139], off nt
	s_andn2_b64 vcc, exec, s[0:1]
	s_cbranch_vccnz .LBB0_121
.LBB0_129:
	s_ashr_i32 s0, s17, 31
	s_lshr_b32 s0, s0, 25
	s_add_i32 s1, s17, s0
	s_ashr_i32 s0, s1, 7
	s_and_b32 s1, s1, 0xff80
	s_sub_i32 s1, s17, s1
	s_bfe_i32 s2, s1, 0x80000
	s_bfe_u32 s2, s2, 0x4000b
	v_cvt_pk_bf16_f32 v136, v104, v36
	v_cvt_pk_bf16_f32 v137, v32, v52
	s_add_i32 s2, s1, s2
	v_cvt_pk_bf16_f32 v138, v48, v60
	v_cvt_pk_bf16_f32 v139, v56, v72
	ds_write_b128 v202, v[136:139]
	v_cvt_pk_bf16_f32 v136, v68, v84
	v_cvt_pk_bf16_f32 v137, v80, v96
	s_bfe_i32 s3, s2, 0x80000
	v_cvt_pk_bf16_f32 v138, v112, v116
	v_cvt_pk_bf16_f32 v139, v120, v124
	ds_write_b128 v203, v[136:139]
	v_cvt_pk_bf16_f32 v136, v105, v37
	v_cvt_pk_bf16_f32 v137, v33, v53
	s_and_b32 s2, s2, 0xf0
	v_cvt_pk_bf16_f32 v138, v49, v61
	v_cvt_pk_bf16_f32 v139, v57, v73
	ds_write_b128 v202, v[136:139] offset:128
	v_cvt_pk_bf16_f32 v136, v69, v85
	v_cvt_pk_bf16_f32 v137, v81, v97
	s_sub_i32 s1, s1, s2
	v_cvt_pk_bf16_f32 v138, v113, v117
	v_cvt_pk_bf16_f32 v139, v121, v125
	ds_write_b128 v203, v[136:139] offset:128
	v_cvt_pk_bf16_f32 v136, v106, v38
	v_cvt_pk_bf16_f32 v137, v34, v54
	s_sext_i32_i8 s2, s1
	s_ashr_i32 s1, s0, 31
	v_cvt_pk_bf16_f32 v138, v50, v62
	v_cvt_pk_bf16_f32 v139, v58, v74
	ds_write_b128 v202, v[136:139] offset:256
	v_cvt_pk_bf16_f32 v136, v70, v86
	v_cvt_pk_bf16_f32 v137, v82, v98
	s_lshl_b64 s[0:1], s[0:1], 10
	v_cvt_pk_bf16_f32 v138, v114, v118
	v_cvt_pk_bf16_f32 v139, v122, v126
	ds_write_b128 v203, v[136:139] offset:256
	v_cvt_pk_bf16_f32 v136, v107, v39
	v_cvt_pk_bf16_f32 v137, v35, v55
	s_add_u32 s0, s24, s0
	v_cvt_pk_bf16_f32 v138, v51, v63
	v_cvt_pk_bf16_f32 v139, v59, v75
	ds_write_b128 v202, v[136:139] offset:384
	v_cvt_pk_bf16_f32 v136, v71, v87
	v_cvt_pk_bf16_f32 v137, v83, v99
	s_addc_u32 s1, s25, s1
	v_cvt_pk_bf16_f32 v138, v115, v119
	v_cvt_pk_bf16_f32 v139, v123, v127
	ds_write_b128 v203, v[136:139] offset:384
	v_lshl_add_u32 v135, s2, 6, v201
	v_mov_b64_e32 v[136:137], s[0:1]
	s_sext_i32_i16 s3, s3
	v_mad_i64_i32 v[140:141], s[0:1], v135, s40, v[136:137]
	s_lshl_b32 s0, s3, 2
	ds_read_b128 v[136:139], v128
	s_andn2_b32 s0, s0, 63
	s_ashr_i32 s1, s0, 31
	v_lshl_add_u64 v[140:141], s[0:1], 1, v[140:141]
	v_lshl_add_u64 v[148:149], v[140:141], 0, v[194:195]
	ds_read_b128 v[140:143], v128 offset:4096
	s_waitcnt lgkmcnt(1)
	global_store_dwordx4 v[148:149], v[136:139], off nt
	ds_read_b128 v[136:139], v129
	ds_read_b128 v[144:147], v130
	v_add_co_u32_e32 v128, vcc, s29, v148
	s_nop 1
	v_addc_co_u32_e32 v129, vcc, 0, v149, vcc
	s_waitcnt lgkmcnt(1)
	global_store_dwordx4 v[128:129], v[136:139], off nt
	v_add_co_u32_e32 v128, vcc, s39, v148
	ds_read_b128 v[136:139], v132
	s_nop 0
	v_addc_co_u32_e32 v129, vcc, 0, v149, vcc
	s_waitcnt lgkmcnt(1)
	global_store_dwordx4 v[128:129], v[144:147], off nt
	ds_read_b128 v[128:131], v131
	s_nop 0
	v_add_co_u32_e32 v144, vcc, s41, v148
	s_nop 1
	v_addc_co_u32_e32 v145, vcc, 0, v149, vcc
	s_waitcnt lgkmcnt(0)
	global_store_dwordx4 v[144:145], v[128:131], off nt
	s_nop 1
	v_add_co_u32_e32 v128, vcc, s42, v148
	s_nop 1
	v_addc_co_u32_e32 v129, vcc, 0, v149, vcc
	global_store_dwordx4 v[128:129], v[140:143], off nt
	v_add_co_u32_e32 v128, vcc, 0x1e000, v148
	s_nop 1
	v_addc_co_u32_e32 v129, vcc, 0, v149, vcc
	global_store_dwordx4 v[128:129], v[136:139], off nt
	ds_read_b128 v[128:131], v133
	ds_read_b128 v[132:135], v134
	v_add_co_u32_e32 v136, vcc, 0x24000, v148
	s_nop 1
	v_addc_co_u32_e32 v137, vcc, 0, v149, vcc
	s_waitcnt lgkmcnt(1)
	global_store_dwordx4 v[136:137], v[128:131], off nt
	s_nop 1
	v_add_co_u32_e32 v128, vcc, 0x2a000, v148
	s_nop 1
	v_addc_co_u32_e32 v129, vcc, 0, v149, vcc
	s_waitcnt lgkmcnt(0)
	global_store_dwordx4 v[128:129], v[132:135], off nt
	s_branch .LBB0_121

.LBB0_133:
	s_add_i32 s39, s8, s23
	s_cmpk_lt_i32 s39, 0x100
	s_cselect_b64 s[4:5], -1, 0
	s_ashr_i32 s2, s23, 31
	s_lshr_b32 s2, s2, 24
	s_add_i32 s2, s23, s2
	s_and_b32 s2, s2, 0xff00
	s_sub_i32 s2, s23, s2
	s_sext_i32_i16 s3, s2
	s_bfe_u32 s3, s3, 0x4001b
	s_add_i32 s3, s2, s3
	s_sext_i32_i16 s14, s3
	s_and_b32 s3, s3, 0xfff0
	s_sub_i32 s2, s2, s3
	s_sext_i32_i16 s2, s2
	s_lshl_b32 s16, s2, 6
	s_lshl_b32 s2, s14, 2
	s_and_b32 s14, s2, 0xffffffc0
	v_add_u32_e32 v128, s14, v193
	v_ashrrev_i32_e32 v129, 31, v128
	v_readlane_b32 s40, v252, 20
	v_lshlrev_b64 v[128:129], 12, v[128:129]
	v_readlane_b32 s41, v252, 21
	s_ashr_i32 s17, s16, 31
	s_cmpk_gt_i32 s39, 0xff
	v_lshl_add_u64 v[128:129], s[40:41], 0, v[128:129]
	v_lshl_add_u64 v[128:129], s[16:17], 2, v[128:129]
	v_lshl_add_u64 v[180:181], v[128:129], 0, v[198:199]
	v_add_co_u32_e32 v128, vcc, s25, v180
	v_readlane_b32 s42, v252, 22
	s_nop 0
	v_addc_co_u32_e32 v129, vcc, 0, v181, vcc
	v_add_co_u32_e32 v136, vcc, s26, v180
	global_load_dwordx4 v[132:135], v[128:129], off offset:-4096 nt
	s_nop 0
	global_load_dwordx4 v[128:131], v[128:129], off nt
	v_addc_co_u32_e32 v137, vcc, 0, v181, vcc
	v_add_co_u32_e32 v140, vcc, s27, v180
	global_load_dwordx4 v[144:147], v[136:137], off offset:-4096 nt
	s_nop 0
	global_load_dwordx4 v[136:139], v[136:137], off nt
	v_addc_co_u32_e32 v141, vcc, 0, v181, vcc
	global_load_dwordx4 v[152:155], v[140:141], off offset:-4096 nt
	global_load_dwordx4 v[148:151], v[140:141], off nt
	v_add_co_u32_e32 v140, vcc, s28, v180
	v_readlane_b32 s43, v252, 23
	s_nop 0
	v_addc_co_u32_e32 v141, vcc, 0, v181, vcc
	v_add_co_u32_e32 v156, vcc, s29, v180
	global_load_dwordx4 v[164:167], v[140:141], off offset:-4096 nt
	s_nop 0
	global_load_dwordx4 v[140:143], v[140:141], off nt
	v_addc_co_u32_e32 v157, vcc, 0, v181, vcc
	v_add_co_u32_e32 v168, vcc, s31, v180
	global_load_dwordx4 v[160:163], v[156:157], off offset:-4096 nt
	s_nop 0
	global_load_dwordx4 v[156:159], v[156:157], off nt
	v_addc_co_u32_e32 v169, vcc, 0, v181, vcc
	v_add_co_u32_e32 v176, vcc, 0xd000, v180
	global_load_dwordx4 v[172:175], v[168:169], off offset:-4096 nt
	s_nop 0
	global_load_dwordx4 v[168:171], v[168:169], off nt
	v_addc_co_u32_e32 v177, vcc, 0, v181, vcc
	v_add_co_u32_e32 v182, vcc, 0xe000, v180
	global_load_dwordx4 v[188:191], v[180:181], off nt
	s_nop 0
	global_load_dwordx4 v[176:179], v[176:177], off nt
	v_addc_co_u32_e32 v183, vcc, 0, v181, vcc
	v_add_co_u32_e32 v184, vcc, 0xf000, v180
	v_readlane_b32 s44, v252, 24
	s_nop 0
	v_addc_co_u32_e32 v185, vcc, 0, v181, vcc
	global_load_dwordx4 v[180:183], v[182:183], off nt
	s_nop 0
	global_load_dwordx4 v[184:187], v[184:185], off nt
	v_readlane_b32 s45, v252, 25
	v_readlane_b32 s46, v252, 26
	v_readlane_b32 s47, v252, 27
	v_readlane_b32 s48, v252, 28
	v_readlane_b32 s49, v252, 29
	v_readlane_b32 s50, v252, 30
	v_readlane_b32 s51, v252, 31
	v_readlane_b32 s52, v252, 32
	v_readlane_b32 s53, v252, 33
	v_readlane_b32 s54, v252, 34
	v_readlane_b32 s55, v252, 35
	s_cbranch_scc1 .LBB0_135
	s_ashr_i32 s2, s39, 31
	s_lshr_b32 s2, s2, 24
	s_add_i32 s2, s39, s2
	s_and_b32 s2, s2, 0xff00
	s_sub_i32 s2, s39, s2
	s_sext_i32_i16 s3, s2
	s_bfe_u32 s3, s3, 0x4001b
	s_add_i32 s3, s2, s3
	s_sext_i32_i16 s15, s3
	s_and_b32 s3, s3, 0xfff0
	s_sub_i32 s2, s2, s3
	s_lshl_b32 s3, s15, 2
	s_andn2_b32 s3, s3, 63
	v_add_u32_e32 v0, s3, v193
	s_sext_i32_i16 s2, s2
	v_ashrrev_i32_e32 v1, 31, v0
	v_readlane_b32 s40, v252, 20
	s_lshl_b32 s2, s2, 6
	v_lshlrev_b64 v[0:1], 12, v[0:1]
	v_readlane_b32 s41, v252, 21
	s_ashr_i32 s3, s2, 31
	v_mov_b32_e32 v197, v195
	v_lshl_add_u64 v[0:1], s[40:41], 0, v[0:1]
	v_lshl_add_u64 v[0:1], s[2:3], 2, v[0:1]
	v_lshl_add_u64 v[100:101], v[0:1], 0, v[196:197]
	v_add_co_u32_e32 v0, vcc, s25, v100
	v_readlane_b32 s42, v252, 22
	s_nop 0
	v_addc_co_u32_e32 v1, vcc, 0, v101, vcc
	v_add_co_u32_e32 v8, vcc, s26, v100
	global_load_dwordx4 v[4:7], v[0:1], off offset:-4096 nt
	s_nop 0
	global_load_dwordx4 v[0:3], v[0:1], off nt
	v_addc_co_u32_e32 v9, vcc, 0, v101, vcc
	v_add_co_u32_e32 v16, vcc, s27, v100
	global_load_dwordx4 v[12:15], v[8:9], off offset:-4096 nt
	s_nop 0
	global_load_dwordx4 v[8:11], v[8:9], off nt
	v_addc_co_u32_e32 v17, vcc, 0, v101, vcc
	v_add_co_u32_e32 v24, vcc, s28, v100
	global_load_dwordx4 v[20:23], v[16:17], off offset:-4096 nt
	s_nop 0
	global_load_dwordx4 v[16:19], v[16:17], off nt
	v_addc_co_u32_e32 v25, vcc, 0, v101, vcc
	v_add_co_u32_e32 v40, vcc, s29, v100
	global_load_dwordx4 v[28:31], v[24:25], off offset:-4096 nt
	s_nop 0
	global_load_dwordx4 v[24:27], v[24:25], off nt
	v_addc_co_u32_e32 v41, vcc, 0, v101, vcc
	v_add_co_u32_e32 v56, vcc, s30, v100
	global_load_dwordx4 v[44:47], v[40:41], off offset:-4096 nt
	s_nop 0
	global_load_dwordx4 v[40:43], v[40:41], off nt
	v_addc_co_u32_e32 v57, vcc, 0, v101, vcc
	v_add_co_u32_e32 v80, vcc, 0xc000, v100
	global_load_dwordx4 v[76:79], v[100:101], off nt
	s_nop 0
	global_load_dwordx4 v[56:59], v[56:57], off nt
	v_addc_co_u32_e32 v81, vcc, 0, v101, vcc
	v_add_co_u32_e32 v84, vcc, 0xd000, v100
	v_readlane_b32 s43, v252, 23
	s_nop 0
	v_addc_co_u32_e32 v85, vcc, 0, v101, vcc
	v_add_co_u32_e32 v102, vcc, 0xe000, v100
	global_load_dwordx4 v[80:83], v[80:81], off nt
	s_nop 0
	global_load_dwordx4 v[84:87], v[84:85], off nt
	v_addc_co_u32_e32 v103, vcc, 0, v101, vcc
	v_add_co_u32_e32 v104, vcc, 0xf000, v100
	v_readlane_b32 s44, v252, 24
	s_nop 0
	v_addc_co_u32_e32 v105, vcc, 0, v101, vcc
	global_load_dwordx4 v[100:103], v[102:103], off nt
	s_nop 0
	global_load_dwordx4 v[104:107], v[104:105], off nt
	v_readlane_b32 s45, v252, 25
	v_readlane_b32 s46, v252, 26
	v_readlane_b32 s47, v252, 27
	v_readlane_b32 s48, v252, 28
	v_readlane_b32 s49, v252, 29
	v_readlane_b32 s50, v252, 30
	v_readlane_b32 s51, v252, 31
	v_readlane_b32 s52, v252, 32
	v_readlane_b32 s53, v252, 33
	v_readlane_b32 s54, v252, 34
	v_readlane_b32 s55, v252, 35
.LBB0_135:
	s_add_i32 s17, s24, s23
	s_cmpk_lt_i32 s17, 0x100
	s_cselect_b64 s[2:3], -1, 0
	s_cmpk_gt_i32 s17, 0xff
	s_cbranch_scc1 .LBB0_137
	s_ashr_i32 s15, s17, 31
	s_lshr_b32 s15, s15, 24
	s_add_i32 s15, s17, s15
	s_and_b32 s15, s15, 0xff00
	s_sub_i32 s15, s17, s15
	s_sext_i32_i16 s40, s15
	s_bfe_u32 s40, s40, 0x4001b
	s_add_i32 s40, s15, s40
	s_sext_i32_i16 s41, s40
	s_and_b32 s40, s40, 0xfff0
	s_sub_i32 s15, s15, s40
	s_sext_i32_i16 s15, s15
	s_lshl_b32 s40, s15, 6
	s_lshl_b32 s15, s41, 2
	s_andn2_b32 s15, s15, 63
	v_add_u32_e32 v32, s15, v193
	v_ashrrev_i32_e32 v33, 31, v32
	v_readlane_b32 s44, v252, 20
	v_lshlrev_b64 v[32:33], 12, v[32:33]
	v_readlane_b32 s45, v252, 21
	s_ashr_i32 s41, s40, 31
	v_mov_b32_e32 v197, v195
	v_lshl_add_u64 v[32:33], s[44:45], 0, v[32:33]
	v_lshl_add_u64 v[32:33], s[40:41], 2, v[32:33]
	v_lshl_add_u64 v[120:121], v[32:33], 0, v[196:197]
	v_add_co_u32_e32 v32, vcc, s25, v120
	v_readlane_b32 s46, v252, 22
	s_nop 0
	v_addc_co_u32_e32 v33, vcc, 0, v121, vcc
	v_add_co_u32_e32 v48, vcc, s26, v120
	global_load_dwordx4 v[36:39], v[32:33], off offset:-4096 nt
	s_nop 0
	global_load_dwordx4 v[32:35], v[32:33], off nt
	v_addc_co_u32_e32 v49, vcc, 0, v121, vcc
	v_add_co_u32_e32 v60, vcc, s27, v120
	global_load_dwordx4 v[52:55], v[48:49], off offset:-4096 nt
	s_nop 0
	global_load_dwordx4 v[48:51], v[48:49], off nt
	v_addc_co_u32_e32 v61, vcc, 0, v121, vcc
	v_add_co_u32_e32 v68, vcc, s28, v120
	global_load_dwordx4 v[64:67], v[60:61], off offset:-4096 nt
	s_nop 0
	global_load_dwordx4 v[60:63], v[60:61], off nt
	v_addc_co_u32_e32 v69, vcc, 0, v121, vcc
	v_add_co_u32_e32 v88, vcc, s29, v120
	global_load_dwordx4 v[72:75], v[68:69], off offset:-4096 nt
	s_nop 0
	global_load_dwordx4 v[68:71], v[68:69], off nt
	v_addc_co_u32_e32 v89, vcc, 0, v121, vcc
	v_add_co_u32_e32 v96, vcc, s30, v120
	global_load_dwordx4 v[92:95], v[88:89], off offset:-4096 nt
	s_nop 0
	global_load_dwordx4 v[88:91], v[88:89], off nt
	v_addc_co_u32_e32 v97, vcc, 0, v121, vcc
	v_add_co_u32_e32 v112, vcc, 0xc000, v120
	global_load_dwordx4 v[108:111], v[120:121], off nt
	s_nop 0
	global_load_dwordx4 v[96:99], v[96:97], off nt
	v_addc_co_u32_e32 v113, vcc, 0, v121, vcc
	v_add_co_u32_e32 v116, vcc, 0xd000, v120
	v_readlane_b32 s47, v252, 23
	s_nop 0
	v_addc_co_u32_e32 v117, vcc, 0, v121, vcc
	v_add_co_u32_e32 v122, vcc, 0xe000, v120
	global_load_dwordx4 v[112:115], v[112:113], off nt
	s_nop 0
	global_load_dwordx4 v[116:119], v[116:117], off nt
	v_addc_co_u32_e32 v123, vcc, 0, v121, vcc
	v_add_co_u32_e32 v124, vcc, 0xf000, v120
	v_readlane_b32 s48, v252, 24
	s_nop 0
	v_addc_co_u32_e32 v125, vcc, 0, v121, vcc
	global_load_dwordx4 v[120:123], v[122:123], off nt
	s_nop 0
	global_load_dwordx4 v[124:127], v[124:125], off nt
	v_readlane_b32 s49, v252, 25
	v_readlane_b32 s50, v252, 26
	v_readlane_b32 s51, v252, 27
	v_readlane_b32 s52, v252, 28
	v_readlane_b32 s53, v252, 29
	v_readlane_b32 s54, v252, 30
	v_readlane_b32 s55, v252, 31
	v_readlane_b32 s56, v252, 32
	v_readlane_b32 s57, v252, 33
	v_readlane_b32 s58, v252, 34
	v_readlane_b32 s59, v252, 35
.LBB0_137:
	s_waitcnt vmcnt(3)
	v_cvt_pk_bf16_f32 v218, v188, v132
	v_cvt_pk_bf16_f32 v219, v128, v144
	v_cvt_pk_bf16_f32 v220, v136, v152
	v_cvt_pk_bf16_f32 v221, v148, v164
	ds_write_b128 v202, v[218:221]
	v_cvt_pk_bf16_f32 v218, v140, v160
	v_cvt_pk_bf16_f32 v219, v156, v172
	s_waitcnt vmcnt(2)
	v_cvt_pk_bf16_f32 v220, v168, v176
	s_waitcnt vmcnt(0)
	v_cvt_pk_bf16_f32 v221, v180, v184
	ds_write_b128 v203, v[218:221]
	v_cvt_pk_bf16_f32 v218, v189, v133
	v_cvt_pk_bf16_f32 v219, v129, v145
	v_cvt_pk_bf16_f32 v220, v137, v153
	v_cvt_pk_bf16_f32 v221, v149, v165
	ds_write_b128 v202, v[218:221] offset:128
	v_cvt_pk_bf16_f32 v218, v141, v161
	v_cvt_pk_bf16_f32 v219, v157, v173
	v_cvt_pk_bf16_f32 v220, v169, v177
	v_cvt_pk_bf16_f32 v221, v181, v185
	ds_write_b128 v203, v[218:221] offset:128
	v_cvt_pk_bf16_f32 v218, v190, v134
	v_cvt_pk_bf16_f32 v219, v130, v146
	v_cvt_pk_bf16_f32 v220, v138, v154
	v_cvt_pk_bf16_f32 v221, v150, v166
	ds_write_b128 v202, v[218:221] offset:256
	v_cvt_pk_bf16_f32 v218, v142, v162
	v_cvt_pk_bf16_f32 v219, v158, v174
	v_cvt_pk_bf16_f32 v220, v170, v178
	v_cvt_pk_bf16_f32 v221, v182, v186
	ds_write_b128 v203, v[218:221] offset:256
	v_cvt_pk_bf16_f32 v128, v191, v135
	v_cvt_pk_bf16_f32 v129, v131, v147
	v_cvt_pk_bf16_f32 v130, v139, v155
	v_cvt_pk_bf16_f32 v131, v151, v167
	ds_write_b128 v202, v[128:131] offset:384
	v_cvt_pk_bf16_f32 v128, v143, v163
	v_cvt_pk_bf16_f32 v129, v159, v175
	v_cvt_pk_bf16_f32 v130, v171, v179
	v_cvt_pk_bf16_f32 v131, v183, v187
	ds_write_b128 v203, v[128:131] offset:384
	v_add_u32_e32 v128, s16, v201
	v_ashrrev_i32_e32 v129, 31, v128
	v_lshlrev_b64 v[128:129], 11, v[128:129]
	v_lshl_add_u64 v[134:135], s[0:1], 0, v[128:129]
	v_add_u32_e32 v128, v204, v205
	ds_read_b128 v[130:133], v128
	s_ashr_i32 s15, s14, 31
	v_add_u32_e32 v129, v206, v207
	v_lshl_add_u64 v[134:135], s[14:15], 1, v[134:135]
	ds_read_b128 v[138:141], v129
	v_lshl_add_u64 v[146:147], v[134:135], 0, v[194:195]
	ds_read_b128 v[134:137], v128 offset:4096
	s_waitcnt lgkmcnt(2)
	global_store_dwordx4 v[146:147], v[130:133], off nt
	s_mov_b32 s14, 0x14000
	s_nop 0
	v_add_u32_e32 v130, v208, v209
	v_add_co_u32_e32 v132, vcc, s26, v146
	ds_read_b128 v[142:145], v130
	s_nop 0
	v_addc_co_u32_e32 v133, vcc, 0, v147, vcc
	v_add_u32_e32 v131, v210, v211
	s_waitcnt lgkmcnt(2)
	global_store_dwordx4 v[132:133], v[138:141], off nt
	ds_read_b128 v[138:141], v131
	v_add_co_u32_e32 v132, vcc, s28, v146
	s_nop 1
	v_addc_co_u32_e32 v133, vcc, 0, v147, vcc
	s_waitcnt lgkmcnt(1)
	global_store_dwordx4 v[132:133], v[142:145], off nt
	v_add_co_u32_e32 v148, vcc, s31, v146
	v_add_u32_e32 v132, v212, v213
	s_nop 0
	v_addc_co_u32_e32 v149, vcc, 0, v147, vcc
	ds_read_b128 v[142:145], v132
	s_waitcnt lgkmcnt(1)
	global_store_dwordx4 v[148:149], v[138:141], off nt
	v_add_u32_e32 v133, v214, v215
	s_nop 0
	v_add_co_u32_e32 v138, vcc, s35, v146
	s_nop 1
	v_addc_co_u32_e32 v139, vcc, 0, v147, vcc
	global_store_dwordx4 v[138:139], v[134:137], off nt
	ds_read_b128 v[136:139], v133
	s_nop 0
	v_add_co_u32_e32 v134, vcc, s14, v146
	s_nop 1
	v_addc_co_u32_e32 v135, vcc, 0, v147, vcc
	s_waitcnt lgkmcnt(1)
	global_store_dwordx4 v[134:135], v[142:145], off nt
	v_add_u32_e32 v134, v216, v217
	ds_read_b128 v[140:143], v134
	v_add_co_u32_e32 v144, vcc, 0x18000, v146
	s_nop 1
	v_addc_co_u32_e32 v145, vcc, 0, v147, vcc
	s_waitcnt lgkmcnt(1)
	global_store_dwordx4 v[144:145], v[136:139], off nt
	s_nop 1
	v_add_co_u32_e32 v136, vcc, 0x1c000, v146
	s_nop 1
	v_addc_co_u32_e32 v137, vcc, 0, v147, vcc
	s_andn2_b64 vcc, exec, s[4:5]
	s_waitcnt lgkmcnt(0)
	global_store_dwordx4 v[136:137], v[140:143], off nt
	s_cbranch_vccz .LBB0_139
	s_andn2_b64 vcc, exec, s[2:3]
	s_cbranch_vccnz .LBB0_132
	s_branch .LBB0_140
.LBB0_139:
	s_ashr_i32 s4, s39, 31
	s_lshr_b32 s4, s4, 24
	s_add_i32 s4, s39, s4
	s_and_b32 s4, s4, 0xff00
	v_cvt_pk_bf16_f32 v136, v76, v4
	s_sub_i32 s4, s39, s4
	v_cvt_pk_bf16_f32 v137, v0, v12
	v_cvt_pk_bf16_f32 v138, v8, v20
	v_cvt_pk_bf16_f32 v139, v16, v28
	ds_write_b128 v202, v[136:139]
	v_cvt_pk_bf16_f32 v136, v24, v44
	s_sext_i32_i16 s5, s4
	v_cvt_pk_bf16_f32 v137, v40, v56
	v_cvt_pk_bf16_f32 v138, v80, v84
	v_cvt_pk_bf16_f32 v139, v100, v104
	ds_write_b128 v203, v[136:139]
	v_cvt_pk_bf16_f32 v136, v77, v5
	s_bfe_u32 s5, s5, 0x4001b
	v_cvt_pk_bf16_f32 v137, v1, v13
	v_cvt_pk_bf16_f32 v138, v9, v21
	v_cvt_pk_bf16_f32 v139, v17, v29
	ds_write_b128 v202, v[136:139] offset:128
	v_cvt_pk_bf16_f32 v136, v25, v45
	s_add_i32 s5, s4, s5
	v_cvt_pk_bf16_f32 v137, v41, v57
	v_cvt_pk_bf16_f32 v138, v81, v85
	v_cvt_pk_bf16_f32 v139, v101, v105
	ds_write_b128 v203, v[136:139] offset:128
	v_cvt_pk_bf16_f32 v136, v78, v6
	s_sext_i32_i16 s14, s5
	v_cvt_pk_bf16_f32 v137, v2, v14
	v_cvt_pk_bf16_f32 v138, v10, v22
	v_cvt_pk_bf16_f32 v139, v18, v30
	ds_write_b128 v202, v[136:139] offset:256
	v_cvt_pk_bf16_f32 v136, v26, v46
	s_and_b32 s5, s5, 0xfff0
	v_cvt_pk_bf16_f32 v137, v42, v58
	v_cvt_pk_bf16_f32 v138, v82, v86
	v_cvt_pk_bf16_f32 v139, v102, v106
	ds_write_b128 v203, v[136:139] offset:256
	v_cvt_pk_bf16_f32 v136, v79, v7
	s_sub_i32 s4, s4, s5
	v_cvt_pk_bf16_f32 v137, v3, v15
	v_cvt_pk_bf16_f32 v138, v11, v23
	v_cvt_pk_bf16_f32 v139, v19, v31
	ds_write_b128 v202, v[136:139] offset:384
	v_cvt_pk_bf16_f32 v136, v27, v47
	s_sext_i32_i16 s4, s4
	v_cvt_pk_bf16_f32 v137, v43, v59
	v_cvt_pk_bf16_f32 v138, v83, v87
	v_cvt_pk_bf16_f32 v139, v103, v107
	ds_write_b128 v203, v[136:139] offset:384
	v_lshl_add_u32 v136, s4, 6, v201
	v_ashrrev_i32_e32 v137, 31, v136
	v_lshlrev_b64 v[136:137], 11, v[136:137]
	v_lshl_add_u64 v[140:141], s[0:1], 0, v[136:137]
	s_lshl_b32 s4, s14, 2
	ds_read_b128 v[136:139], v128
	s_andn2_b32 s4, s4, 63
	s_ashr_i32 s5, s4, 31
	v_lshl_add_u64 v[140:141], s[4:5], 1, v[140:141]
	v_lshl_add_u64 v[148:149], v[140:141], 0, v[194:195]
	ds_read_b128 v[140:143], v128 offset:4096
	s_waitcnt lgkmcnt(1)
	global_store_dwordx4 v[148:149], v[136:139], off nt
	ds_read_b128 v[136:139], v129
	ds_read_b128 v[144:147], v130
	v_add_co_u32_e32 v150, vcc, s26, v148
	s_nop 1
	v_addc_co_u32_e32 v151, vcc, 0, v149, vcc
	s_waitcnt lgkmcnt(1)
	global_store_dwordx4 v[150:151], v[136:139], off nt
	s_nop 1
	v_add_co_u32_e32 v136, vcc, s28, v148
	s_nop 1
	v_addc_co_u32_e32 v137, vcc, 0, v149, vcc
	s_waitcnt lgkmcnt(0)
	global_store_dwordx4 v[136:137], v[144:147], off nt
	ds_read_b128 v[136:139], v131
	ds_read_b128 v[144:147], v132
	v_add_co_u32_e32 v150, vcc, s31, v148
	s_nop 1
	v_addc_co_u32_e32 v151, vcc, 0, v149, vcc
	s_waitcnt lgkmcnt(1)
	global_store_dwordx4 v[150:151], v[136:139], off nt
	s_nop 1
	v_add_co_u32_e32 v136, vcc, s35, v148
	s_nop 1
	v_addc_co_u32_e32 v137, vcc, 0, v149, vcc
	global_store_dwordx4 v[136:137], v[140:143], off nt
	v_add_co_u32_e32 v136, vcc, 0x14000, v148
	ds_read_b128 v[140:143], v134
	s_nop 0
	v_addc_co_u32_e32 v137, vcc, 0, v149, vcc
	s_waitcnt lgkmcnt(1)
	global_store_dwordx4 v[136:137], v[144:147], off nt
	ds_read_b128 v[136:139], v133
	s_nop 0
	v_add_co_u32_e32 v144, vcc, 0x18000, v148
	s_nop 1
	v_addc_co_u32_e32 v145, vcc, 0, v149, vcc
	s_waitcnt lgkmcnt(0)
	global_store_dwordx4 v[144:145], v[136:139], off nt
	s_nop 1
	v_add_co_u32_e32 v136, vcc, 0x1c000, v148
	s_nop 1
	v_addc_co_u32_e32 v137, vcc, 0, v149, vcc
	global_store_dwordx4 v[136:137], v[140:143], off nt
	s_andn2_b64 vcc, exec, s[2:3]
	s_cbranch_vccnz .LBB0_132
.LBB0_140:
	s_ashr_i32 s2, s17, 31
	s_lshr_b32 s2, s2, 24
	s_add_i32 s2, s17, s2
	s_and_b32 s2, s2, 0xff00
	v_cvt_pk_bf16_f32 v136, v108, v36
	s_sub_i32 s2, s17, s2
	v_cvt_pk_bf16_f32 v137, v32, v52
	v_cvt_pk_bf16_f32 v138, v48, v64
	v_cvt_pk_bf16_f32 v139, v60, v72
	ds_write_b128 v202, v[136:139]
	v_cvt_pk_bf16_f32 v136, v68, v92
	s_sext_i32_i16 s3, s2
	v_cvt_pk_bf16_f32 v137, v88, v96
	v_cvt_pk_bf16_f32 v138, v112, v116
	v_cvt_pk_bf16_f32 v139, v120, v124
	ds_write_b128 v203, v[136:139]
	v_cvt_pk_bf16_f32 v136, v109, v37
	s_bfe_u32 s3, s3, 0x4001b
	v_cvt_pk_bf16_f32 v137, v33, v53
	v_cvt_pk_bf16_f32 v138, v49, v65
	v_cvt_pk_bf16_f32 v139, v61, v73
	ds_write_b128 v202, v[136:139] offset:128
	v_cvt_pk_bf16_f32 v136, v69, v93
	s_add_i32 s3, s2, s3
	v_cvt_pk_bf16_f32 v137, v89, v97
	v_cvt_pk_bf16_f32 v138, v113, v117
	v_cvt_pk_bf16_f32 v139, v121, v125
	ds_write_b128 v203, v[136:139] offset:128
	v_cvt_pk_bf16_f32 v136, v110, v38
	s_sext_i32_i16 s4, s3
	v_cvt_pk_bf16_f32 v137, v34, v54
	v_cvt_pk_bf16_f32 v138, v50, v66
	v_cvt_pk_bf16_f32 v139, v62, v74
	ds_write_b128 v202, v[136:139] offset:256
	v_cvt_pk_bf16_f32 v136, v70, v94
	s_and_b32 s3, s3, 0xfff0
	v_cvt_pk_bf16_f32 v137, v90, v98
	v_cvt_pk_bf16_f32 v138, v114, v118
	v_cvt_pk_bf16_f32 v139, v122, v126
	ds_write_b128 v203, v[136:139] offset:256
	v_cvt_pk_bf16_f32 v136, v111, v39
	s_sub_i32 s2, s2, s3
	v_cvt_pk_bf16_f32 v137, v35, v55
	v_cvt_pk_bf16_f32 v138, v51, v67
	v_cvt_pk_bf16_f32 v139, v63, v75
	ds_write_b128 v202, v[136:139] offset:384
	v_cvt_pk_bf16_f32 v136, v71, v95
	s_sext_i32_i16 s2, s2
	v_cvt_pk_bf16_f32 v137, v91, v99
	v_cvt_pk_bf16_f32 v138, v115, v119
	v_cvt_pk_bf16_f32 v139, v123, v127
	ds_write_b128 v203, v[136:139] offset:384
	v_lshl_add_u32 v136, s2, 6, v201
	v_ashrrev_i32_e32 v137, 31, v136
	v_lshlrev_b64 v[136:137], 11, v[136:137]
	v_lshl_add_u64 v[140:141], s[0:1], 0, v[136:137]
	s_lshl_b32 s2, s4, 2
	ds_read_b128 v[136:139], v128
	s_andn2_b32 s2, s2, 63
	s_ashr_i32 s3, s2, 31
	v_lshl_add_u64 v[140:141], s[2:3], 1, v[140:141]
	v_lshl_add_u64 v[148:149], v[140:141], 0, v[194:195]
	ds_read_b128 v[140:143], v128 offset:4096
	s_waitcnt lgkmcnt(1)
	global_store_dwordx4 v[148:149], v[136:139], off nt
	ds_read_b128 v[136:139], v129
	ds_read_b128 v[144:147], v130
	v_add_co_u32_e32 v128, vcc, s26, v148
	s_nop 1
	v_addc_co_u32_e32 v129, vcc, 0, v149, vcc
	s_waitcnt lgkmcnt(1)
	global_store_dwordx4 v[128:129], v[136:139], off nt
	v_add_co_u32_e32 v128, vcc, s28, v148
	ds_read_b128 v[136:139], v132
	s_nop 0
	v_addc_co_u32_e32 v129, vcc, 0, v149, vcc
	s_waitcnt lgkmcnt(1)
	global_store_dwordx4 v[128:129], v[144:147], off nt
	ds_read_b128 v[128:131], v131
	s_nop 0
	v_add_co_u32_e32 v144, vcc, s31, v148
	s_nop 1
	v_addc_co_u32_e32 v145, vcc, 0, v149, vcc
	s_waitcnt lgkmcnt(0)
	global_store_dwordx4 v[144:145], v[128:131], off nt
	s_nop 1
	v_add_co_u32_e32 v128, vcc, s35, v148
	s_nop 1
	v_addc_co_u32_e32 v129, vcc, 0, v149, vcc
	global_store_dwordx4 v[128:129], v[140:143], off nt
	v_add_co_u32_e32 v128, vcc, 0x14000, v148
	s_nop 1
	v_addc_co_u32_e32 v129, vcc, 0, v149, vcc
	global_store_dwordx4 v[128:129], v[136:139], off nt
	ds_read_b128 v[128:131], v133
	ds_read_b128 v[132:135], v134
	v_add_co_u32_e32 v136, vcc, 0x18000, v148
	s_nop 1
	v_addc_co_u32_e32 v137, vcc, 0, v149, vcc
	s_waitcnt lgkmcnt(1)
	global_store_dwordx4 v[136:137], v[128:131], off nt
	s_nop 1
	v_add_co_u32_e32 v128, vcc, 0x1c000, v148
	s_nop 1
	v_addc_co_u32_e32 v129, vcc, 0, v149, vcc
	s_waitcnt lgkmcnt(0)
	global_store_dwordx4 v[128:129], v[132:135], off nt
	s_branch .LBB0_132

.LBB0_144:
	s_add_i32 s35, s8, s23
	s_cmpk_lt_i32 s35, 0x80
	s_cselect_b64 s[4:5], -1, 0
	s_ashr_i32 s2, s23, 31
	s_lshr_b32 s2, s2, 25
	s_add_i32 s2, s23, s2
	s_and_b32 s2, s2, 0xff80
	s_sub_i32 s2, s23, s2
	s_bfe_i32 s3, s2, 0x80000
	s_bfe_u32 s3, s3, 0x3000c
	s_add_i32 s3, s2, s3
	s_bfe_i32 s14, s3, 0x80000
	s_and_b32 s3, s3, 0xf8
	s_sub_i32 s2, s2, s3
	s_sext_i32_i16 s14, s14
	s_sext_i32_i8 s2, s2
	s_lshl_b32 s16, s2, 6
	s_lshl_b32 s2, s14, 3
	s_and_b32 s14, s2, 0xffffffc0
	v_add_u32_e32 v128, s14, v193
	v_ashrrev_i32_e32 v129, 31, v128
	v_readlane_b32 s40, v252, 20
	v_lshlrev_b64 v[128:129], 11, v[128:129]
	v_readlane_b32 s46, v252, 26
	v_readlane_b32 s47, v252, 27
	s_ashr_i32 s17, s16, 31
	s_movk_i32 s2, 0x5000
	v_lshl_add_u64 v[128:129], s[46:47], 0, v[128:129]
	v_lshl_add_u64 v[128:129], s[16:17], 2, v[128:129]
	v_lshl_add_u64 v[184:185], v[128:129], 0, v[198:199]
	v_add_co_u32_e32 v144, vcc, s25, v184
	global_load_dwordx4 v[128:131], v[184:185], off nt
	global_load_dwordx4 v[132:135], v[184:185], off offset:2048 nt
	v_addc_co_u32_e32 v145, vcc, 0, v185, vcc
	v_add_co_u32_e32 v146, vcc, s26, v184
	s_cmpk_gt_i32 s35, 0x7f
	s_nop 0
	v_addc_co_u32_e32 v147, vcc, 0, v185, vcc
	v_add_co_u32_e32 v148, vcc, s27, v184
	global_load_dwordx4 v[140:143], v[146:147], off offset:-4096 nt
	global_load_dwordx4 v[136:139], v[146:147], off nt
	v_addc_co_u32_e32 v149, vcc, 0, v185, vcc
	v_add_co_u32_e32 v150, vcc, s28, v184
	v_readlane_b32 s41, v252, 21
	s_nop 0
	v_addc_co_u32_e32 v151, vcc, 0, v185, vcc
	v_add_co_u32_e32 v164, vcc, s2, v184
	global_load_dwordx4 v[152:155], v[146:147], off offset:2048 nt
	global_load_dwordx4 v[156:159], v[150:151], off offset:-4096 nt
	global_load_dwordx4 v[180:183], v[144:145], off offset:2048 nt
	global_load_dwordx4 v[168:171], v[148:149], off offset:2048 nt
	s_nop 0
	global_load_dwordx4 v[144:147], v[150:151], off nt
	s_nop 0
	global_load_dwordx4 v[148:151], v[150:151], off offset:2048 nt
	v_addc_co_u32_e32 v165, vcc, 0, v185, vcc
	v_add_co_u32_e32 v176, vcc, 0x6000, v184
	global_load_dwordx4 v[160:163], v[164:165], off nt
	s_nop 0
	global_load_dwordx4 v[164:167], v[164:165], off offset:2048 nt
	v_addc_co_u32_e32 v177, vcc, 0, v185, vcc
	v_add_co_u32_e32 v188, vcc, 0x7000, v184
	global_load_dwordx4 v[172:175], v[176:177], off nt
	s_nop 0
	global_load_dwordx4 v[176:179], v[176:177], off offset:2048 nt
	v_addc_co_u32_e32 v189, vcc, 0, v185, vcc
	global_load_dwordx4 v[184:187], v[188:189], off nt
	s_nop 0
	global_load_dwordx4 v[188:191], v[188:189], off offset:2048 nt
	v_readlane_b32 s42, v252, 22
	v_readlane_b32 s43, v252, 23
	v_readlane_b32 s44, v252, 24
	v_readlane_b32 s45, v252, 25
	v_readlane_b32 s48, v252, 28
	v_readlane_b32 s49, v252, 29
	v_readlane_b32 s50, v252, 30
	v_readlane_b32 s51, v252, 31
	v_readlane_b32 s52, v252, 32
	v_readlane_b32 s53, v252, 33
	v_readlane_b32 s54, v252, 34
	v_readlane_b32 s55, v252, 35
	s_cbranch_scc1 .LBB0_146
	s_ashr_i32 s2, s35, 31
	s_lshr_b32 s2, s2, 25
	s_add_i32 s2, s35, s2
	s_and_b32 s2, s2, 0xff80
	s_sub_i32 s2, s35, s2
	s_bfe_i32 s3, s2, 0x80000
	s_bfe_u32 s3, s3, 0x3000c
	s_add_i32 s3, s2, s3
	s_bfe_i32 s15, s3, 0x80000
	s_sext_i32_i16 s15, s15
	s_and_b32 s3, s3, 0xf8
	s_sub_i32 s2, s2, s3
	s_lshl_b32 s3, s15, 3
	s_andn2_b32 s3, s3, 63
	v_add_u32_e32 v0, s3, v193
	s_sext_i32_i8 s2, s2
	v_ashrrev_i32_e32 v1, 31, v0
	v_readlane_b32 s40, v252, 20
	s_lshl_b32 s2, s2, 6
	v_lshlrev_b64 v[0:1], 11, v[0:1]
	v_readlane_b32 s46, v252, 26
	v_readlane_b32 s47, v252, 27
	s_ashr_i32 s3, s2, 31
	v_mov_b32_e32 v197, v195
	v_lshl_add_u64 v[0:1], s[46:47], 0, v[0:1]
	v_lshl_add_u64 v[0:1], s[2:3], 2, v[0:1]
	v_lshl_add_u64 v[72:73], v[0:1], 0, v[196:197]
	v_add_co_u32_e32 v32, vcc, s25, v72
	global_load_dwordx4 v[4:7], v[72:73], off nt
	global_load_dwordx4 v[0:3], v[72:73], off offset:2048 nt
	v_addc_co_u32_e32 v33, vcc, 0, v73, vcc
	v_add_co_u32_e32 v24, vcc, s26, v72
	v_readlane_b32 s41, v252, 21
	s_nop 0
	v_addc_co_u32_e32 v25, vcc, 0, v73, vcc
	v_add_co_u32_e32 v34, vcc, s27, v72
	global_load_dwordx4 v[12:15], v[24:25], off offset:-4096 nt
	global_load_dwordx4 v[8:11], v[24:25], off nt
	v_addc_co_u32_e32 v35, vcc, 0, v73, vcc
	v_add_co_u32_e32 v56, vcc, s28, v72
	v_readlane_b32 s42, v252, 22
	s_nop 0
	v_addc_co_u32_e32 v57, vcc, 0, v73, vcc
	global_load_dwordx4 v[24:27], v[24:25], off offset:2048 nt
	s_nop 0
	global_load_dwordx4 v[28:31], v[56:57], off offset:-4096 nt
	global_load_dwordx4 v[44:47], v[32:33], off offset:2048 nt
	global_load_dwordx4 v[40:43], v[34:35], off offset:2048 nt
	global_load_dwordx4 v[36:39], v[56:57], off nt
	s_nop 0
	global_load_dwordx4 v[32:35], v[56:57], off offset:2048 nt
	v_add_co_u32_e32 v56, vcc, 0x5000, v72
	v_readlane_b32 s43, v252, 23
	s_nop 0
	v_addc_co_u32_e32 v57, vcc, 0, v73, vcc
	v_add_co_u32_e32 v64, vcc, 0x6000, v72
	global_load_dwordx4 v[60:63], v[56:57], off nt
	s_nop 0
	global_load_dwordx4 v[56:59], v[56:57], off offset:2048 nt
	v_addc_co_u32_e32 v65, vcc, 0, v73, vcc
	v_add_co_u32_e32 v72, vcc, 0x7000, v72
	global_load_dwordx4 v[68:71], v[64:65], off nt
	s_nop 0
	global_load_dwordx4 v[64:67], v[64:65], off offset:2048 nt
	v_addc_co_u32_e32 v73, vcc, 0, v73, vcc
	global_load_dwordx4 v[76:79], v[72:73], off nt
	s_nop 0
	global_load_dwordx4 v[72:75], v[72:73], off offset:2048 nt
	v_readlane_b32 s44, v252, 24
	v_readlane_b32 s45, v252, 25
	v_readlane_b32 s48, v252, 28
	v_readlane_b32 s49, v252, 29
	v_readlane_b32 s50, v252, 30
	v_readlane_b32 s51, v252, 31
	v_readlane_b32 s52, v252, 32
	v_readlane_b32 s53, v252, 33
	v_readlane_b32 s54, v252, 34
	v_readlane_b32 s55, v252, 35
.LBB0_146:
	s_add_i32 s17, s24, s23
	s_cmpk_lt_i32 s17, 0x80
	s_cselect_b64 s[2:3], -1, 0
	s_cmpk_gt_i32 s17, 0x7f
	s_cbranch_scc1 .LBB0_148
	s_ashr_i32 s15, s17, 31
	s_lshr_b32 s15, s15, 25
	s_add_i32 s15, s17, s15
	s_and_b32 s15, s15, 0xff80
	s_sub_i32 s15, s17, s15
	s_bfe_i32 s39, s15, 0x80000
	s_bfe_u32 s39, s39, 0x3000c
	s_add_i32 s39, s15, s39
	s_bfe_i32 s40, s39, 0x80000
	s_and_b32 s39, s39, 0xf8
	s_sub_i32 s15, s15, s39
	s_sext_i32_i16 s41, s40
	s_sext_i32_i8 s15, s15
	s_lshl_b32 s40, s15, 6
	s_lshl_b32 s15, s41, 3
	s_andn2_b32 s15, s15, 63
	v_add_u32_e32 v16, s15, v193
	v_ashrrev_i32_e32 v17, 31, v16
	v_readlane_b32 s44, v252, 20
	v_lshlrev_b64 v[16:17], 11, v[16:17]
	v_readlane_b32 s50, v252, 26
	v_readlane_b32 s51, v252, 27
	s_ashr_i32 s41, s40, 31
	v_mov_b32_e32 v197, v195
	v_lshl_add_u64 v[16:17], s[50:51], 0, v[16:17]
	v_lshl_add_u64 v[16:17], s[40:41], 2, v[16:17]
	v_lshl_add_u64 v[120:121], v[16:17], 0, v[196:197]
	v_add_co_u32_e32 v88, vcc, s25, v120
	global_load_dwordx4 v[20:23], v[120:121], off nt
	global_load_dwordx4 v[16:19], v[120:121], off offset:2048 nt
	v_addc_co_u32_e32 v89, vcc, 0, v121, vcc
	v_add_co_u32_e32 v80, vcc, s26, v120
	v_readlane_b32 s45, v252, 21
	s_nop 0
	v_addc_co_u32_e32 v81, vcc, 0, v121, vcc
	v_add_co_u32_e32 v90, vcc, s27, v120
	global_load_dwordx4 v[52:55], v[80:81], off offset:-4096 nt
	global_load_dwordx4 v[48:51], v[80:81], off nt
	v_addc_co_u32_e32 v91, vcc, 0, v121, vcc
	v_add_co_u32_e32 v104, vcc, s28, v120
	v_readlane_b32 s46, v252, 22
	s_nop 0
	v_addc_co_u32_e32 v105, vcc, 0, v121, vcc
	global_load_dwordx4 v[80:83], v[80:81], off offset:2048 nt
	s_nop 0
	global_load_dwordx4 v[84:87], v[104:105], off offset:-4096 nt
	global_load_dwordx4 v[100:103], v[88:89], off offset:2048 nt
	global_load_dwordx4 v[96:99], v[90:91], off offset:2048 nt
	global_load_dwordx4 v[92:95], v[104:105], off nt
	s_nop 0
	global_load_dwordx4 v[88:91], v[104:105], off offset:2048 nt
	v_add_co_u32_e32 v104, vcc, 0x5000, v120
	v_readlane_b32 s47, v252, 23
	s_nop 0
	v_addc_co_u32_e32 v105, vcc, 0, v121, vcc
	v_add_co_u32_e32 v112, vcc, 0x6000, v120
	global_load_dwordx4 v[108:111], v[104:105], off nt
	s_nop 0
	global_load_dwordx4 v[104:107], v[104:105], off offset:2048 nt
	v_addc_co_u32_e32 v113, vcc, 0, v121, vcc
	v_add_co_u32_e32 v120, vcc, 0x7000, v120
	global_load_dwordx4 v[116:119], v[112:113], off nt
	s_nop 0
	global_load_dwordx4 v[112:115], v[112:113], off offset:2048 nt
	v_addc_co_u32_e32 v121, vcc, 0, v121, vcc
	global_load_dwordx4 v[124:127], v[120:121], off nt
	s_nop 0
	global_load_dwordx4 v[120:123], v[120:121], off offset:2048 nt
	v_readlane_b32 s48, v252, 24
	v_readlane_b32 s49, v252, 25
	v_readlane_b32 s52, v252, 28
	v_readlane_b32 s53, v252, 29
	v_readlane_b32 s54, v252, 30
	v_readlane_b32 s55, v252, 31
	v_readlane_b32 s56, v252, 32
	v_readlane_b32 s57, v252, 33
	v_readlane_b32 s58, v252, 34
	v_readlane_b32 s59, v252, 35
.LBB0_148:
	s_waitcnt vmcnt(14)
	v_cvt_pk_bf16_f32 v218, v128, v132
	s_waitcnt vmcnt(9)
	v_cvt_pk_bf16_f32 v219, v140, v180
	v_cvt_pk_bf16_f32 v220, v136, v152
	s_waitcnt vmcnt(8)
	v_cvt_pk_bf16_f32 v221, v156, v168
	ds_write_b128 v202, v[218:221]
	s_waitcnt vmcnt(6)
	v_cvt_pk_bf16_f32 v218, v144, v148
	s_waitcnt vmcnt(4)
	v_cvt_pk_bf16_f32 v219, v160, v164
	s_waitcnt vmcnt(2)
	v_cvt_pk_bf16_f32 v220, v172, v176
	s_waitcnt vmcnt(0)
	v_cvt_pk_bf16_f32 v221, v184, v188
	ds_write_b128 v203, v[218:221]
	v_cvt_pk_bf16_f32 v218, v129, v133
	v_cvt_pk_bf16_f32 v219, v141, v181
	v_cvt_pk_bf16_f32 v220, v137, v153
	v_cvt_pk_bf16_f32 v221, v157, v169
	ds_write_b128 v202, v[218:221] offset:128
	v_cvt_pk_bf16_f32 v218, v145, v149
	v_cvt_pk_bf16_f32 v219, v161, v165
	v_cvt_pk_bf16_f32 v220, v173, v177
	v_cvt_pk_bf16_f32 v221, v185, v189
	ds_write_b128 v203, v[218:221] offset:128
	v_cvt_pk_bf16_f32 v218, v130, v134
	v_cvt_pk_bf16_f32 v219, v142, v182
	v_cvt_pk_bf16_f32 v220, v138, v154
	v_cvt_pk_bf16_f32 v221, v158, v170
	ds_write_b128 v202, v[218:221] offset:256
	v_cvt_pk_bf16_f32 v218, v146, v150
	v_cvt_pk_bf16_f32 v219, v162, v166
	v_cvt_pk_bf16_f32 v220, v174, v178
	v_cvt_pk_bf16_f32 v221, v186, v190
	ds_write_b128 v203, v[218:221] offset:256
	v_cvt_pk_bf16_f32 v128, v131, v135
	v_cvt_pk_bf16_f32 v129, v143, v183
	v_cvt_pk_bf16_f32 v130, v139, v155
	v_cvt_pk_bf16_f32 v131, v159, v171
	ds_write_b128 v202, v[128:131] offset:384
	v_cvt_pk_bf16_f32 v128, v147, v151
	v_cvt_pk_bf16_f32 v129, v163, v167
	v_cvt_pk_bf16_f32 v130, v175, v179
	v_cvt_pk_bf16_f32 v131, v187, v191
	ds_write_b128 v203, v[128:131] offset:384
	v_add_u32_e32 v128, s16, v201
	v_ashrrev_i32_e32 v129, 31, v128
	v_lshlrev_b64 v[128:129], 11, v[128:129]
	v_lshl_add_u64 v[134:135], s[0:1], 0, v[128:129]
	v_add_u32_e32 v128, v204, v205
	ds_read_b128 v[130:133], v128
	s_ashr_i32 s15, s14, 31
	v_add_u32_e32 v129, v206, v207
	v_lshl_add_u64 v[134:135], s[14:15], 1, v[134:135]
	ds_read_b128 v[138:141], v129
	v_lshl_add_u64 v[146:147], v[134:135], 0, v[194:195]
	ds_read_b128 v[134:137], v128 offset:4096
	s_waitcnt lgkmcnt(2)
	global_store_dwordx4 v[146:147], v[130:133], off nt
	s_mov_b32 s14, 0x14000
	s_nop 0
	v_add_u32_e32 v130, v208, v209
	v_add_co_u32_e32 v132, vcc, s28, v146
	ds_read_b128 v[142:145], v130
	s_nop 0
	v_addc_co_u32_e32 v133, vcc, 0, v147, vcc
	v_add_u32_e32 v131, v210, v211
	s_waitcnt lgkmcnt(2)
	global_store_dwordx4 v[132:133], v[138:141], off nt
	ds_read_b128 v[138:141], v131
	v_add_co_u32_e32 v132, vcc, s29, v146
	s_nop 1
	v_addc_co_u32_e32 v133, vcc, 0, v147, vcc
	s_waitcnt lgkmcnt(1)
	global_store_dwordx4 v[132:133], v[142:145], off nt
	v_add_co_u32_e32 v148, vcc, s30, v146
	v_add_u32_e32 v132, v212, v213
	s_nop 0
	v_addc_co_u32_e32 v149, vcc, 0, v147, vcc
	ds_read_b128 v[142:145], v132
	s_waitcnt lgkmcnt(1)
	global_store_dwordx4 v[148:149], v[138:141], off nt
	v_add_u32_e32 v133, v214, v215
	s_nop 0
	v_add_co_u32_e32 v138, vcc, s31, v146
	s_nop 1
	v_addc_co_u32_e32 v139, vcc, 0, v147, vcc
	global_store_dwordx4 v[138:139], v[134:137], off nt
	ds_read_b128 v[136:139], v133
	s_nop 0
	v_add_co_u32_e32 v134, vcc, s14, v146
	s_nop 1
	v_addc_co_u32_e32 v135, vcc, 0, v147, vcc
	s_waitcnt lgkmcnt(1)
	global_store_dwordx4 v[134:135], v[142:145], off nt
	v_add_u32_e32 v134, v216, v217
	ds_read_b128 v[140:143], v134
	v_add_co_u32_e32 v144, vcc, 0x18000, v146
	s_nop 1
	v_addc_co_u32_e32 v145, vcc, 0, v147, vcc
	s_waitcnt lgkmcnt(1)
	global_store_dwordx4 v[144:145], v[136:139], off nt
	s_nop 1
	v_add_co_u32_e32 v136, vcc, 0x1c000, v146
	s_nop 1
	v_addc_co_u32_e32 v137, vcc, 0, v147, vcc
	s_andn2_b64 vcc, exec, s[4:5]
	s_waitcnt lgkmcnt(0)
	global_store_dwordx4 v[136:137], v[140:143], off nt
	s_cbranch_vccz .LBB0_150
	s_andn2_b64 vcc, exec, s[2:3]
	s_cbranch_vccnz .LBB0_143
	s_branch .LBB0_151
.LBB0_150:
	s_ashr_i32 s4, s35, 31
	s_lshr_b32 s4, s4, 25
	s_add_i32 s4, s35, s4
	s_and_b32 s4, s4, 0xff80
	v_cvt_pk_bf16_f32 v136, v4, v0
	s_sub_i32 s4, s35, s4
	v_cvt_pk_bf16_f32 v137, v12, v44
	v_cvt_pk_bf16_f32 v138, v8, v24
	v_cvt_pk_bf16_f32 v139, v28, v40
	ds_write_b128 v202, v[136:139]
	v_cvt_pk_bf16_f32 v136, v36, v32
	s_bfe_i32 s5, s4, 0x80000
	v_cvt_pk_bf16_f32 v137, v60, v56
	v_cvt_pk_bf16_f32 v138, v68, v64
	v_cvt_pk_bf16_f32 v139, v76, v72
	ds_write_b128 v203, v[136:139]
	v_cvt_pk_bf16_f32 v136, v5, v1
	s_bfe_u32 s5, s5, 0x3000c
	v_cvt_pk_bf16_f32 v137, v13, v45
	v_cvt_pk_bf16_f32 v138, v9, v25
	v_cvt_pk_bf16_f32 v139, v29, v41
	ds_write_b128 v202, v[136:139] offset:128
	v_cvt_pk_bf16_f32 v136, v37, v33
	s_add_i32 s5, s4, s5
	v_cvt_pk_bf16_f32 v137, v61, v57
	v_cvt_pk_bf16_f32 v138, v69, v65
	v_cvt_pk_bf16_f32 v139, v77, v73
	ds_write_b128 v203, v[136:139] offset:128
	v_cvt_pk_bf16_f32 v136, v6, v2
	s_bfe_i32 s14, s5, 0x80000
	v_cvt_pk_bf16_f32 v137, v14, v46
	v_cvt_pk_bf16_f32 v138, v10, v26
	v_cvt_pk_bf16_f32 v139, v30, v42
	ds_write_b128 v202, v[136:139] offset:256
	v_cvt_pk_bf16_f32 v136, v38, v34
	s_and_b32 s5, s5, 0xf8
	v_cvt_pk_bf16_f32 v137, v62, v58
	v_cvt_pk_bf16_f32 v138, v70, v66
	v_cvt_pk_bf16_f32 v139, v78, v74
	ds_write_b128 v203, v[136:139] offset:256
	v_cvt_pk_bf16_f32 v136, v7, v3
	s_sub_i32 s4, s4, s5
	v_cvt_pk_bf16_f32 v137, v15, v47
	v_cvt_pk_bf16_f32 v138, v11, v27
	v_cvt_pk_bf16_f32 v139, v31, v43
	ds_write_b128 v202, v[136:139] offset:384
	v_cvt_pk_bf16_f32 v136, v39, v35
	s_sext_i32_i8 s4, s4
	v_cvt_pk_bf16_f32 v137, v63, v59
	v_cvt_pk_bf16_f32 v138, v71, v67
	v_cvt_pk_bf16_f32 v139, v79, v75
	ds_write_b128 v203, v[136:139] offset:384
	v_lshl_add_u32 v136, s4, 6, v201
	v_ashrrev_i32_e32 v137, 31, v136
	s_sext_i32_i16 s14, s14
	v_lshlrev_b64 v[136:137], 11, v[136:137]
	v_lshl_add_u64 v[140:141], s[0:1], 0, v[136:137]
	s_lshl_b32 s4, s14, 3
	ds_read_b128 v[136:139], v128
	s_andn2_b32 s4, s4, 63
	s_ashr_i32 s5, s4, 31
	v_lshl_add_u64 v[140:141], s[4:5], 1, v[140:141]
	v_lshl_add_u64 v[148:149], v[140:141], 0, v[194:195]
	ds_read_b128 v[140:143], v128 offset:4096
	s_waitcnt lgkmcnt(1)
	global_store_dwordx4 v[148:149], v[136:139], off nt
	ds_read_b128 v[136:139], v129
	ds_read_b128 v[144:147], v130
	v_add_co_u32_e32 v150, vcc, s28, v148
	s_nop 1
	v_addc_co_u32_e32 v151, vcc, 0, v149, vcc
	s_waitcnt lgkmcnt(1)
	global_store_dwordx4 v[150:151], v[136:139], off nt
	s_nop 1
	v_add_co_u32_e32 v136, vcc, s29, v148
	s_nop 1
	v_addc_co_u32_e32 v137, vcc, 0, v149, vcc
	s_waitcnt lgkmcnt(0)
	global_store_dwordx4 v[136:137], v[144:147], off nt
	ds_read_b128 v[136:139], v131
	ds_read_b128 v[144:147], v132
	v_add_co_u32_e32 v150, vcc, s30, v148
	s_nop 1
	v_addc_co_u32_e32 v151, vcc, 0, v149, vcc
	s_waitcnt lgkmcnt(1)
	global_store_dwordx4 v[150:151], v[136:139], off nt
	s_nop 1
	v_add_co_u32_e32 v136, vcc, s31, v148
	s_nop 1
	v_addc_co_u32_e32 v137, vcc, 0, v149, vcc
	global_store_dwordx4 v[136:137], v[140:143], off nt
	v_add_co_u32_e32 v136, vcc, 0x14000, v148
	ds_read_b128 v[140:143], v134
	s_nop 0
	v_addc_co_u32_e32 v137, vcc, 0, v149, vcc
	s_waitcnt lgkmcnt(1)
	global_store_dwordx4 v[136:137], v[144:147], off nt
	ds_read_b128 v[136:139], v133
	s_nop 0
	v_add_co_u32_e32 v144, vcc, 0x18000, v148
	s_nop 1
	v_addc_co_u32_e32 v145, vcc, 0, v149, vcc
	s_waitcnt lgkmcnt(0)
	global_store_dwordx4 v[144:145], v[136:139], off nt
	s_nop 1
	v_add_co_u32_e32 v136, vcc, 0x1c000, v148
	s_nop 1
	v_addc_co_u32_e32 v137, vcc, 0, v149, vcc
	global_store_dwordx4 v[136:137], v[140:143], off nt
	s_andn2_b64 vcc, exec, s[2:3]
	s_cbranch_vccnz .LBB0_143
.LBB0_151:
	s_ashr_i32 s2, s17, 31
	s_lshr_b32 s2, s2, 25
	s_add_i32 s2, s17, s2
	s_and_b32 s2, s2, 0xff80
	v_cvt_pk_bf16_f32 v136, v20, v16
	s_sub_i32 s2, s17, s2
	v_cvt_pk_bf16_f32 v137, v52, v100
	v_cvt_pk_bf16_f32 v138, v48, v80
	v_cvt_pk_bf16_f32 v139, v84, v96
	ds_write_b128 v202, v[136:139]
	v_cvt_pk_bf16_f32 v136, v92, v88
	s_bfe_i32 s3, s2, 0x80000
	v_cvt_pk_bf16_f32 v137, v108, v104
	v_cvt_pk_bf16_f32 v138, v116, v112
	v_cvt_pk_bf16_f32 v139, v124, v120
	ds_write_b128 v203, v[136:139]
	v_cvt_pk_bf16_f32 v136, v21, v17
	s_bfe_u32 s3, s3, 0x3000c
	v_cvt_pk_bf16_f32 v137, v53, v101
	v_cvt_pk_bf16_f32 v138, v49, v81
	v_cvt_pk_bf16_f32 v139, v85, v97
	ds_write_b128 v202, v[136:139] offset:128
	v_cvt_pk_bf16_f32 v136, v93, v89
	s_add_i32 s3, s2, s3
	v_cvt_pk_bf16_f32 v137, v109, v105
	v_cvt_pk_bf16_f32 v138, v117, v113
	v_cvt_pk_bf16_f32 v139, v125, v121
	ds_write_b128 v203, v[136:139] offset:128
	v_cvt_pk_bf16_f32 v136, v22, v18
	s_bfe_i32 s4, s3, 0x80000
	v_cvt_pk_bf16_f32 v137, v54, v102
	v_cvt_pk_bf16_f32 v138, v50, v82
	v_cvt_pk_bf16_f32 v139, v86, v98
	ds_write_b128 v202, v[136:139] offset:256
	v_cvt_pk_bf16_f32 v136, v94, v90
	s_and_b32 s3, s3, 0xf8
	v_cvt_pk_bf16_f32 v137, v110, v106
	v_cvt_pk_bf16_f32 v138, v118, v114
	v_cvt_pk_bf16_f32 v139, v126, v122
	ds_write_b128 v203, v[136:139] offset:256
	v_cvt_pk_bf16_f32 v136, v23, v19
	s_sub_i32 s2, s2, s3
	v_cvt_pk_bf16_f32 v137, v55, v103
	v_cvt_pk_bf16_f32 v138, v51, v83
	v_cvt_pk_bf16_f32 v139, v87, v99
	ds_write_b128 v202, v[136:139] offset:384
	v_cvt_pk_bf16_f32 v136, v95, v91
	s_sext_i32_i8 s2, s2
	v_cvt_pk_bf16_f32 v137, v111, v107
	v_cvt_pk_bf16_f32 v138, v119, v115
	v_cvt_pk_bf16_f32 v139, v127, v123
	ds_write_b128 v203, v[136:139] offset:384
	v_lshl_add_u32 v136, s2, 6, v201
	v_ashrrev_i32_e32 v137, 31, v136
	s_sext_i32_i16 s4, s4
	v_lshlrev_b64 v[136:137], 11, v[136:137]
	v_lshl_add_u64 v[140:141], s[0:1], 0, v[136:137]
	s_lshl_b32 s2, s4, 3
	ds_read_b128 v[136:139], v128
	s_andn2_b32 s2, s2, 63
	s_ashr_i32 s3, s2, 31
	v_lshl_add_u64 v[140:141], s[2:3], 1, v[140:141]
	v_lshl_add_u64 v[148:149], v[140:141], 0, v[194:195]
	ds_read_b128 v[140:143], v128 offset:4096
	s_waitcnt lgkmcnt(1)
	global_store_dwordx4 v[148:149], v[136:139], off nt
	ds_read_b128 v[136:139], v129
	ds_read_b128 v[144:147], v130
	v_add_co_u32_e32 v128, vcc, s28, v148
	s_nop 1
	v_addc_co_u32_e32 v129, vcc, 0, v149, vcc
	s_waitcnt lgkmcnt(1)
	global_store_dwordx4 v[128:129], v[136:139], off nt
	v_add_co_u32_e32 v128, vcc, s29, v148
	ds_read_b128 v[136:139], v132
	s_nop 0
	v_addc_co_u32_e32 v129, vcc, 0, v149, vcc
	s_waitcnt lgkmcnt(1)
	global_store_dwordx4 v[128:129], v[144:147], off nt
	ds_read_b128 v[128:131], v131
	s_nop 0
	v_add_co_u32_e32 v144, vcc, s30, v148
	s_nop 1
	v_addc_co_u32_e32 v145, vcc, 0, v149, vcc
	s_waitcnt lgkmcnt(0)
	global_store_dwordx4 v[144:145], v[128:131], off nt
	s_nop 1
	v_add_co_u32_e32 v128, vcc, s31, v148
	s_nop 1
	v_addc_co_u32_e32 v129, vcc, 0, v149, vcc
	global_store_dwordx4 v[128:129], v[140:143], off nt
	v_add_co_u32_e32 v128, vcc, 0x14000, v148
	s_nop 1
	v_addc_co_u32_e32 v129, vcc, 0, v149, vcc
	global_store_dwordx4 v[128:129], v[136:139], off nt
	ds_read_b128 v[128:131], v133
	ds_read_b128 v[132:135], v134
	v_add_co_u32_e32 v136, vcc, 0x18000, v148
	s_nop 1
	v_addc_co_u32_e32 v137, vcc, 0, v149, vcc
	s_waitcnt lgkmcnt(1)
	global_store_dwordx4 v[136:137], v[128:131], off nt
	s_nop 1
	v_add_co_u32_e32 v128, vcc, 0x1c000, v148
	s_nop 1
	v_addc_co_u32_e32 v129, vcc, 0, v149, vcc
	s_waitcnt lgkmcnt(0)
	global_store_dwordx4 v[128:129], v[132:135], off nt
	s_branch .LBB0_143

.LBB0_155:
	s_add_i32 s39, s8, s23
	s_cmpk_lt_i32 s39, 0x100
	s_cselect_b64 s[4:5], -1, 0
	s_ashr_i32 s2, s23, 31
	s_lshr_b32 s2, s2, 24
	s_add_i32 s2, s23, s2
	s_and_b32 s2, s2, 0xff00
	s_sub_i32 s2, s23, s2
	s_sext_i32_i16 s3, s2
	s_bfe_u32 s3, s3, 0x4001b
	s_add_i32 s3, s2, s3
	s_sext_i32_i16 s14, s3
	s_and_b32 s3, s3, 0xfff0
	s_sub_i32 s2, s2, s3
	s_sext_i32_i16 s2, s2
	s_lshl_b32 s16, s2, 6
	s_lshl_b32 s2, s14, 2
	s_and_b32 s14, s2, 0xffffffc0
	v_add_u32_e32 v128, s14, v193
	v_ashrrev_i32_e32 v129, 31, v128
	v_readlane_b32 s40, v252, 20
	v_lshlrev_b64 v[128:129], 12, v[128:129]
	v_readlane_b32 s48, v252, 28
	v_readlane_b32 s49, v252, 29
	s_ashr_i32 s17, s16, 31
	s_cmpk_gt_i32 s39, 0xff
	v_lshl_add_u64 v[128:129], s[48:49], 0, v[128:129]
	v_lshl_add_u64 v[128:129], s[16:17], 2, v[128:129]
	v_lshl_add_u64 v[180:181], v[128:129], 0, v[198:199]
	v_add_co_u32_e32 v128, vcc, s25, v180
	v_readlane_b32 s41, v252, 21
	s_nop 0
	v_addc_co_u32_e32 v129, vcc, 0, v181, vcc
	v_add_co_u32_e32 v136, vcc, s26, v180
	global_load_dwordx4 v[132:135], v[128:129], off offset:-4096 nt
	s_nop 0
	global_load_dwordx4 v[128:131], v[128:129], off nt
	v_addc_co_u32_e32 v137, vcc, 0, v181, vcc
	v_add_co_u32_e32 v140, vcc, s27, v180
	global_load_dwordx4 v[144:147], v[136:137], off offset:-4096 nt
	s_nop 0
	global_load_dwordx4 v[136:139], v[136:137], off nt
	v_addc_co_u32_e32 v141, vcc, 0, v181, vcc
	global_load_dwordx4 v[152:155], v[140:141], off offset:-4096 nt
	global_load_dwordx4 v[148:151], v[140:141], off nt
	v_add_co_u32_e32 v140, vcc, s28, v180
	v_readlane_b32 s42, v252, 22
	s_nop 0
	v_addc_co_u32_e32 v141, vcc, 0, v181, vcc
	v_add_co_u32_e32 v156, vcc, s29, v180
	global_load_dwordx4 v[164:167], v[140:141], off offset:-4096 nt
	s_nop 0
	global_load_dwordx4 v[140:143], v[140:141], off nt
	v_addc_co_u32_e32 v157, vcc, 0, v181, vcc
	v_add_co_u32_e32 v168, vcc, s31, v180
	global_load_dwordx4 v[160:163], v[156:157], off offset:-4096 nt
	s_nop 0
	global_load_dwordx4 v[156:159], v[156:157], off nt
	v_addc_co_u32_e32 v169, vcc, 0, v181, vcc
	v_add_co_u32_e32 v176, vcc, 0xd000, v180
	global_load_dwordx4 v[172:175], v[168:169], off offset:-4096 nt
	s_nop 0
	global_load_dwordx4 v[168:171], v[168:169], off nt
	v_addc_co_u32_e32 v177, vcc, 0, v181, vcc
	v_add_co_u32_e32 v182, vcc, 0xe000, v180
	global_load_dwordx4 v[188:191], v[180:181], off nt
	s_nop 0
	global_load_dwordx4 v[176:179], v[176:177], off nt
	v_addc_co_u32_e32 v183, vcc, 0, v181, vcc
	v_add_co_u32_e32 v184, vcc, 0xf000, v180
	v_readlane_b32 s43, v252, 23
	s_nop 0
	v_addc_co_u32_e32 v185, vcc, 0, v181, vcc
	global_load_dwordx4 v[180:183], v[182:183], off nt
	s_nop 0
	global_load_dwordx4 v[184:187], v[184:185], off nt
	v_readlane_b32 s44, v252, 24
	v_readlane_b32 s45, v252, 25
	v_readlane_b32 s46, v252, 26
	v_readlane_b32 s47, v252, 27
	v_readlane_b32 s50, v252, 30
	v_readlane_b32 s51, v252, 31
	v_readlane_b32 s52, v252, 32
	v_readlane_b32 s53, v252, 33
	v_readlane_b32 s54, v252, 34
	v_readlane_b32 s55, v252, 35
	s_cbranch_scc1 .LBB0_157
	s_ashr_i32 s2, s39, 31
	s_lshr_b32 s2, s2, 24
	s_add_i32 s2, s39, s2
	s_and_b32 s2, s2, 0xff00
	s_sub_i32 s2, s39, s2
	s_sext_i32_i16 s3, s2
	s_bfe_u32 s3, s3, 0x4001b
	s_add_i32 s3, s2, s3
	s_sext_i32_i16 s15, s3
	s_and_b32 s3, s3, 0xfff0
	s_sub_i32 s2, s2, s3
	s_lshl_b32 s3, s15, 2
	s_andn2_b32 s3, s3, 63
	v_add_u32_e32 v0, s3, v193
	s_sext_i32_i16 s2, s2
	v_ashrrev_i32_e32 v1, 31, v0
	v_readlane_b32 s40, v252, 20
	s_lshl_b32 s2, s2, 6
	v_lshlrev_b64 v[0:1], 12, v[0:1]
	v_readlane_b32 s48, v252, 28
	v_readlane_b32 s49, v252, 29
	s_ashr_i32 s3, s2, 31
	v_mov_b32_e32 v197, v195
	v_lshl_add_u64 v[0:1], s[48:49], 0, v[0:1]
	v_lshl_add_u64 v[0:1], s[2:3], 2, v[0:1]
	v_lshl_add_u64 v[100:101], v[0:1], 0, v[196:197]
	v_add_co_u32_e32 v0, vcc, s25, v100
	v_readlane_b32 s41, v252, 21
	s_nop 0
	v_addc_co_u32_e32 v1, vcc, 0, v101, vcc
	v_add_co_u32_e32 v8, vcc, s26, v100
	global_load_dwordx4 v[4:7], v[0:1], off offset:-4096 nt
	s_nop 0
	global_load_dwordx4 v[0:3], v[0:1], off nt
	v_addc_co_u32_e32 v9, vcc, 0, v101, vcc
	v_add_co_u32_e32 v16, vcc, s27, v100
	global_load_dwordx4 v[12:15], v[8:9], off offset:-4096 nt
	s_nop 0
	global_load_dwordx4 v[8:11], v[8:9], off nt
	v_addc_co_u32_e32 v17, vcc, 0, v101, vcc
	v_add_co_u32_e32 v24, vcc, s28, v100
	global_load_dwordx4 v[20:23], v[16:17], off offset:-4096 nt
	s_nop 0
	global_load_dwordx4 v[16:19], v[16:17], off nt
	v_addc_co_u32_e32 v25, vcc, 0, v101, vcc
	v_add_co_u32_e32 v40, vcc, s29, v100
	global_load_dwordx4 v[28:31], v[24:25], off offset:-4096 nt
	s_nop 0
	global_load_dwordx4 v[24:27], v[24:25], off nt
	v_addc_co_u32_e32 v41, vcc, 0, v101, vcc
	v_add_co_u32_e32 v56, vcc, s30, v100
	global_load_dwordx4 v[44:47], v[40:41], off offset:-4096 nt
	s_nop 0
	global_load_dwordx4 v[40:43], v[40:41], off nt
	v_addc_co_u32_e32 v57, vcc, 0, v101, vcc
	v_add_co_u32_e32 v80, vcc, 0xc000, v100
	global_load_dwordx4 v[76:79], v[100:101], off nt
	s_nop 0
	global_load_dwordx4 v[56:59], v[56:57], off nt
	v_addc_co_u32_e32 v81, vcc, 0, v101, vcc
	v_add_co_u32_e32 v84, vcc, 0xd000, v100
	v_readlane_b32 s42, v252, 22
	s_nop 0
	v_addc_co_u32_e32 v85, vcc, 0, v101, vcc
	v_add_co_u32_e32 v102, vcc, 0xe000, v100
	global_load_dwordx4 v[80:83], v[80:81], off nt
	s_nop 0
	global_load_dwordx4 v[84:87], v[84:85], off nt
	v_addc_co_u32_e32 v103, vcc, 0, v101, vcc
	v_add_co_u32_e32 v104, vcc, 0xf000, v100
	v_readlane_b32 s43, v252, 23
	s_nop 0
	v_addc_co_u32_e32 v105, vcc, 0, v101, vcc
	global_load_dwordx4 v[100:103], v[102:103], off nt
	s_nop 0
	global_load_dwordx4 v[104:107], v[104:105], off nt
	v_readlane_b32 s44, v252, 24
	v_readlane_b32 s45, v252, 25
	v_readlane_b32 s46, v252, 26
	v_readlane_b32 s47, v252, 27
	v_readlane_b32 s50, v252, 30
	v_readlane_b32 s51, v252, 31
	v_readlane_b32 s52, v252, 32
	v_readlane_b32 s53, v252, 33
	v_readlane_b32 s54, v252, 34
	v_readlane_b32 s55, v252, 35
.LBB0_157:
	s_add_i32 s17, s24, s23
	s_cmpk_lt_i32 s17, 0x100
	s_cselect_b64 s[2:3], -1, 0
	s_cmpk_gt_i32 s17, 0xff
	s_cbranch_scc1 .LBB0_159
	s_ashr_i32 s15, s17, 31
	s_lshr_b32 s15, s15, 24
	s_add_i32 s15, s17, s15
	s_and_b32 s15, s15, 0xff00
	s_sub_i32 s15, s17, s15
	s_sext_i32_i16 s40, s15
	s_bfe_u32 s40, s40, 0x4001b
	s_add_i32 s40, s15, s40
	s_sext_i32_i16 s41, s40
	s_and_b32 s40, s40, 0xfff0
	s_sub_i32 s15, s15, s40
	s_sext_i32_i16 s15, s15
	s_lshl_b32 s40, s15, 6
	s_lshl_b32 s15, s41, 2
	s_andn2_b32 s15, s15, 63
	v_add_u32_e32 v32, s15, v193
	v_ashrrev_i32_e32 v33, 31, v32
	v_readlane_b32 s44, v252, 20
	v_lshlrev_b64 v[32:33], 12, v[32:33]
	v_readlane_b32 s52, v252, 28
	v_readlane_b32 s53, v252, 29
	s_ashr_i32 s41, s40, 31
	v_mov_b32_e32 v197, v195
	v_lshl_add_u64 v[32:33], s[52:53], 0, v[32:33]
	v_lshl_add_u64 v[32:33], s[40:41], 2, v[32:33]
	v_lshl_add_u64 v[120:121], v[32:33], 0, v[196:197]
	v_add_co_u32_e32 v32, vcc, s25, v120
	v_readlane_b32 s45, v252, 21
	s_nop 0
	v_addc_co_u32_e32 v33, vcc, 0, v121, vcc
	v_add_co_u32_e32 v48, vcc, s26, v120
	global_load_dwordx4 v[36:39], v[32:33], off offset:-4096 nt
	s_nop 0
	global_load_dwordx4 v[32:35], v[32:33], off nt
	v_addc_co_u32_e32 v49, vcc, 0, v121, vcc
	v_add_co_u32_e32 v60, vcc, s27, v120
	global_load_dwordx4 v[52:55], v[48:49], off offset:-4096 nt
	s_nop 0
	global_load_dwordx4 v[48:51], v[48:49], off nt
	v_addc_co_u32_e32 v61, vcc, 0, v121, vcc
	v_add_co_u32_e32 v68, vcc, s28, v120
	global_load_dwordx4 v[64:67], v[60:61], off offset:-4096 nt
	s_nop 0
	global_load_dwordx4 v[60:63], v[60:61], off nt
	v_addc_co_u32_e32 v69, vcc, 0, v121, vcc
	v_add_co_u32_e32 v88, vcc, s29, v120
	global_load_dwordx4 v[72:75], v[68:69], off offset:-4096 nt
	s_nop 0
	global_load_dwordx4 v[68:71], v[68:69], off nt
	v_addc_co_u32_e32 v89, vcc, 0, v121, vcc
	v_add_co_u32_e32 v96, vcc, s30, v120
	global_load_dwordx4 v[92:95], v[88:89], off offset:-4096 nt
	s_nop 0
	global_load_dwordx4 v[88:91], v[88:89], off nt
	v_addc_co_u32_e32 v97, vcc, 0, v121, vcc
	v_add_co_u32_e32 v112, vcc, 0xc000, v120
	global_load_dwordx4 v[108:111], v[120:121], off nt
	s_nop 0
	global_load_dwordx4 v[96:99], v[96:97], off nt
	v_addc_co_u32_e32 v113, vcc, 0, v121, vcc
	v_add_co_u32_e32 v116, vcc, 0xd000, v120
	v_readlane_b32 s46, v252, 22
	s_nop 0
	v_addc_co_u32_e32 v117, vcc, 0, v121, vcc
	v_add_co_u32_e32 v122, vcc, 0xe000, v120
	global_load_dwordx4 v[112:115], v[112:113], off nt
	s_nop 0
	global_load_dwordx4 v[116:119], v[116:117], off nt
	v_addc_co_u32_e32 v123, vcc, 0, v121, vcc
	v_add_co_u32_e32 v124, vcc, 0xf000, v120
	v_readlane_b32 s47, v252, 23
	s_nop 0
	v_addc_co_u32_e32 v125, vcc, 0, v121, vcc
	global_load_dwordx4 v[120:123], v[122:123], off nt
	s_nop 0
	global_load_dwordx4 v[124:127], v[124:125], off nt
	v_readlane_b32 s48, v252, 24
	v_readlane_b32 s49, v252, 25
	v_readlane_b32 s50, v252, 26
	v_readlane_b32 s51, v252, 27
	v_readlane_b32 s54, v252, 30
	v_readlane_b32 s55, v252, 31
	v_readlane_b32 s56, v252, 32
	v_readlane_b32 s57, v252, 33
	v_readlane_b32 s58, v252, 34
	v_readlane_b32 s59, v252, 35

.LBB0_166:
	s_add_i32 s35, s8, s23
	s_cmpk_lt_i32 s35, 0x80
	s_cselect_b64 s[4:5], -1, 0
	s_ashr_i32 s2, s23, 31
	s_lshr_b32 s2, s2, 25
	s_add_i32 s2, s23, s2
	s_and_b32 s2, s2, 0xff80
	s_sub_i32 s2, s23, s2
	s_bfe_i32 s3, s2, 0x80000
	s_bfe_u32 s3, s3, 0x4000b
	s_add_i32 s3, s2, s3
	s_bfe_i32 s14, s3, 0x80000
	s_and_b32 s3, s3, 0xf0
	s_sub_i32 s2, s2, s3
	s_sext_i32_i16 s14, s14
	s_sext_i32_i8 s2, s2
	s_lshl_b32 s16, s2, 6
	s_lshl_b32 s2, s14, 2
	s_and_b32 s14, s2, 0xffffffc0
	v_add_u32_e32 v128, s14, v193
	v_ashrrev_i32_e32 v129, 31, v128
	v_readlane_b32 s40, v252, 20
	v_lshlrev_b64 v[128:129], 12, v[128:129]
	v_readlane_b32 s50, v252, 30
	v_readlane_b32 s51, v252, 31
	s_ashr_i32 s17, s16, 31
	s_cmpk_gt_i32 s35, 0x7f
	v_lshl_add_u64 v[128:129], s[50:51], 0, v[128:129]
	v_lshl_add_u64 v[128:129], s[16:17], 2, v[128:129]
	v_lshl_add_u64 v[180:181], v[128:129], 0, v[198:199]
	v_add_co_u32_e32 v128, vcc, s25, v180
	v_readlane_b32 s41, v252, 21
	s_nop 0
	v_addc_co_u32_e32 v129, vcc, 0, v181, vcc
	v_add_co_u32_e32 v136, vcc, s26, v180
	global_load_dwordx4 v[132:135], v[128:129], off offset:-4096 nt
	s_nop 0
	global_load_dwordx4 v[128:131], v[128:129], off nt
	v_addc_co_u32_e32 v137, vcc, 0, v181, vcc
	v_add_co_u32_e32 v140, vcc, s27, v180
	global_load_dwordx4 v[144:147], v[136:137], off offset:-4096 nt
	s_nop 0
	global_load_dwordx4 v[136:139], v[136:137], off nt
	v_addc_co_u32_e32 v141, vcc, 0, v181, vcc
	global_load_dwordx4 v[152:155], v[140:141], off offset:-4096 nt
	global_load_dwordx4 v[148:151], v[140:141], off nt
	v_add_co_u32_e32 v140, vcc, s28, v180
	v_readlane_b32 s42, v252, 22
	s_nop 0
	v_addc_co_u32_e32 v141, vcc, 0, v181, vcc
	v_add_co_u32_e32 v156, vcc, s29, v180
	global_load_dwordx4 v[164:167], v[140:141], off offset:-4096 nt
	s_nop 0
	global_load_dwordx4 v[140:143], v[140:141], off nt
	v_addc_co_u32_e32 v157, vcc, 0, v181, vcc
	v_add_co_u32_e32 v168, vcc, s31, v180
	global_load_dwordx4 v[160:163], v[156:157], off offset:-4096 nt
	s_nop 0
	global_load_dwordx4 v[156:159], v[156:157], off nt
	v_addc_co_u32_e32 v169, vcc, 0, v181, vcc
	v_add_co_u32_e32 v176, vcc, 0xd000, v180
	global_load_dwordx4 v[172:175], v[168:169], off offset:-4096 nt
	s_nop 0
	global_load_dwordx4 v[168:171], v[168:169], off nt
	v_addc_co_u32_e32 v177, vcc, 0, v181, vcc
	v_add_co_u32_e32 v182, vcc, 0xe000, v180
	global_load_dwordx4 v[188:191], v[180:181], off nt
	s_nop 0
	global_load_dwordx4 v[176:179], v[176:177], off nt
	v_addc_co_u32_e32 v183, vcc, 0, v181, vcc
	v_add_co_u32_e32 v184, vcc, 0xf000, v180
	v_readlane_b32 s43, v252, 23
	s_nop 0
	v_addc_co_u32_e32 v185, vcc, 0, v181, vcc
	global_load_dwordx4 v[180:183], v[182:183], off nt
	s_nop 0
	global_load_dwordx4 v[184:187], v[184:185], off nt
	v_readlane_b32 s44, v252, 24
	v_readlane_b32 s45, v252, 25
	v_readlane_b32 s46, v252, 26
	v_readlane_b32 s47, v252, 27
	v_readlane_b32 s48, v252, 28
	v_readlane_b32 s49, v252, 29
	v_readlane_b32 s52, v252, 32
	v_readlane_b32 s53, v252, 33
	v_readlane_b32 s54, v252, 34
	v_readlane_b32 s55, v252, 35
	s_cbranch_scc1 .LBB0_168
	s_ashr_i32 s2, s35, 31
	s_lshr_b32 s2, s2, 25
	s_add_i32 s2, s35, s2
	s_and_b32 s2, s2, 0xff80
	s_sub_i32 s2, s35, s2
	s_bfe_i32 s3, s2, 0x80000
	s_bfe_u32 s3, s3, 0x4000b
	s_add_i32 s3, s2, s3
	s_bfe_i32 s15, s3, 0x80000
	s_sext_i32_i16 s15, s15
	s_and_b32 s3, s3, 0xf0
	s_sub_i32 s2, s2, s3
	s_lshl_b32 s3, s15, 2
	s_andn2_b32 s3, s3, 63
	v_add_u32_e32 v0, s3, v193
	s_sext_i32_i8 s2, s2
	v_ashrrev_i32_e32 v1, 31, v0
	v_readlane_b32 s40, v252, 20
	s_lshl_b32 s2, s2, 6
	v_lshlrev_b64 v[0:1], 12, v[0:1]
	v_readlane_b32 s50, v252, 30
	v_readlane_b32 s51, v252, 31
	s_ashr_i32 s3, s2, 31
	v_mov_b32_e32 v197, v195
	v_lshl_add_u64 v[0:1], s[50:51], 0, v[0:1]
	v_lshl_add_u64 v[0:1], s[2:3], 2, v[0:1]
	v_lshl_add_u64 v[100:101], v[0:1], 0, v[196:197]
	v_add_co_u32_e32 v0, vcc, s25, v100
	v_readlane_b32 s41, v252, 21
	s_nop 0
	v_addc_co_u32_e32 v1, vcc, 0, v101, vcc
	v_add_co_u32_e32 v8, vcc, s26, v100
	global_load_dwordx4 v[4:7], v[0:1], off offset:-4096 nt
	s_nop 0
	global_load_dwordx4 v[0:3], v[0:1], off nt
	v_addc_co_u32_e32 v9, vcc, 0, v101, vcc
	v_add_co_u32_e32 v16, vcc, s27, v100
	global_load_dwordx4 v[12:15], v[8:9], off offset:-4096 nt
	s_nop 0
	global_load_dwordx4 v[8:11], v[8:9], off nt
	v_addc_co_u32_e32 v17, vcc, 0, v101, vcc
	v_add_co_u32_e32 v24, vcc, s28, v100
	global_load_dwordx4 v[20:23], v[16:17], off offset:-4096 nt
	s_nop 0
	global_load_dwordx4 v[16:19], v[16:17], off nt
	v_addc_co_u32_e32 v25, vcc, 0, v101, vcc
	v_add_co_u32_e32 v40, vcc, s29, v100
	global_load_dwordx4 v[28:31], v[24:25], off offset:-4096 nt
	s_nop 0
	global_load_dwordx4 v[24:27], v[24:25], off nt
	v_addc_co_u32_e32 v41, vcc, 0, v101, vcc
	v_add_co_u32_e32 v56, vcc, s30, v100
	global_load_dwordx4 v[44:47], v[40:41], off offset:-4096 nt
	s_nop 0
	global_load_dwordx4 v[40:43], v[40:41], off nt
	v_addc_co_u32_e32 v57, vcc, 0, v101, vcc
	v_add_co_u32_e32 v80, vcc, 0xc000, v100
	global_load_dwordx4 v[76:79], v[100:101], off nt
	s_nop 0
	global_load_dwordx4 v[56:59], v[56:57], off nt
	v_addc_co_u32_e32 v81, vcc, 0, v101, vcc
	v_add_co_u32_e32 v92, vcc, 0xd000, v100
	v_readlane_b32 s42, v252, 22
	s_nop 0
	v_addc_co_u32_e32 v93, vcc, 0, v101, vcc
	v_add_co_u32_e32 v102, vcc, 0xe000, v100
	global_load_dwordx4 v[80:83], v[80:81], off nt
	s_nop 0
	global_load_dwordx4 v[92:95], v[92:93], off nt
	v_addc_co_u32_e32 v103, vcc, 0, v101, vcc
	v_add_co_u32_e32 v104, vcc, 0xf000, v100
	v_readlane_b32 s43, v252, 23
	s_nop 0
	v_addc_co_u32_e32 v105, vcc, 0, v101, vcc
	global_load_dwordx4 v[100:103], v[102:103], off nt
	s_nop 0
	global_load_dwordx4 v[104:107], v[104:105], off nt
	v_readlane_b32 s44, v252, 24
	v_readlane_b32 s45, v252, 25
	v_readlane_b32 s46, v252, 26
	v_readlane_b32 s47, v252, 27
	v_readlane_b32 s48, v252, 28
	v_readlane_b32 s49, v252, 29
	v_readlane_b32 s52, v252, 32
	v_readlane_b32 s53, v252, 33
	v_readlane_b32 s54, v252, 34
	v_readlane_b32 s55, v252, 35
.LBB0_168:
	s_add_i32 s17, s24, s23
	s_cmpk_lt_i32 s17, 0x80
	s_cselect_b64 s[2:3], -1, 0
	s_cmpk_gt_i32 s17, 0x7f
	s_cbranch_scc1 .LBB0_170
	s_ashr_i32 s15, s17, 31
	s_lshr_b32 s15, s15, 25
	s_add_i32 s15, s17, s15
	s_and_b32 s15, s15, 0xff80
	s_sub_i32 s15, s17, s15
	s_bfe_i32 s39, s15, 0x80000
	s_bfe_u32 s39, s39, 0x4000b
	s_add_i32 s39, s15, s39
	s_bfe_i32 s40, s39, 0x80000
	s_and_b32 s39, s39, 0xf0
	s_sub_i32 s15, s15, s39
	s_sext_i32_i16 s41, s40
	s_sext_i32_i8 s15, s15
	s_lshl_b32 s40, s15, 6
	s_lshl_b32 s15, s41, 2
	s_andn2_b32 s15, s15, 63
	v_add_u32_e32 v32, s15, v193
	v_ashrrev_i32_e32 v33, 31, v32
	v_readlane_b32 s44, v252, 20
	v_lshlrev_b64 v[32:33], 12, v[32:33]
	v_readlane_b32 s54, v252, 30
	v_readlane_b32 s55, v252, 31
	s_ashr_i32 s41, s40, 31
	v_mov_b32_e32 v197, v195
	v_lshl_add_u64 v[32:33], s[54:55], 0, v[32:33]
	v_lshl_add_u64 v[32:33], s[40:41], 2, v[32:33]
	v_lshl_add_u64 v[120:121], v[32:33], 0, v[196:197]
	v_add_co_u32_e32 v32, vcc, s25, v120
	v_readlane_b32 s45, v252, 21
	s_nop 0
	v_addc_co_u32_e32 v33, vcc, 0, v121, vcc
	v_add_co_u32_e32 v48, vcc, s26, v120
	global_load_dwordx4 v[36:39], v[32:33], off offset:-4096 nt
	s_nop 0
	global_load_dwordx4 v[32:35], v[32:33], off nt
	v_addc_co_u32_e32 v49, vcc, 0, v121, vcc
	v_add_co_u32_e32 v60, vcc, s27, v120
	global_load_dwordx4 v[52:55], v[48:49], off offset:-4096 nt
	s_nop 0
	global_load_dwordx4 v[48:51], v[48:49], off nt
	v_addc_co_u32_e32 v61, vcc, 0, v121, vcc
	v_add_co_u32_e32 v68, vcc, s28, v120
	global_load_dwordx4 v[64:67], v[60:61], off offset:-4096 nt
	s_nop 0
	global_load_dwordx4 v[60:63], v[60:61], off nt
	v_addc_co_u32_e32 v69, vcc, 0, v121, vcc
	v_add_co_u32_e32 v84, vcc, s29, v120
	global_load_dwordx4 v[72:75], v[68:69], off offset:-4096 nt
	s_nop 0
	global_load_dwordx4 v[68:71], v[68:69], off nt
	v_addc_co_u32_e32 v85, vcc, 0, v121, vcc
	v_add_co_u32_e32 v96, vcc, s30, v120
	global_load_dwordx4 v[88:91], v[84:85], off offset:-4096 nt
	s_nop 0
	global_load_dwordx4 v[84:87], v[84:85], off nt
	v_addc_co_u32_e32 v97, vcc, 0, v121, vcc
	v_add_co_u32_e32 v112, vcc, 0xc000, v120
	global_load_dwordx4 v[108:111], v[120:121], off nt
	s_nop 0
	global_load_dwordx4 v[96:99], v[96:97], off nt
	v_addc_co_u32_e32 v113, vcc, 0, v121, vcc
	v_add_co_u32_e32 v116, vcc, 0xd000, v120
	v_readlane_b32 s46, v252, 22
	s_nop 0
	v_addc_co_u32_e32 v117, vcc, 0, v121, vcc
	v_add_co_u32_e32 v122, vcc, 0xe000, v120
	global_load_dwordx4 v[112:115], v[112:113], off nt
	s_nop 0
	global_load_dwordx4 v[116:119], v[116:117], off nt
	v_addc_co_u32_e32 v123, vcc, 0, v121, vcc
	v_add_co_u32_e32 v124, vcc, 0xf000, v120
	v_readlane_b32 s47, v252, 23
	s_nop 0
	v_addc_co_u32_e32 v125, vcc, 0, v121, vcc
	global_load_dwordx4 v[120:123], v[122:123], off nt
	s_nop 0
	global_load_dwordx4 v[124:127], v[124:125], off nt
	v_readlane_b32 s48, v252, 24
	v_readlane_b32 s49, v252, 25
	v_readlane_b32 s50, v252, 26
	v_readlane_b32 s51, v252, 27
	v_readlane_b32 s52, v252, 28
	v_readlane_b32 s53, v252, 29
	v_readlane_b32 s56, v252, 32
	v_readlane_b32 s57, v252, 33
	v_readlane_b32 s58, v252, 34
	v_readlane_b32 s59, v252, 35
.LBB0_170:
	s_waitcnt vmcnt(3)
	v_cvt_pk_bf16_f32 v218, v188, v132
	v_cvt_pk_bf16_f32 v219, v128, v144
	v_cvt_pk_bf16_f32 v220, v136, v152
	v_cvt_pk_bf16_f32 v221, v148, v164
	ds_write_b128 v202, v[218:221]
	v_cvt_pk_bf16_f32 v218, v140, v160
	v_cvt_pk_bf16_f32 v219, v156, v172
	s_waitcnt vmcnt(2)
	v_cvt_pk_bf16_f32 v220, v168, v176
	s_waitcnt vmcnt(0)
	v_cvt_pk_bf16_f32 v221, v180, v184
	ds_write_b128 v203, v[218:221]
	v_cvt_pk_bf16_f32 v218, v189, v133
	v_cvt_pk_bf16_f32 v219, v129, v145
	v_cvt_pk_bf16_f32 v220, v137, v153
	v_cvt_pk_bf16_f32 v221, v149, v165
	ds_write_b128 v202, v[218:221] offset:128
	v_cvt_pk_bf16_f32 v218, v141, v161
	v_cvt_pk_bf16_f32 v219, v157, v173
	v_cvt_pk_bf16_f32 v220, v169, v177
	v_cvt_pk_bf16_f32 v221, v181, v185
	ds_write_b128 v203, v[218:221] offset:128
	v_cvt_pk_bf16_f32 v218, v190, v134
	v_cvt_pk_bf16_f32 v219, v130, v146
	v_cvt_pk_bf16_f32 v220, v138, v154
	v_cvt_pk_bf16_f32 v221, v150, v166
	ds_write_b128 v202, v[218:221] offset:256
	v_cvt_pk_bf16_f32 v218, v142, v162
	v_cvt_pk_bf16_f32 v219, v158, v174
	v_cvt_pk_bf16_f32 v220, v170, v178
	v_cvt_pk_bf16_f32 v221, v182, v186
	ds_write_b128 v203, v[218:221] offset:256
	v_cvt_pk_bf16_f32 v128, v191, v135
	v_cvt_pk_bf16_f32 v129, v131, v147
	v_cvt_pk_bf16_f32 v130, v139, v155
	v_cvt_pk_bf16_f32 v131, v151, v167
	ds_write_b128 v202, v[128:131] offset:384
	v_cvt_pk_bf16_f32 v128, v143, v163
	v_cvt_pk_bf16_f32 v129, v159, v175
	v_cvt_pk_bf16_f32 v130, v171, v179
	v_cvt_pk_bf16_f32 v131, v183, v187
	ds_write_b128 v203, v[128:131] offset:384
	v_add_u32_e32 v128, s16, v201
	v_ashrrev_i32_e32 v129, 31, v128
	v_lshlrev_b64 v[128:129], 10, v[128:129]
	v_lshl_add_u64 v[134:135], s[0:1], 0, v[128:129]
	v_add_u32_e32 v128, v204, v205
	ds_read_b128 v[130:133], v128
	s_ashr_i32 s15, s14, 31
	v_add_u32_e32 v129, v206, v207
	v_lshl_add_u64 v[134:135], s[14:15], 1, v[134:135]
	ds_read_b128 v[138:141], v129
	v_lshl_add_u64 v[146:147], v[134:135], 0, v[194:195]
	ds_read_b128 v[134:137], v128 offset:4096
	s_waitcnt lgkmcnt(2)
	global_store_dwordx4 v[146:147], v[130:133], off nt
	s_nop 1
	v_add_u32_e32 v130, v208, v209
	v_add_co_u32_e32 v132, vcc, s25, v146
	ds_read_b128 v[142:145], v130
	s_nop 0
	v_addc_co_u32_e32 v133, vcc, 0, v147, vcc
	v_add_u32_e32 v131, v210, v211
	s_waitcnt lgkmcnt(2)
	global_store_dwordx4 v[132:133], v[138:141], off nt
	ds_read_b128 v[138:141], v131
	v_add_co_u32_e32 v132, vcc, s26, v146
	s_nop 1
	v_addc_co_u32_e32 v133, vcc, 0, v147, vcc
	s_waitcnt lgkmcnt(1)
	global_store_dwordx4 v[132:133], v[142:145], off nt
	v_add_co_u32_e32 v148, vcc, s27, v146
	v_add_u32_e32 v132, v212, v213
	s_nop 0
	v_addc_co_u32_e32 v149, vcc, 0, v147, vcc
	ds_read_b128 v[142:145], v132
	s_waitcnt lgkmcnt(1)
	global_store_dwordx4 v[148:149], v[138:141], off nt
	v_add_u32_e32 v133, v214, v215
	s_nop 0
	v_add_co_u32_e32 v138, vcc, s28, v146
	s_nop 1
	v_addc_co_u32_e32 v139, vcc, 0, v147, vcc
	global_store_dwordx4 v[138:139], v[134:137], off nt
	ds_read_b128 v[136:139], v133
	s_nop 0
	v_add_co_u32_e32 v134, vcc, s29, v146
	s_nop 1
	v_addc_co_u32_e32 v135, vcc, 0, v147, vcc
	s_waitcnt lgkmcnt(1)
	global_store_dwordx4 v[134:135], v[142:145], off nt
	v_add_u32_e32 v134, v216, v217
	ds_read_b128 v[140:143], v134
	v_add_co_u32_e32 v144, vcc, 0xc000, v146
	s_nop 1
	v_addc_co_u32_e32 v145, vcc, 0, v147, vcc
	s_waitcnt lgkmcnt(1)
	global_store_dwordx4 v[144:145], v[136:139], off nt
	s_nop 1
	v_add_co_u32_e32 v136, vcc, 0xe000, v146
	s_nop 1
	v_addc_co_u32_e32 v137, vcc, 0, v147, vcc
	s_andn2_b64 vcc, exec, s[4:5]
	s_waitcnt lgkmcnt(0)
	global_store_dwordx4 v[136:137], v[140:143], off nt
	s_cbranch_vccz .LBB0_172
	s_andn2_b64 vcc, exec, s[2:3]
	s_cbranch_vccnz .LBB0_165
	s_branch .LBB0_173
.LBB0_172:
	s_ashr_i32 s4, s35, 31
	s_lshr_b32 s4, s4, 25
	s_add_i32 s4, s35, s4
	s_and_b32 s4, s4, 0xff80
	v_cvt_pk_bf16_f32 v136, v76, v4
	s_sub_i32 s4, s35, s4
	v_cvt_pk_bf16_f32 v137, v0, v12
	v_cvt_pk_bf16_f32 v138, v8, v20
	v_cvt_pk_bf16_f32 v139, v16, v28
	ds_write_b128 v202, v[136:139]
	v_cvt_pk_bf16_f32 v136, v24, v44
	s_bfe_i32 s5, s4, 0x80000
	v_cvt_pk_bf16_f32 v137, v40, v56
	v_cvt_pk_bf16_f32 v138, v80, v92
	v_cvt_pk_bf16_f32 v139, v100, v104
	ds_write_b128 v203, v[136:139]
	v_cvt_pk_bf16_f32 v136, v77, v5
	s_bfe_u32 s5, s5, 0x4000b
	v_cvt_pk_bf16_f32 v137, v1, v13
	v_cvt_pk_bf16_f32 v138, v9, v21
	v_cvt_pk_bf16_f32 v139, v17, v29
	ds_write_b128 v202, v[136:139] offset:128
	v_cvt_pk_bf16_f32 v136, v25, v45
	s_add_i32 s5, s4, s5
	v_cvt_pk_bf16_f32 v137, v41, v57
	v_cvt_pk_bf16_f32 v138, v81, v93
	v_cvt_pk_bf16_f32 v139, v101, v105
	ds_write_b128 v203, v[136:139] offset:128
	v_cvt_pk_bf16_f32 v136, v78, v6
	s_bfe_i32 s14, s5, 0x80000
	v_cvt_pk_bf16_f32 v137, v2, v14
	v_cvt_pk_bf16_f32 v138, v10, v22
	v_cvt_pk_bf16_f32 v139, v18, v30
	ds_write_b128 v202, v[136:139] offset:256
	v_cvt_pk_bf16_f32 v136, v26, v46
	s_and_b32 s5, s5, 0xf0
	v_cvt_pk_bf16_f32 v137, v42, v58
	v_cvt_pk_bf16_f32 v138, v82, v94
	v_cvt_pk_bf16_f32 v139, v102, v106
	ds_write_b128 v203, v[136:139] offset:256
	v_cvt_pk_bf16_f32 v136, v79, v7
	s_sub_i32 s4, s4, s5
	v_cvt_pk_bf16_f32 v137, v3, v15
	v_cvt_pk_bf16_f32 v138, v11, v23
	v_cvt_pk_bf16_f32 v139, v19, v31
	ds_write_b128 v202, v[136:139] offset:384
	v_cvt_pk_bf16_f32 v136, v27, v47
	s_sext_i32_i8 s4, s4
	v_cvt_pk_bf16_f32 v137, v43, v59
	v_cvt_pk_bf16_f32 v138, v83, v95
	v_cvt_pk_bf16_f32 v139, v103, v107
	ds_write_b128 v203, v[136:139] offset:384
	v_lshl_add_u32 v136, s4, 6, v201
	v_ashrrev_i32_e32 v137, 31, v136
	s_sext_i32_i16 s14, s14
	v_lshlrev_b64 v[136:137], 10, v[136:137]
	v_lshl_add_u64 v[140:141], s[0:1], 0, v[136:137]
	s_lshl_b32 s4, s14, 2
	ds_read_b128 v[136:139], v128
	s_andn2_b32 s4, s4, 63
	s_ashr_i32 s5, s4, 31
	v_lshl_add_u64 v[140:141], s[4:5], 1, v[140:141]
	v_lshl_add_u64 v[148:149], v[140:141], 0, v[194:195]
	ds_read_b128 v[140:143], v128 offset:4096
	s_waitcnt lgkmcnt(1)
	global_store_dwordx4 v[148:149], v[136:139], off nt
	ds_read_b128 v[136:139], v129
	ds_read_b128 v[144:147], v130
	v_add_co_u32_e32 v150, vcc, s25, v148
	s_nop 1
	v_addc_co_u32_e32 v151, vcc, 0, v149, vcc
	s_waitcnt lgkmcnt(1)
	global_store_dwordx4 v[150:151], v[136:139], off nt
	s_nop 1
	v_add_co_u32_e32 v136, vcc, s26, v148
	s_nop 1
	v_addc_co_u32_e32 v137, vcc, 0, v149, vcc
	s_waitcnt lgkmcnt(0)
	global_store_dwordx4 v[136:137], v[144:147], off nt
	ds_read_b128 v[136:139], v131
	ds_read_b128 v[144:147], v132
	v_add_co_u32_e32 v150, vcc, s27, v148
	s_nop 1
	v_addc_co_u32_e32 v151, vcc, 0, v149, vcc
	s_waitcnt lgkmcnt(1)
	global_store_dwordx4 v[150:151], v[136:139], off nt
	s_nop 1
	v_add_co_u32_e32 v136, vcc, s28, v148
	s_nop 1
	v_addc_co_u32_e32 v137, vcc, 0, v149, vcc
	global_store_dwordx4 v[136:137], v[140:143], off nt
	v_add_co_u32_e32 v136, vcc, 0xa000, v148
	ds_read_b128 v[140:143], v134
	s_nop 0
	v_addc_co_u32_e32 v137, vcc, 0, v149, vcc
	s_waitcnt lgkmcnt(1)
	global_store_dwordx4 v[136:137], v[144:147], off nt
	ds_read_b128 v[136:139], v133
	s_nop 0
	v_add_co_u32_e32 v144, vcc, 0xc000, v148
	s_nop 1
	v_addc_co_u32_e32 v145, vcc, 0, v149, vcc
	s_waitcnt lgkmcnt(0)
	global_store_dwordx4 v[144:145], v[136:139], off nt
	s_nop 1
	v_add_co_u32_e32 v136, vcc, 0xe000, v148
	s_nop 1
	v_addc_co_u32_e32 v137, vcc, 0, v149, vcc
	global_store_dwordx4 v[136:137], v[140:143], off nt
	s_andn2_b64 vcc, exec, s[2:3]
	s_cbranch_vccnz .LBB0_165
.LBB0_173:
	s_ashr_i32 s2, s17, 31
	s_lshr_b32 s2, s2, 25
	s_add_i32 s2, s17, s2
	s_and_b32 s2, s2, 0xff80
	v_cvt_pk_bf16_f32 v136, v108, v36
	s_sub_i32 s2, s17, s2
	v_cvt_pk_bf16_f32 v137, v32, v52
	v_cvt_pk_bf16_f32 v138, v48, v64
	v_cvt_pk_bf16_f32 v139, v60, v72
	ds_write_b128 v202, v[136:139]
	v_cvt_pk_bf16_f32 v136, v68, v88
	s_bfe_i32 s3, s2, 0x80000
	v_cvt_pk_bf16_f32 v137, v84, v96
	v_cvt_pk_bf16_f32 v138, v112, v116
	v_cvt_pk_bf16_f32 v139, v120, v124
	ds_write_b128 v203, v[136:139]
	v_cvt_pk_bf16_f32 v136, v109, v37
	s_bfe_u32 s3, s3, 0x4000b
	v_cvt_pk_bf16_f32 v137, v33, v53
	v_cvt_pk_bf16_f32 v138, v49, v65
	v_cvt_pk_bf16_f32 v139, v61, v73
	ds_write_b128 v202, v[136:139] offset:128
	v_cvt_pk_bf16_f32 v136, v69, v89
	s_add_i32 s3, s2, s3
	v_cvt_pk_bf16_f32 v137, v85, v97
	v_cvt_pk_bf16_f32 v138, v113, v117
	v_cvt_pk_bf16_f32 v139, v121, v125
	ds_write_b128 v203, v[136:139] offset:128
	v_cvt_pk_bf16_f32 v136, v110, v38
	s_bfe_i32 s4, s3, 0x80000
	v_cvt_pk_bf16_f32 v137, v34, v54
	v_cvt_pk_bf16_f32 v138, v50, v66
	v_cvt_pk_bf16_f32 v139, v62, v74
	ds_write_b128 v202, v[136:139] offset:256
	v_cvt_pk_bf16_f32 v136, v70, v90
	s_and_b32 s3, s3, 0xf0
	v_cvt_pk_bf16_f32 v137, v86, v98
	v_cvt_pk_bf16_f32 v138, v114, v118
	v_cvt_pk_bf16_f32 v139, v122, v126
	ds_write_b128 v203, v[136:139] offset:256
	v_cvt_pk_bf16_f32 v136, v111, v39
	s_sub_i32 s2, s2, s3
	v_cvt_pk_bf16_f32 v137, v35, v55
	v_cvt_pk_bf16_f32 v138, v51, v67
	v_cvt_pk_bf16_f32 v139, v63, v75
	ds_write_b128 v202, v[136:139] offset:384
	v_cvt_pk_bf16_f32 v136, v71, v91
	s_sext_i32_i8 s2, s2
	v_cvt_pk_bf16_f32 v137, v87, v99
	v_cvt_pk_bf16_f32 v138, v115, v119
	v_cvt_pk_bf16_f32 v139, v123, v127
	ds_write_b128 v203, v[136:139] offset:384
	v_lshl_add_u32 v136, s2, 6, v201
	v_ashrrev_i32_e32 v137, 31, v136
	s_sext_i32_i16 s4, s4
	v_lshlrev_b64 v[136:137], 10, v[136:137]
	v_lshl_add_u64 v[140:141], s[0:1], 0, v[136:137]
	s_lshl_b32 s2, s4, 2
	ds_read_b128 v[136:139], v128
	s_andn2_b32 s2, s2, 63
	s_ashr_i32 s3, s2, 31
	v_lshl_add_u64 v[140:141], s[2:3], 1, v[140:141]
	v_lshl_add_u64 v[148:149], v[140:141], 0, v[194:195]
	ds_read_b128 v[140:143], v128 offset:4096
	s_waitcnt lgkmcnt(1)
	global_store_dwordx4 v[148:149], v[136:139], off nt
	ds_read_b128 v[136:139], v129
	ds_read_b128 v[144:147], v130
	v_add_co_u32_e32 v128, vcc, s25, v148
	s_nop 1
	v_addc_co_u32_e32 v129, vcc, 0, v149, vcc
	s_waitcnt lgkmcnt(1)
	global_store_dwordx4 v[128:129], v[136:139], off nt
	v_add_co_u32_e32 v128, vcc, s26, v148
	ds_read_b128 v[136:139], v132
	s_nop 0
	v_addc_co_u32_e32 v129, vcc, 0, v149, vcc
	s_waitcnt lgkmcnt(1)
	global_store_dwordx4 v[128:129], v[144:147], off nt
	ds_read_b128 v[128:131], v131
	s_nop 0
	v_add_co_u32_e32 v144, vcc, s27, v148
	s_nop 1
	v_addc_co_u32_e32 v145, vcc, 0, v149, vcc
	s_waitcnt lgkmcnt(0)
	global_store_dwordx4 v[144:145], v[128:131], off nt
	s_nop 1
	v_add_co_u32_e32 v128, vcc, s28, v148
	s_nop 1
	v_addc_co_u32_e32 v129, vcc, 0, v149, vcc
	global_store_dwordx4 v[128:129], v[140:143], off nt
	v_add_co_u32_e32 v128, vcc, 0xa000, v148
	s_nop 1
	v_addc_co_u32_e32 v129, vcc, 0, v149, vcc
	global_store_dwordx4 v[128:129], v[136:139], off nt
	ds_read_b128 v[128:131], v133
	ds_read_b128 v[132:135], v134
	v_add_co_u32_e32 v136, vcc, 0xc000, v148
	s_nop 1
	v_addc_co_u32_e32 v137, vcc, 0, v149, vcc
	s_waitcnt lgkmcnt(1)
	global_store_dwordx4 v[136:137], v[128:131], off nt
	s_nop 1
	v_add_co_u32_e32 v128, vcc, 0xe000, v148
	s_nop 1
	v_addc_co_u32_e32 v129, vcc, 0, v149, vcc
	s_waitcnt lgkmcnt(0)
	global_store_dwordx4 v[128:129], v[132:135], off nt
	s_branch .LBB0_165

.LBB0_177:
	s_add_i32 s31, s8, s23
	s_cmp_lt_i32 s31, 64
	s_cselect_b64 s[4:5], -1, 0
	s_ashr_i32 s2, s23, 31
	s_lshr_b32 s2, s2, 26
	s_add_i32 s2, s23, s2
	s_and_b32 s2, s2, 0xffc0
	s_sub_i32 s2, s23, s2
	s_bfe_i32 s3, s2, 0x80000
	s_bfe_u32 s3, s3, 0x2000d
	s_add_i32 s3, s2, s3
	s_bfe_i32 s14, s3, 0x80000
	s_and_b32 s3, s3, 0xfc
	s_sub_i32 s2, s2, s3
	s_sext_i32_i16 s14, s14
	s_sext_i32_i8 s2, s2
	s_lshl_b32 s16, s2, 6
	s_lshl_b32 s2, s14, 4
	s_and_b32 s14, s2, 0xffffffc0
	v_add_u32_e32 v128, s14, v193
	v_ashrrev_i32_e32 v129, 31, v128
	v_readlane_b32 s40, v252, 36
	v_lshlrev_b64 v[128:129], 10, v[128:129]
	v_readlane_b32 s41, v252, 37
	s_ashr_i32 s17, s16, 31
	s_cmp_gt_i32 s31, 63
	v_lshl_add_u64 v[128:129], s[40:41], 0, v[128:129]
	v_lshl_add_u64 v[128:129], s[16:17], 2, v[128:129]
	v_lshl_add_u64 v[172:173], v[128:129], 0, v[198:199]
	v_add_co_u32_e32 v140, vcc, s25, v172
	global_load_dwordx4 v[132:135], v[172:173], off nt
	global_load_dwordx4 v[144:147], v[172:173], off offset:1024 nt
	global_load_dwordx4 v[128:131], v[172:173], off offset:2048 nt
	global_load_dwordx4 v[136:139], v[172:173], off offset:3072 nt
	v_addc_co_u32_e32 v141, vcc, 0, v173, vcc
	v_add_co_u32_e32 v152, vcc, 0x2000, v172
	global_load_dwordx4 v[164:167], v[140:141], off nt
	global_load_dwordx4 v[176:179], v[140:141], off offset:1024 nt
	global_load_dwordx4 v[156:159], v[140:141], off offset:2048 nt
	global_load_dwordx4 v[168:171], v[140:141], off offset:3072 nt
	v_addc_co_u32_e32 v153, vcc, 0, v173, vcc
	v_add_co_u32_e32 v184, vcc, 0x3000, v172
	global_load_dwordx4 v[148:151], v[152:153], off nt
	global_load_dwordx4 v[160:163], v[152:153], off offset:1024 nt
	global_load_dwordx4 v[140:143], v[152:153], off offset:2048 nt
	s_nop 0
	global_load_dwordx4 v[152:155], v[152:153], off offset:3072 nt
	v_addc_co_u32_e32 v185, vcc, 0, v173, vcc
	global_load_dwordx4 v[180:183], v[184:185], off nt
	global_load_dwordx4 v[188:191], v[184:185], off offset:1024 nt
	global_load_dwordx4 v[172:175], v[184:185], off offset:2048 nt
	s_nop 0
	global_load_dwordx4 v[184:187], v[184:185], off offset:3072 nt
	v_readlane_b32 s42, v252, 38
	v_readlane_b32 s43, v252, 39
	v_readlane_b32 s44, v252, 40
	v_readlane_b32 s45, v252, 41
	v_readlane_b32 s46, v252, 42
	v_readlane_b32 s47, v252, 43
	v_readlane_b32 s48, v252, 44
	v_readlane_b32 s49, v252, 45
	v_readlane_b32 s50, v252, 46
	v_readlane_b32 s51, v252, 47
	v_readlane_b32 s52, v252, 48
	v_readlane_b32 s53, v252, 49
	v_readlane_b32 s54, v252, 50
	v_readlane_b32 s55, v252, 51
	s_cbranch_scc1 .LBB0_179
	s_ashr_i32 s2, s31, 31
	s_lshr_b32 s2, s2, 26
	s_add_i32 s2, s31, s2
	s_and_b32 s2, s2, 0xffc0
	s_sub_i32 s2, s31, s2
	s_bfe_i32 s3, s2, 0x80000
	s_bfe_u32 s3, s3, 0x2000d
	s_add_i32 s3, s2, s3
	s_bfe_i32 s15, s3, 0x80000
	s_sext_i32_i16 s15, s15
	s_and_b32 s3, s3, 0xfc
	s_sub_i32 s2, s2, s3
	s_lshl_b32 s3, s15, 4
	s_andn2_b32 s3, s3, 63
	v_add_u32_e32 v0, s3, v193
	s_sext_i32_i8 s2, s2
	v_ashrrev_i32_e32 v1, 31, v0
	v_readlane_b32 s40, v252, 36
	s_lshl_b32 s2, s2, 6
	v_lshlrev_b64 v[0:1], 10, v[0:1]
	v_readlane_b32 s41, v252, 37
	s_ashr_i32 s3, s2, 31
	v_mov_b32_e32 v197, v195
	v_lshl_add_u64 v[0:1], s[40:41], 0, v[0:1]
	v_lshl_add_u64 v[0:1], s[2:3], 2, v[0:1]
	v_lshl_add_u64 v[48:49], v[0:1], 0, v[196:197]
	v_add_co_u32_e32 v16, vcc, s25, v48
	global_load_dwordx4 v[12:15], v[48:49], off nt
	global_load_dwordx4 v[8:11], v[48:49], off offset:1024 nt
	global_load_dwordx4 v[4:7], v[48:49], off offset:2048 nt
	global_load_dwordx4 v[0:3], v[48:49], off offset:3072 nt
	v_addc_co_u32_e32 v17, vcc, 0, v49, vcc
	v_add_co_u32_e32 v32, vcc, 0x2000, v48
	global_load_dwordx4 v[28:31], v[16:17], off nt
	global_load_dwordx4 v[24:27], v[16:17], off offset:1024 nt
	global_load_dwordx4 v[20:23], v[16:17], off offset:2048 nt
	s_nop 0
	global_load_dwordx4 v[16:19], v[16:17], off offset:3072 nt
	v_addc_co_u32_e32 v33, vcc, 0, v49, vcc
	v_add_co_u32_e32 v48, vcc, 0x3000, v48
	global_load_dwordx4 v[44:47], v[32:33], off nt
	global_load_dwordx4 v[40:43], v[32:33], off offset:1024 nt
	global_load_dwordx4 v[36:39], v[32:33], off offset:2048 nt
	s_nop 0
	global_load_dwordx4 v[32:35], v[32:33], off offset:3072 nt
	v_addc_co_u32_e32 v49, vcc, 0, v49, vcc
	global_load_dwordx4 v[60:63], v[48:49], off nt
	global_load_dwordx4 v[56:59], v[48:49], off offset:1024 nt
	global_load_dwordx4 v[52:55], v[48:49], off offset:2048 nt
	s_nop 0
	global_load_dwordx4 v[48:51], v[48:49], off offset:3072 nt
	v_readlane_b32 s42, v252, 38
	v_readlane_b32 s43, v252, 39
	v_readlane_b32 s44, v252, 40
	v_readlane_b32 s45, v252, 41
	v_readlane_b32 s46, v252, 42
	v_readlane_b32 s47, v252, 43
	v_readlane_b32 s48, v252, 44
	v_readlane_b32 s49, v252, 45
	v_readlane_b32 s50, v252, 46
	v_readlane_b32 s51, v252, 47
	v_readlane_b32 s52, v252, 48
	v_readlane_b32 s53, v252, 49
	v_readlane_b32 s54, v252, 50
	v_readlane_b32 s55, v252, 51
.LBB0_179:
	s_add_i32 s17, s24, s23
	s_cmp_lt_i32 s17, 64
	s_cselect_b64 s[2:3], -1, 0
	s_cmp_gt_i32 s17, 63
	s_cbranch_scc1 .LBB0_181
	s_ashr_i32 s15, s17, 31
	s_lshr_b32 s15, s15, 26
	s_add_i32 s15, s17, s15
	s_and_b32 s15, s15, 0xffc0
	s_sub_i32 s15, s17, s15
	s_bfe_i32 s35, s15, 0x80000
	s_bfe_u32 s35, s35, 0x2000d
	s_add_i32 s35, s15, s35
	s_bfe_i32 s39, s35, 0x80000
	s_and_b32 s35, s35, 0xfc
	s_sub_i32 s15, s15, s35
	s_sext_i32_i16 s39, s39
	s_sext_i32_i8 s15, s15
	s_lshl_b32 s40, s15, 6
	s_lshl_b32 s15, s39, 4
	s_andn2_b32 s15, s15, 63
	v_add_u32_e32 v64, s15, v193
	v_ashrrev_i32_e32 v65, 31, v64
	v_readlane_b32 s44, v252, 36
	v_lshlrev_b64 v[64:65], 10, v[64:65]
	v_readlane_b32 s45, v252, 37
	s_ashr_i32 s41, s40, 31
	v_mov_b32_e32 v197, v195
	v_lshl_add_u64 v[64:65], s[44:45], 0, v[64:65]
	v_lshl_add_u64 v[64:65], s[40:41], 2, v[64:65]
	v_lshl_add_u64 v[112:113], v[64:65], 0, v[196:197]
	v_add_co_u32_e32 v80, vcc, s25, v112
	global_load_dwordx4 v[76:79], v[112:113], off nt
	global_load_dwordx4 v[72:75], v[112:113], off offset:1024 nt
	global_load_dwordx4 v[68:71], v[112:113], off offset:2048 nt
	global_load_dwordx4 v[64:67], v[112:113], off offset:3072 nt
	v_addc_co_u32_e32 v81, vcc, 0, v113, vcc
	v_add_co_u32_e32 v96, vcc, 0x2000, v112
	global_load_dwordx4 v[92:95], v[80:81], off nt
	global_load_dwordx4 v[88:91], v[80:81], off offset:1024 nt
	global_load_dwordx4 v[84:87], v[80:81], off offset:2048 nt
	s_nop 0
	global_load_dwordx4 v[80:83], v[80:81], off offset:3072 nt
	v_addc_co_u32_e32 v97, vcc, 0, v113, vcc
	v_add_co_u32_e32 v112, vcc, 0x3000, v112
	global_load_dwordx4 v[108:111], v[96:97], off nt
	global_load_dwordx4 v[104:107], v[96:97], off offset:1024 nt
	global_load_dwordx4 v[100:103], v[96:97], off offset:2048 nt
	s_nop 0
	global_load_dwordx4 v[96:99], v[96:97], off offset:3072 nt
	v_addc_co_u32_e32 v113, vcc, 0, v113, vcc
	global_load_dwordx4 v[124:127], v[112:113], off nt
	global_load_dwordx4 v[120:123], v[112:113], off offset:1024 nt
	global_load_dwordx4 v[116:119], v[112:113], off offset:2048 nt
	s_nop 0
	global_load_dwordx4 v[112:115], v[112:113], off offset:3072 nt
	v_readlane_b32 s46, v252, 38
	v_readlane_b32 s47, v252, 39
	v_readlane_b32 s48, v252, 40
	v_readlane_b32 s49, v252, 41
	v_readlane_b32 s50, v252, 42
	v_readlane_b32 s51, v252, 43
	v_readlane_b32 s52, v252, 44
	v_readlane_b32 s53, v252, 45
	v_readlane_b32 s54, v252, 46
	v_readlane_b32 s55, v252, 47
	v_readlane_b32 s56, v252, 48
	v_readlane_b32 s57, v252, 49
	v_readlane_b32 s58, v252, 50
	v_readlane_b32 s59, v252, 51
.LBB0_181:
	s_waitcnt vmcnt(14)
	v_cvt_pk_bf16_f32 v218, v132, v144
	s_waitcnt vmcnt(12)
	v_cvt_pk_bf16_f32 v219, v128, v136
	s_waitcnt vmcnt(10)
	v_cvt_pk_bf16_f32 v220, v164, v176
	s_waitcnt vmcnt(8)
	v_cvt_pk_bf16_f32 v221, v156, v168
	ds_write_b128 v202, v[218:221]
	s_waitcnt vmcnt(6)
	v_cvt_pk_bf16_f32 v218, v148, v160
	s_waitcnt vmcnt(4)
	v_cvt_pk_bf16_f32 v219, v140, v152
	s_waitcnt vmcnt(2)
	v_cvt_pk_bf16_f32 v220, v180, v188
	s_waitcnt vmcnt(0)
	v_cvt_pk_bf16_f32 v221, v172, v184
	ds_write_b128 v203, v[218:221]
	v_cvt_pk_bf16_f32 v218, v133, v145
	v_cvt_pk_bf16_f32 v219, v129, v137
	v_cvt_pk_bf16_f32 v220, v165, v177
	v_cvt_pk_bf16_f32 v221, v157, v169
	ds_write_b128 v202, v[218:221] offset:128
	v_cvt_pk_bf16_f32 v218, v149, v161
	v_cvt_pk_bf16_f32 v219, v141, v153
	v_cvt_pk_bf16_f32 v220, v181, v189
	v_cvt_pk_bf16_f32 v221, v173, v185
	ds_write_b128 v203, v[218:221] offset:128
	v_cvt_pk_bf16_f32 v218, v134, v146
	v_cvt_pk_bf16_f32 v219, v130, v138
	v_cvt_pk_bf16_f32 v220, v166, v178
	v_cvt_pk_bf16_f32 v221, v158, v170
	ds_write_b128 v202, v[218:221] offset:256
	v_cvt_pk_bf16_f32 v218, v150, v162
	v_cvt_pk_bf16_f32 v219, v142, v154
	v_cvt_pk_bf16_f32 v220, v182, v190
	v_cvt_pk_bf16_f32 v221, v174, v186
	ds_write_b128 v203, v[218:221] offset:256
	v_cvt_pk_bf16_f32 v128, v135, v147
	v_cvt_pk_bf16_f32 v129, v131, v139
	v_cvt_pk_bf16_f32 v130, v167, v179
	v_cvt_pk_bf16_f32 v131, v159, v171
	ds_write_b128 v202, v[128:131] offset:384
	v_cvt_pk_bf16_f32 v128, v151, v163
	v_cvt_pk_bf16_f32 v129, v143, v155
	v_cvt_pk_bf16_f32 v130, v183, v191
	v_cvt_pk_bf16_f32 v131, v175, v187
	ds_write_b128 v203, v[128:131] offset:384
	v_add_u32_e32 v128, s16, v201
	v_ashrrev_i32_e32 v129, 31, v128
	v_lshlrev_b64 v[128:129], 11, v[128:129]
	v_lshl_add_u64 v[134:135], s[0:1], 0, v[128:129]
	v_add_u32_e32 v128, v204, v205
	ds_read_b128 v[130:133], v128
	s_ashr_i32 s15, s14, 31
	v_add_u32_e32 v129, v206, v207
	v_lshl_add_u64 v[134:135], s[14:15], 1, v[134:135]
	ds_read_b128 v[138:141], v129
	v_lshl_add_u64 v[146:147], v[134:135], 0, v[194:195]
	ds_read_b128 v[134:137], v128 offset:4096
	s_waitcnt lgkmcnt(2)
	global_store_dwordx4 v[146:147], v[130:133], off nt
	s_nop 1
	v_add_u32_e32 v130, v208, v209
	v_add_co_u32_e32 v132, vcc, s26, v146
	ds_read_b128 v[142:145], v130
	s_nop 0
	v_addc_co_u32_e32 v133, vcc, 0, v147, vcc
	v_add_u32_e32 v131, v210, v211
	s_waitcnt lgkmcnt(2)
	global_store_dwordx4 v[132:133], v[138:141], off nt
	ds_read_b128 v[138:141], v131
	v_add_co_u32_e32 v132, vcc, s27, v146
	s_nop 1
	v_addc_co_u32_e32 v133, vcc, 0, v147, vcc
	s_waitcnt lgkmcnt(1)
	global_store_dwordx4 v[132:133], v[142:145], off nt
	v_add_co_u32_e32 v148, vcc, s28, v146
	v_add_u32_e32 v132, v212, v213
	s_nop 0
	v_addc_co_u32_e32 v149, vcc, 0, v147, vcc
	ds_read_b128 v[142:145], v132
	s_waitcnt lgkmcnt(1)
	global_store_dwordx4 v[148:149], v[138:141], off nt
	v_add_u32_e32 v133, v214, v215
	s_nop 0
	v_add_co_u32_e32 v138, vcc, s29, v146
	s_nop 1
	v_addc_co_u32_e32 v139, vcc, 0, v147, vcc
	global_store_dwordx4 v[138:139], v[134:137], off nt
	ds_read_b128 v[136:139], v133
	s_nop 0
	v_add_co_u32_e32 v134, vcc, s30, v146
	s_nop 1
	v_addc_co_u32_e32 v135, vcc, 0, v147, vcc
	s_waitcnt lgkmcnt(1)
	global_store_dwordx4 v[134:135], v[142:145], off nt
	v_add_u32_e32 v134, v216, v217
	ds_read_b128 v[140:143], v134
	v_add_co_u32_e32 v144, vcc, 0x18000, v146
	s_nop 1
	v_addc_co_u32_e32 v145, vcc, 0, v147, vcc
	s_waitcnt lgkmcnt(1)
	global_store_dwordx4 v[144:145], v[136:139], off nt
	s_nop 1
	v_add_co_u32_e32 v136, vcc, 0x1c000, v146
	s_nop 1
	v_addc_co_u32_e32 v137, vcc, 0, v147, vcc
	s_andn2_b64 vcc, exec, s[4:5]
	s_waitcnt lgkmcnt(0)
	global_store_dwordx4 v[136:137], v[140:143], off nt
	s_cbranch_vccz .LBB0_183
	s_andn2_b64 vcc, exec, s[2:3]
	s_cbranch_vccnz .LBB0_176
	s_branch .LBB0_184
.LBB0_183:
	s_ashr_i32 s4, s31, 31
	s_lshr_b32 s4, s4, 26
	s_add_i32 s4, s31, s4
	s_and_b32 s4, s4, 0xffc0
	v_cvt_pk_bf16_f32 v136, v12, v8
	s_sub_i32 s4, s31, s4
	v_cvt_pk_bf16_f32 v137, v4, v0
	v_cvt_pk_bf16_f32 v138, v28, v24
	v_cvt_pk_bf16_f32 v139, v20, v16
	ds_write_b128 v202, v[136:139]
	v_cvt_pk_bf16_f32 v136, v44, v40
	s_bfe_i32 s5, s4, 0x80000
	v_cvt_pk_bf16_f32 v137, v36, v32
	v_cvt_pk_bf16_f32 v138, v60, v56
	v_cvt_pk_bf16_f32 v139, v52, v48
	ds_write_b128 v203, v[136:139]
	v_cvt_pk_bf16_f32 v136, v13, v9
	s_bfe_u32 s5, s5, 0x2000d
	v_cvt_pk_bf16_f32 v137, v5, v1
	v_cvt_pk_bf16_f32 v138, v29, v25
	v_cvt_pk_bf16_f32 v139, v21, v17
	ds_write_b128 v202, v[136:139] offset:128
	v_cvt_pk_bf16_f32 v136, v45, v41
	s_add_i32 s5, s4, s5
	v_cvt_pk_bf16_f32 v137, v37, v33
	v_cvt_pk_bf16_f32 v138, v61, v57
	v_cvt_pk_bf16_f32 v139, v53, v49
	ds_write_b128 v203, v[136:139] offset:128
	v_cvt_pk_bf16_f32 v136, v14, v10
	s_bfe_i32 s14, s5, 0x80000
	v_cvt_pk_bf16_f32 v137, v6, v2
	v_cvt_pk_bf16_f32 v138, v30, v26
	v_cvt_pk_bf16_f32 v139, v22, v18
	ds_write_b128 v202, v[136:139] offset:256
	v_cvt_pk_bf16_f32 v136, v46, v42
	s_and_b32 s5, s5, 0xfc
	v_cvt_pk_bf16_f32 v137, v38, v34
	v_cvt_pk_bf16_f32 v138, v62, v58
	v_cvt_pk_bf16_f32 v139, v54, v50
	ds_write_b128 v203, v[136:139] offset:256
	v_cvt_pk_bf16_f32 v136, v15, v11
	s_sub_i32 s4, s4, s5
	v_cvt_pk_bf16_f32 v137, v7, v3
	v_cvt_pk_bf16_f32 v138, v31, v27
	v_cvt_pk_bf16_f32 v139, v23, v19
	ds_write_b128 v202, v[136:139] offset:384
	v_cvt_pk_bf16_f32 v136, v47, v43
	s_sext_i32_i8 s4, s4
	v_cvt_pk_bf16_f32 v137, v39, v35
	v_cvt_pk_bf16_f32 v138, v63, v59
	v_cvt_pk_bf16_f32 v139, v55, v51
	ds_write_b128 v203, v[136:139] offset:384
	v_lshl_add_u32 v136, s4, 6, v201
	v_ashrrev_i32_e32 v137, 31, v136
	s_sext_i32_i16 s14, s14
	v_lshlrev_b64 v[136:137], 11, v[136:137]
	v_lshl_add_u64 v[140:141], s[0:1], 0, v[136:137]
	s_lshl_b32 s4, s14, 4
	ds_read_b128 v[136:139], v128
	s_andn2_b32 s4, s4, 63
	s_ashr_i32 s5, s4, 31
	v_lshl_add_u64 v[140:141], s[4:5], 1, v[140:141]
	v_lshl_add_u64 v[148:149], v[140:141], 0, v[194:195]
	ds_read_b128 v[140:143], v128 offset:4096
	s_waitcnt lgkmcnt(1)
	global_store_dwordx4 v[148:149], v[136:139], off nt
	ds_read_b128 v[136:139], v129
	ds_read_b128 v[144:147], v130
	v_add_co_u32_e32 v150, vcc, s26, v148
	s_nop 1
	v_addc_co_u32_e32 v151, vcc, 0, v149, vcc
	s_waitcnt lgkmcnt(1)
	global_store_dwordx4 v[150:151], v[136:139], off nt
	s_nop 1
	v_add_co_u32_e32 v136, vcc, s27, v148
	s_nop 1
	v_addc_co_u32_e32 v137, vcc, 0, v149, vcc
	s_waitcnt lgkmcnt(0)
	global_store_dwordx4 v[136:137], v[144:147], off nt
	ds_read_b128 v[136:139], v131
	ds_read_b128 v[144:147], v132
	v_add_co_u32_e32 v150, vcc, s28, v148
	s_nop 1
	v_addc_co_u32_e32 v151, vcc, 0, v149, vcc
	s_waitcnt lgkmcnt(1)
	global_store_dwordx4 v[150:151], v[136:139], off nt
	s_nop 1
	v_add_co_u32_e32 v136, vcc, s29, v148
	s_nop 1
	v_addc_co_u32_e32 v137, vcc, 0, v149, vcc
	global_store_dwordx4 v[136:137], v[140:143], off nt
	v_add_co_u32_e32 v136, vcc, 0x14000, v148
	ds_read_b128 v[140:143], v134
	s_nop 0
	v_addc_co_u32_e32 v137, vcc, 0, v149, vcc
	s_waitcnt lgkmcnt(1)
	global_store_dwordx4 v[136:137], v[144:147], off nt
	ds_read_b128 v[136:139], v133
	s_nop 0
	v_add_co_u32_e32 v144, vcc, 0x18000, v148
	s_nop 1
	v_addc_co_u32_e32 v145, vcc, 0, v149, vcc
	s_waitcnt lgkmcnt(0)
	global_store_dwordx4 v[144:145], v[136:139], off nt
	s_nop 1
	v_add_co_u32_e32 v136, vcc, 0x1c000, v148
	s_nop 1
	v_addc_co_u32_e32 v137, vcc, 0, v149, vcc
	global_store_dwordx4 v[136:137], v[140:143], off nt
	s_andn2_b64 vcc, exec, s[2:3]
	s_cbranch_vccnz .LBB0_176
.LBB0_184:
	s_ashr_i32 s2, s17, 31
	s_lshr_b32 s2, s2, 26
	s_add_i32 s2, s17, s2
	s_and_b32 s2, s2, 0xffc0
	v_cvt_pk_bf16_f32 v136, v76, v72
	s_sub_i32 s2, s17, s2
	v_cvt_pk_bf16_f32 v137, v68, v64
	v_cvt_pk_bf16_f32 v138, v92, v88
	v_cvt_pk_bf16_f32 v139, v84, v80
	ds_write_b128 v202, v[136:139]
	v_cvt_pk_bf16_f32 v136, v108, v104
	s_bfe_i32 s3, s2, 0x80000
	v_cvt_pk_bf16_f32 v137, v100, v96
	v_cvt_pk_bf16_f32 v138, v124, v120
	v_cvt_pk_bf16_f32 v139, v116, v112
	ds_write_b128 v203, v[136:139]
	v_cvt_pk_bf16_f32 v136, v77, v73
	s_bfe_u32 s3, s3, 0x2000d
	v_cvt_pk_bf16_f32 v137, v69, v65
	v_cvt_pk_bf16_f32 v138, v93, v89
	v_cvt_pk_bf16_f32 v139, v85, v81
	ds_write_b128 v202, v[136:139] offset:128
	v_cvt_pk_bf16_f32 v136, v109, v105
	s_add_i32 s3, s2, s3
	v_cvt_pk_bf16_f32 v137, v101, v97
	v_cvt_pk_bf16_f32 v138, v125, v121
	v_cvt_pk_bf16_f32 v139, v117, v113
	ds_write_b128 v203, v[136:139] offset:128
	v_cvt_pk_bf16_f32 v136, v78, v74
	s_bfe_i32 s4, s3, 0x80000
	v_cvt_pk_bf16_f32 v137, v70, v66
	v_cvt_pk_bf16_f32 v138, v94, v90
	v_cvt_pk_bf16_f32 v139, v86, v82
	ds_write_b128 v202, v[136:139] offset:256
	v_cvt_pk_bf16_f32 v136, v110, v106
	s_and_b32 s3, s3, 0xfc
	v_cvt_pk_bf16_f32 v137, v102, v98
	v_cvt_pk_bf16_f32 v138, v126, v122
	v_cvt_pk_bf16_f32 v139, v118, v114
	ds_write_b128 v203, v[136:139] offset:256
	v_cvt_pk_bf16_f32 v136, v79, v75
	s_sub_i32 s2, s2, s3
	v_cvt_pk_bf16_f32 v137, v71, v67
	v_cvt_pk_bf16_f32 v138, v95, v91
	v_cvt_pk_bf16_f32 v139, v87, v83
	ds_write_b128 v202, v[136:139] offset:384
	v_cvt_pk_bf16_f32 v136, v111, v107
	s_sext_i32_i8 s2, s2
	v_cvt_pk_bf16_f32 v137, v103, v99
	v_cvt_pk_bf16_f32 v138, v127, v123
	v_cvt_pk_bf16_f32 v139, v119, v115
	ds_write_b128 v203, v[136:139] offset:384
	v_lshl_add_u32 v136, s2, 6, v201
	v_ashrrev_i32_e32 v137, 31, v136
	s_sext_i32_i16 s4, s4
	v_lshlrev_b64 v[136:137], 11, v[136:137]
	v_lshl_add_u64 v[140:141], s[0:1], 0, v[136:137]
	s_lshl_b32 s2, s4, 4
	ds_read_b128 v[136:139], v128
	s_andn2_b32 s2, s2, 63
	s_ashr_i32 s3, s2, 31
	v_lshl_add_u64 v[140:141], s[2:3], 1, v[140:141]
	v_lshl_add_u64 v[148:149], v[140:141], 0, v[194:195]
	ds_read_b128 v[140:143], v128 offset:4096
	s_waitcnt lgkmcnt(1)
	global_store_dwordx4 v[148:149], v[136:139], off nt
	ds_read_b128 v[136:139], v129
	ds_read_b128 v[144:147], v130
	v_add_co_u32_e32 v128, vcc, s26, v148
	s_nop 1
	v_addc_co_u32_e32 v129, vcc, 0, v149, vcc
	s_waitcnt lgkmcnt(1)
	global_store_dwordx4 v[128:129], v[136:139], off nt
	v_add_co_u32_e32 v128, vcc, s27, v148
	ds_read_b128 v[136:139], v132
	s_nop 0
	v_addc_co_u32_e32 v129, vcc, 0, v149, vcc
	s_waitcnt lgkmcnt(1)
	global_store_dwordx4 v[128:129], v[144:147], off nt
	ds_read_b128 v[128:131], v131
	s_nop 0
	v_add_co_u32_e32 v144, vcc, s28, v148
	s_nop 1
	v_addc_co_u32_e32 v145, vcc, 0, v149, vcc
	s_waitcnt lgkmcnt(0)
	global_store_dwordx4 v[144:145], v[128:131], off nt
	s_nop 1
	v_add_co_u32_e32 v128, vcc, s29, v148
	s_nop 1
	v_addc_co_u32_e32 v129, vcc, 0, v149, vcc
	global_store_dwordx4 v[128:129], v[140:143], off nt
	v_add_co_u32_e32 v128, vcc, 0x14000, v148
	s_nop 1
	v_addc_co_u32_e32 v129, vcc, 0, v149, vcc
	global_store_dwordx4 v[128:129], v[136:139], off nt
	ds_read_b128 v[128:131], v133
	ds_read_b128 v[132:135], v134
	v_add_co_u32_e32 v136, vcc, 0x18000, v148
	s_nop 1
	v_addc_co_u32_e32 v137, vcc, 0, v149, vcc
	s_waitcnt lgkmcnt(1)
	global_store_dwordx4 v[136:137], v[128:131], off nt
	s_nop 1
	v_add_co_u32_e32 v128, vcc, 0x1c000, v148
	s_nop 1
	v_addc_co_u32_e32 v129, vcc, 0, v149, vcc
	s_waitcnt lgkmcnt(0)
	global_store_dwordx4 v[128:129], v[132:135], off nt
	s_branch .LBB0_176

.LBB0_188:
	s_add_i32 s31, s8, s16
	s_cmpk_lt_i32 s31, 0x80
	s_cselect_b64 s[4:5], -1, 0
	s_ashr_i32 s2, s16, 31
	s_lshr_b32 s2, s2, 25
	s_add_i32 s2, s16, s2
	s_and_b32 s2, s2, 0xff80
	s_sub_i32 s2, s16, s2
	s_bfe_i32 s3, s2, 0x80000
	s_bfe_u32 s3, s3, 0x3000c
	s_add_i32 s3, s2, s3
	s_bfe_i32 s14, s3, 0x80000
	s_and_b32 s3, s3, 0xf8
	s_sub_i32 s2, s2, s3
	s_sext_i32_i8 s2, s2
	s_lshl_b32 s15, s2, 6
	s_lshl_b32 s2, s2, 5
	s_and_b32 s3, s15, 0xc0
	s_and_b32 s2, s2, 0xffffff80
	s_or_b32 s30, s2, s3
	s_add_i32 s2, s3, s2
	s_addk_i32 s2, 0x80
	s_sext_i32_i16 s14, s14
	s_cmpk_lt_u32 s3, 0x80
	s_cselect_b32 s2, s30, s2
	s_lshl_b32 s3, s14, 3
	s_and_b32 s14, s3, 0xffffffc0
	v_add_u32_e32 v128, s14, v193
	v_ashrrev_i32_e32 v129, 31, v128
	v_readlane_b32 s40, v252, 36
	v_lshlrev_b64 v[128:129], 11, v[128:129]
	v_readlane_b32 s48, v252, 44
	v_readlane_b32 s49, v252, 45
	s_ashr_i32 s3, s2, 31
	s_cmpk_gt_i32 s31, 0x7f
	v_lshl_add_u64 v[128:129], s[48:49], 0, v[128:129]
	v_lshl_add_u64 v[128:129], s[2:3], 2, v[128:129]
	v_lshl_add_u64 v[184:185], v[128:129], 0, v[198:199]
	v_add_co_u32_e32 v144, vcc, s23, v184
	s_movk_i32 s2, 0x5000
	s_nop 0
	v_addc_co_u32_e32 v145, vcc, 0, v185, vcc
	v_add_co_u32_e32 v146, vcc, s24, v184
	global_load_dwordx4 v[128:131], v[184:185], off nt
	global_load_dwordx4 v[132:135], v[184:185], off offset:2048 nt
	v_addc_co_u32_e32 v147, vcc, 0, v185, vcc
	v_add_co_u32_e32 v148, vcc, s25, v184
	global_load_dwordx4 v[140:143], v[146:147], off offset:-4096 nt
	global_load_dwordx4 v[136:139], v[146:147], off nt
	v_addc_co_u32_e32 v149, vcc, 0, v185, vcc
	v_add_co_u32_e32 v150, vcc, s26, v184
	v_readlane_b32 s41, v252, 37
	s_nop 0
	v_addc_co_u32_e32 v151, vcc, 0, v185, vcc
	v_add_co_u32_e32 v164, vcc, s2, v184
	global_load_dwordx4 v[152:155], v[146:147], off offset:2048 nt
	global_load_dwordx4 v[156:159], v[150:151], off offset:-4096 nt
	global_load_dwordx4 v[180:183], v[144:145], off offset:2048 nt
	global_load_dwordx4 v[168:171], v[148:149], off offset:2048 nt
	s_nop 0
	global_load_dwordx4 v[144:147], v[150:151], off nt
	s_nop 0
	global_load_dwordx4 v[148:151], v[150:151], off offset:2048 nt
	v_addc_co_u32_e32 v165, vcc, 0, v185, vcc
	v_add_co_u32_e32 v176, vcc, 0x6000, v184
	global_load_dwordx4 v[160:163], v[164:165], off nt
	s_nop 0
	global_load_dwordx4 v[164:167], v[164:165], off offset:2048 nt
	v_addc_co_u32_e32 v177, vcc, 0, v185, vcc
	v_add_co_u32_e32 v188, vcc, 0x7000, v184
	global_load_dwordx4 v[172:175], v[176:177], off nt
	s_nop 0
	global_load_dwordx4 v[176:179], v[176:177], off offset:2048 nt
	v_addc_co_u32_e32 v189, vcc, 0, v185, vcc
	global_load_dwordx4 v[184:187], v[188:189], off nt
	s_nop 0
	global_load_dwordx4 v[188:191], v[188:189], off offset:2048 nt
	v_readlane_b32 s42, v252, 38
	v_readlane_b32 s43, v252, 39
	v_readlane_b32 s44, v252, 40
	v_readlane_b32 s45, v252, 41
	v_readlane_b32 s46, v252, 42
	v_readlane_b32 s47, v252, 43
	v_readlane_b32 s50, v252, 46
	v_readlane_b32 s51, v252, 47
	v_readlane_b32 s52, v252, 48
	v_readlane_b32 s53, v252, 49
	v_readlane_b32 s54, v252, 50
	v_readlane_b32 s55, v252, 51
	s_cbranch_scc1 .LBB0_190
	s_ashr_i32 s2, s31, 31
	s_lshr_b32 s2, s2, 25
	s_add_i32 s2, s31, s2
	s_and_b32 s2, s2, 0xff80
	s_sub_i32 s2, s31, s2
	s_bfe_i32 s3, s2, 0x80000
	s_bfe_u32 s3, s3, 0x3000c
	s_add_i32 s3, s2, s3
	s_bfe_i32 s30, s3, 0x80000
	s_and_b32 s3, s3, 0xf8
	s_sub_i32 s2, s2, s3
	s_sext_i32_i8 s3, s2
	s_lshl_b32 s2, s2, 6
	s_lshl_b32 s3, s3, 5
	s_and_b32 s2, s2, 0xc0
	s_and_b32 s3, s3, 0xffffff80
	s_or_b32 s35, s3, s2
	s_add_i32 s3, s2, s3
	s_addk_i32 s3, 0x80
	s_sext_i32_i16 s30, s30
	s_cmpk_lt_u32 s2, 0x80
	s_cselect_b32 s2, s35, s3
	s_lshl_b32 s3, s30, 3
	s_andn2_b32 s3, s3, 63
	v_add_u32_e32 v0, s3, v193
	v_ashrrev_i32_e32 v1, 31, v0
	v_readlane_b32 s40, v252, 36
	v_lshlrev_b64 v[0:1], 11, v[0:1]
	v_readlane_b32 s48, v252, 44
	v_readlane_b32 s49, v252, 45
	s_ashr_i32 s3, s2, 31
	v_mov_b32_e32 v197, v195
	v_lshl_add_u64 v[0:1], s[48:49], 0, v[0:1]
	v_lshl_add_u64 v[0:1], s[2:3], 2, v[0:1]
	v_lshl_add_u64 v[72:73], v[0:1], 0, v[196:197]
	v_add_co_u32_e32 v32, vcc, s23, v72
	global_load_dwordx4 v[4:7], v[72:73], off nt
	global_load_dwordx4 v[0:3], v[72:73], off offset:2048 nt
	v_addc_co_u32_e32 v33, vcc, 0, v73, vcc
	v_add_co_u32_e32 v24, vcc, s24, v72
	v_readlane_b32 s41, v252, 37
	s_nop 0
	v_addc_co_u32_e32 v25, vcc, 0, v73, vcc
	v_add_co_u32_e32 v34, vcc, s25, v72
	global_load_dwordx4 v[12:15], v[24:25], off offset:-4096 nt
	global_load_dwordx4 v[8:11], v[24:25], off nt
	v_addc_co_u32_e32 v35, vcc, 0, v73, vcc
	v_add_co_u32_e32 v56, vcc, s26, v72
	v_readlane_b32 s42, v252, 38
	s_nop 0
	v_addc_co_u32_e32 v57, vcc, 0, v73, vcc
	global_load_dwordx4 v[24:27], v[24:25], off offset:2048 nt
	s_nop 0
	global_load_dwordx4 v[28:31], v[56:57], off offset:-4096 nt
	global_load_dwordx4 v[44:47], v[32:33], off offset:2048 nt
	global_load_dwordx4 v[40:43], v[34:35], off offset:2048 nt
	global_load_dwordx4 v[36:39], v[56:57], off nt
	s_nop 0
	global_load_dwordx4 v[32:35], v[56:57], off offset:2048 nt
	v_add_co_u32_e32 v56, vcc, 0x5000, v72
	v_readlane_b32 s43, v252, 39
	s_nop 0
	v_addc_co_u32_e32 v57, vcc, 0, v73, vcc
	v_add_co_u32_e32 v64, vcc, 0x6000, v72
	global_load_dwordx4 v[60:63], v[56:57], off nt
	s_nop 0
	global_load_dwordx4 v[56:59], v[56:57], off offset:2048 nt
	v_addc_co_u32_e32 v65, vcc, 0, v73, vcc
	v_add_co_u32_e32 v72, vcc, 0x7000, v72
	global_load_dwordx4 v[68:71], v[64:65], off nt
	s_nop 0
	global_load_dwordx4 v[64:67], v[64:65], off offset:2048 nt
	v_addc_co_u32_e32 v73, vcc, 0, v73, vcc
	global_load_dwordx4 v[76:79], v[72:73], off nt
	s_nop 0
	global_load_dwordx4 v[72:75], v[72:73], off offset:2048 nt
	v_readlane_b32 s44, v252, 40
	v_readlane_b32 s45, v252, 41
	v_readlane_b32 s46, v252, 42
	v_readlane_b32 s47, v252, 43
	v_readlane_b32 s50, v252, 46
	v_readlane_b32 s51, v252, 47
	v_readlane_b32 s52, v252, 48
	v_readlane_b32 s53, v252, 49
	v_readlane_b32 s54, v252, 50
	v_readlane_b32 s55, v252, 51
.LBB0_190:
	s_add_i32 s30, s17, s16
	s_cmpk_lt_i32 s30, 0x80
	s_cselect_b64 s[2:3], -1, 0
	s_cmpk_gt_i32 s30, 0x7f
	s_cbranch_scc1 .LBB0_192
	s_ashr_i32 s35, s30, 31
	s_lshr_b32 s35, s35, 25
	s_add_i32 s35, s30, s35
	s_and_b32 s35, s35, 0xff80
	s_sub_i32 s35, s30, s35
	s_bfe_i32 s39, s35, 0x80000
	s_bfe_u32 s39, s39, 0x3000c
	s_add_i32 s39, s35, s39
	s_bfe_i32 s40, s39, 0x80000
	s_and_b32 s39, s39, 0xf8
	s_sub_i32 s35, s35, s39
	s_sext_i32_i8 s39, s35
	s_lshl_b32 s35, s35, 6
	s_lshl_b32 s39, s39, 5
	s_and_b32 s35, s35, 0xc0
	s_and_b32 s39, s39, 0xffffff80
	s_sext_i32_i16 s41, s40
	s_or_b32 s40, s39, s35
	s_add_i32 s39, s35, s39
	s_addk_i32 s39, 0x80
	s_cmpk_lt_u32 s35, 0x80
	s_cselect_b32 s40, s40, s39
	s_lshl_b32 s35, s41, 3
	s_andn2_b32 s35, s35, 63
	v_add_u32_e32 v16, s35, v193
	v_ashrrev_i32_e32 v17, 31, v16
	v_readlane_b32 s44, v252, 36
	v_lshlrev_b64 v[16:17], 11, v[16:17]
	v_readlane_b32 s52, v252, 44
	v_readlane_b32 s53, v252, 45
	s_ashr_i32 s41, s40, 31
	v_mov_b32_e32 v197, v195
	v_lshl_add_u64 v[16:17], s[52:53], 0, v[16:17]
	v_lshl_add_u64 v[16:17], s[40:41], 2, v[16:17]
	v_lshl_add_u64 v[120:121], v[16:17], 0, v[196:197]
	v_add_co_u32_e32 v88, vcc, s23, v120
	global_load_dwordx4 v[20:23], v[120:121], off nt
	global_load_dwordx4 v[16:19], v[120:121], off offset:2048 nt
	v_addc_co_u32_e32 v89, vcc, 0, v121, vcc
	v_add_co_u32_e32 v80, vcc, s24, v120
	v_readlane_b32 s45, v252, 37
	s_nop 0
	v_addc_co_u32_e32 v81, vcc, 0, v121, vcc
	v_add_co_u32_e32 v90, vcc, s25, v120
	global_load_dwordx4 v[52:55], v[80:81], off offset:-4096 nt
	global_load_dwordx4 v[48:51], v[80:81], off nt
	v_addc_co_u32_e32 v91, vcc, 0, v121, vcc
	v_add_co_u32_e32 v104, vcc, s26, v120
	v_readlane_b32 s46, v252, 38
	s_nop 0
	v_addc_co_u32_e32 v105, vcc, 0, v121, vcc
	global_load_dwordx4 v[80:83], v[80:81], off offset:2048 nt
	s_nop 0
	global_load_dwordx4 v[84:87], v[104:105], off offset:-4096 nt
	global_load_dwordx4 v[100:103], v[88:89], off offset:2048 nt
	global_load_dwordx4 v[96:99], v[90:91], off offset:2048 nt
	global_load_dwordx4 v[92:95], v[104:105], off nt
	s_nop 0
	global_load_dwordx4 v[88:91], v[104:105], off offset:2048 nt
	v_add_co_u32_e32 v104, vcc, 0x5000, v120
	v_readlane_b32 s47, v252, 39
	s_nop 0
	v_addc_co_u32_e32 v105, vcc, 0, v121, vcc
	v_add_co_u32_e32 v112, vcc, 0x6000, v120
	global_load_dwordx4 v[108:111], v[104:105], off nt
	s_nop 0
	global_load_dwordx4 v[104:107], v[104:105], off offset:2048 nt
	v_addc_co_u32_e32 v113, vcc, 0, v121, vcc
	v_add_co_u32_e32 v120, vcc, 0x7000, v120
	global_load_dwordx4 v[116:119], v[112:113], off nt
	s_nop 0
	global_load_dwordx4 v[112:115], v[112:113], off offset:2048 nt
	v_addc_co_u32_e32 v121, vcc, 0, v121, vcc
	global_load_dwordx4 v[124:127], v[120:121], off nt
	s_nop 0
	global_load_dwordx4 v[120:123], v[120:121], off offset:2048 nt
	v_readlane_b32 s48, v252, 40
	v_readlane_b32 s49, v252, 41
	v_readlane_b32 s50, v252, 42
	v_readlane_b32 s51, v252, 43
	v_readlane_b32 s54, v252, 46
	v_readlane_b32 s55, v252, 47
	v_readlane_b32 s56, v252, 48
	v_readlane_b32 s57, v252, 49
	v_readlane_b32 s58, v252, 50
	v_readlane_b32 s59, v252, 51
.LBB0_192:
	s_waitcnt vmcnt(14)
	v_cvt_pk_bf16_f32 v218, v128, v132
	s_waitcnt vmcnt(9)
	v_cvt_pk_bf16_f32 v219, v140, v180
	v_cvt_pk_bf16_f32 v220, v136, v152
	s_waitcnt vmcnt(8)
	v_cvt_pk_bf16_f32 v221, v156, v168
	ds_write_b128 v202, v[218:221]
	s_waitcnt vmcnt(6)
	v_cvt_pk_bf16_f32 v218, v144, v148
	s_waitcnt vmcnt(4)
	v_cvt_pk_bf16_f32 v219, v160, v164
	s_waitcnt vmcnt(2)
	v_cvt_pk_bf16_f32 v220, v172, v176
	s_waitcnt vmcnt(0)
	v_cvt_pk_bf16_f32 v221, v184, v188
	ds_write_b128 v203, v[218:221]
	v_cvt_pk_bf16_f32 v218, v129, v133
	v_cvt_pk_bf16_f32 v219, v141, v181
	v_cvt_pk_bf16_f32 v220, v137, v153
	v_cvt_pk_bf16_f32 v221, v157, v169
	ds_write_b128 v202, v[218:221] offset:128
	v_cvt_pk_bf16_f32 v218, v145, v149
	v_cvt_pk_bf16_f32 v219, v161, v165
	v_cvt_pk_bf16_f32 v220, v173, v177
	v_cvt_pk_bf16_f32 v221, v185, v189
	ds_write_b128 v203, v[218:221] offset:128
	v_cvt_pk_bf16_f32 v218, v130, v134
	v_cvt_pk_bf16_f32 v219, v142, v182
	v_cvt_pk_bf16_f32 v220, v138, v154
	v_cvt_pk_bf16_f32 v221, v158, v170
	ds_write_b128 v202, v[218:221] offset:256
	v_cvt_pk_bf16_f32 v218, v146, v150
	v_cvt_pk_bf16_f32 v219, v162, v166
	v_cvt_pk_bf16_f32 v220, v174, v178
	v_cvt_pk_bf16_f32 v221, v186, v190
	ds_write_b128 v203, v[218:221] offset:256
	v_cvt_pk_bf16_f32 v128, v131, v135
	v_cvt_pk_bf16_f32 v129, v143, v183
	v_cvt_pk_bf16_f32 v130, v139, v155
	v_cvt_pk_bf16_f32 v131, v159, v171
	ds_write_b128 v202, v[128:131] offset:384
	v_cvt_pk_bf16_f32 v128, v147, v151
	v_cvt_pk_bf16_f32 v129, v163, v167
	v_cvt_pk_bf16_f32 v130, v175, v179
	v_cvt_pk_bf16_f32 v131, v187, v191
	ds_write_b128 v203, v[128:131] offset:384
	v_add_u32_e32 v128, s15, v201
	v_ashrrev_i32_e32 v129, 31, v128
	v_lshlrev_b64 v[128:129], 11, v[128:129]
	v_lshl_add_u64 v[134:135], s[0:1], 0, v[128:129]
	v_add_u32_e32 v128, v204, v205
	ds_read_b128 v[130:133], v128
	s_ashr_i32 s15, s14, 31
	v_add_u32_e32 v129, v206, v207
	v_lshl_add_u64 v[134:135], s[14:15], 1, v[134:135]
	ds_read_b128 v[138:141], v129
	v_lshl_add_u64 v[146:147], v[134:135], 0, v[194:195]
	ds_read_b128 v[134:137], v128 offset:4096
	s_waitcnt lgkmcnt(2)
	global_store_dwordx4 v[146:147], v[130:133], off nt
	s_mov_b32 s14, 0x14000
	s_nop 0
	v_add_u32_e32 v130, v208, v209
	v_add_co_u32_e32 v132, vcc, s26, v146
	ds_read_b128 v[142:145], v130
	s_nop 0
	v_addc_co_u32_e32 v133, vcc, 0, v147, vcc
	v_add_u32_e32 v131, v210, v211
	s_waitcnt lgkmcnt(2)
	global_store_dwordx4 v[132:133], v[138:141], off nt
	ds_read_b128 v[138:141], v131
	v_add_co_u32_e32 v132, vcc, s27, v146
	s_nop 1
	v_addc_co_u32_e32 v133, vcc, 0, v147, vcc
	s_waitcnt lgkmcnt(1)
	global_store_dwordx4 v[132:133], v[142:145], off nt
	v_add_co_u32_e32 v148, vcc, s28, v146
	v_add_u32_e32 v132, v212, v213
	s_nop 0
	v_addc_co_u32_e32 v149, vcc, 0, v147, vcc
	ds_read_b128 v[142:145], v132
	s_waitcnt lgkmcnt(1)
	global_store_dwordx4 v[148:149], v[138:141], off nt
	v_add_u32_e32 v133, v214, v215
	s_nop 0
	v_add_co_u32_e32 v138, vcc, s29, v146
	s_nop 1
	v_addc_co_u32_e32 v139, vcc, 0, v147, vcc
	global_store_dwordx4 v[138:139], v[134:137], off nt
	ds_read_b128 v[136:139], v133
	s_nop 0
	v_add_co_u32_e32 v134, vcc, s14, v146
	s_nop 1
	v_addc_co_u32_e32 v135, vcc, 0, v147, vcc
	s_waitcnt lgkmcnt(1)
	global_store_dwordx4 v[134:135], v[142:145], off nt
	v_add_u32_e32 v134, v216, v217
	ds_read_b128 v[140:143], v134
	v_add_co_u32_e32 v144, vcc, 0x18000, v146
	s_nop 1
	v_addc_co_u32_e32 v145, vcc, 0, v147, vcc
	s_waitcnt lgkmcnt(1)
	global_store_dwordx4 v[144:145], v[136:139], off nt
	s_nop 1
	v_add_co_u32_e32 v136, vcc, 0x1c000, v146
	s_nop 1
	v_addc_co_u32_e32 v137, vcc, 0, v147, vcc
	s_andn2_b64 vcc, exec, s[4:5]
	s_waitcnt lgkmcnt(0)
	global_store_dwordx4 v[136:137], v[140:143], off nt
	s_cbranch_vccz .LBB0_194
	s_andn2_b64 vcc, exec, s[2:3]
	s_cbranch_vccnz .LBB0_187
	s_branch .LBB0_195
.LBB0_194:
	s_ashr_i32 s4, s31, 31
	s_lshr_b32 s4, s4, 25
	s_add_i32 s4, s31, s4
	s_and_b32 s4, s4, 0xff80
	v_cvt_pk_bf16_f32 v136, v4, v0
	s_sub_i32 s4, s31, s4
	v_cvt_pk_bf16_f32 v137, v12, v44
	v_cvt_pk_bf16_f32 v138, v8, v24
	v_cvt_pk_bf16_f32 v139, v28, v40
	ds_write_b128 v202, v[136:139]
	v_cvt_pk_bf16_f32 v136, v36, v32
	s_bfe_i32 s5, s4, 0x80000
	v_cvt_pk_bf16_f32 v137, v60, v56
	v_cvt_pk_bf16_f32 v138, v68, v64
	v_cvt_pk_bf16_f32 v139, v76, v72
	ds_write_b128 v203, v[136:139]
	v_cvt_pk_bf16_f32 v136, v5, v1
	s_bfe_u32 s5, s5, 0x3000c
	v_cvt_pk_bf16_f32 v137, v13, v45
	v_cvt_pk_bf16_f32 v138, v9, v25
	v_cvt_pk_bf16_f32 v139, v29, v41
	ds_write_b128 v202, v[136:139] offset:128
	v_cvt_pk_bf16_f32 v136, v37, v33
	s_add_i32 s5, s4, s5
	v_cvt_pk_bf16_f32 v137, v61, v57
	v_cvt_pk_bf16_f32 v138, v69, v65
	v_cvt_pk_bf16_f32 v139, v77, v73
	ds_write_b128 v203, v[136:139] offset:128
	v_cvt_pk_bf16_f32 v136, v6, v2
	s_bfe_i32 s14, s5, 0x80000
	s_and_b32 s5, s5, 0xf8
	v_cvt_pk_bf16_f32 v137, v14, v46
	v_cvt_pk_bf16_f32 v138, v10, v26
	v_cvt_pk_bf16_f32 v139, v30, v42
	ds_write_b128 v202, v[136:139] offset:256
	v_cvt_pk_bf16_f32 v136, v38, v34
	s_sub_i32 s4, s4, s5
	v_cvt_pk_bf16_f32 v137, v62, v58
	v_cvt_pk_bf16_f32 v138, v70, v66
	v_cvt_pk_bf16_f32 v139, v78, v74
	ds_write_b128 v203, v[136:139] offset:256
	v_cvt_pk_bf16_f32 v136, v7, v3
	v_cvt_pk_bf16_f32 v137, v15, v47
	v_cvt_pk_bf16_f32 v138, v11, v27
	v_cvt_pk_bf16_f32 v139, v31, v43
	ds_write_b128 v202, v[136:139] offset:384
	v_cvt_pk_bf16_f32 v136, v39, v35
	s_sext_i32_i8 s4, s4
	v_cvt_pk_bf16_f32 v137, v63, v59
	v_cvt_pk_bf16_f32 v138, v71, v67
	v_cvt_pk_bf16_f32 v139, v79, v75
	ds_write_b128 v203, v[136:139] offset:384
	v_lshl_add_u32 v136, s4, 6, v201
	v_ashrrev_i32_e32 v137, 31, v136
	s_sext_i32_i16 s14, s14
	v_lshlrev_b64 v[136:137], 11, v[136:137]
	v_lshl_add_u64 v[140:141], s[0:1], 0, v[136:137]
	s_lshl_b32 s4, s14, 3
	ds_read_b128 v[136:139], v128
	s_andn2_b32 s4, s4, 63
	s_ashr_i32 s5, s4, 31
	v_lshl_add_u64 v[140:141], s[4:5], 1, v[140:141]
	v_lshl_add_u64 v[148:149], v[140:141], 0, v[194:195]
	ds_read_b128 v[140:143], v128 offset:4096
	s_waitcnt lgkmcnt(1)
	global_store_dwordx4 v[148:149], v[136:139], off nt
	ds_read_b128 v[136:139], v129
	ds_read_b128 v[144:147], v130
	v_add_co_u32_e32 v150, vcc, s26, v148
	s_nop 1
	v_addc_co_u32_e32 v151, vcc, 0, v149, vcc
	s_waitcnt lgkmcnt(1)
	global_store_dwordx4 v[150:151], v[136:139], off nt
	s_nop 1
	v_add_co_u32_e32 v136, vcc, s27, v148
	s_nop 1
	v_addc_co_u32_e32 v137, vcc, 0, v149, vcc
	s_waitcnt lgkmcnt(0)
	global_store_dwordx4 v[136:137], v[144:147], off nt
	ds_read_b128 v[136:139], v131
	ds_read_b128 v[144:147], v132
	v_add_co_u32_e32 v150, vcc, s28, v148
	s_nop 1
	v_addc_co_u32_e32 v151, vcc, 0, v149, vcc
	s_waitcnt lgkmcnt(1)
	global_store_dwordx4 v[150:151], v[136:139], off nt
	s_nop 1
	v_add_co_u32_e32 v136, vcc, s29, v148
	s_nop 1
	v_addc_co_u32_e32 v137, vcc, 0, v149, vcc
	global_store_dwordx4 v[136:137], v[140:143], off nt
	v_add_co_u32_e32 v136, vcc, 0x14000, v148
	ds_read_b128 v[140:143], v134
	s_nop 0
	v_addc_co_u32_e32 v137, vcc, 0, v149, vcc
	s_waitcnt lgkmcnt(1)
	global_store_dwordx4 v[136:137], v[144:147], off nt
	ds_read_b128 v[136:139], v133
	s_nop 0
	v_add_co_u32_e32 v144, vcc, 0x18000, v148
	s_nop 1
	v_addc_co_u32_e32 v145, vcc, 0, v149, vcc
	s_waitcnt lgkmcnt(0)
	global_store_dwordx4 v[144:145], v[136:139], off nt
	s_nop 1
	v_add_co_u32_e32 v136, vcc, 0x1c000, v148
	s_nop 1
	v_addc_co_u32_e32 v137, vcc, 0, v149, vcc
	global_store_dwordx4 v[136:137], v[140:143], off nt
	s_andn2_b64 vcc, exec, s[2:3]
	s_cbranch_vccnz .LBB0_187
.LBB0_195:
	s_ashr_i32 s2, s30, 31
	s_lshr_b32 s2, s2, 25
	s_add_i32 s2, s30, s2
	s_and_b32 s2, s2, 0xff80
	v_cvt_pk_bf16_f32 v136, v20, v16
	s_sub_i32 s2, s30, s2
	v_cvt_pk_bf16_f32 v137, v52, v100
	v_cvt_pk_bf16_f32 v138, v48, v80
	v_cvt_pk_bf16_f32 v139, v84, v96
	ds_write_b128 v202, v[136:139]
	v_cvt_pk_bf16_f32 v136, v92, v88
	s_bfe_i32 s3, s2, 0x80000
	v_cvt_pk_bf16_f32 v137, v108, v104
	v_cvt_pk_bf16_f32 v138, v116, v112
	v_cvt_pk_bf16_f32 v139, v124, v120
	ds_write_b128 v203, v[136:139]
	v_cvt_pk_bf16_f32 v136, v21, v17
	s_bfe_u32 s3, s3, 0x3000c
	v_cvt_pk_bf16_f32 v137, v53, v101
	v_cvt_pk_bf16_f32 v138, v49, v81
	v_cvt_pk_bf16_f32 v139, v85, v97
	ds_write_b128 v202, v[136:139] offset:128
	v_cvt_pk_bf16_f32 v136, v93, v89
	s_add_i32 s3, s2, s3
	v_cvt_pk_bf16_f32 v137, v109, v105
	v_cvt_pk_bf16_f32 v138, v117, v113
	v_cvt_pk_bf16_f32 v139, v125, v121
	ds_write_b128 v203, v[136:139] offset:128
	v_cvt_pk_bf16_f32 v136, v22, v18
	s_bfe_i32 s4, s3, 0x80000
	s_and_b32 s3, s3, 0xf8
	v_cvt_pk_bf16_f32 v137, v54, v102
	v_cvt_pk_bf16_f32 v138, v50, v82
	v_cvt_pk_bf16_f32 v139, v86, v98
	ds_write_b128 v202, v[136:139] offset:256
	v_cvt_pk_bf16_f32 v136, v94, v90
	s_sub_i32 s2, s2, s3
	v_cvt_pk_bf16_f32 v137, v110, v106
	v_cvt_pk_bf16_f32 v138, v118, v114
	v_cvt_pk_bf16_f32 v139, v126, v122
	ds_write_b128 v203, v[136:139] offset:256
	v_cvt_pk_bf16_f32 v136, v23, v19
	v_cvt_pk_bf16_f32 v137, v55, v103
	v_cvt_pk_bf16_f32 v138, v51, v83
	v_cvt_pk_bf16_f32 v139, v87, v99
	ds_write_b128 v202, v[136:139] offset:384
	v_cvt_pk_bf16_f32 v136, v95, v91
	s_sext_i32_i8 s2, s2
	v_cvt_pk_bf16_f32 v137, v111, v107
	v_cvt_pk_bf16_f32 v138, v119, v115
	v_cvt_pk_bf16_f32 v139, v127, v123
	ds_write_b128 v203, v[136:139] offset:384
	v_lshl_add_u32 v136, s2, 6, v201
	v_ashrrev_i32_e32 v137, 31, v136
	s_sext_i32_i16 s4, s4
	v_lshlrev_b64 v[136:137], 11, v[136:137]
	v_lshl_add_u64 v[140:141], s[0:1], 0, v[136:137]
	s_lshl_b32 s2, s4, 3
	ds_read_b128 v[136:139], v128
	s_andn2_b32 s2, s2, 63
	s_ashr_i32 s3, s2, 31
	v_lshl_add_u64 v[140:141], s[2:3], 1, v[140:141]
	v_lshl_add_u64 v[148:149], v[140:141], 0, v[194:195]
	ds_read_b128 v[140:143], v128 offset:4096
	s_waitcnt lgkmcnt(1)
	global_store_dwordx4 v[148:149], v[136:139], off nt
	ds_read_b128 v[136:139], v129
	ds_read_b128 v[144:147], v130
	v_add_co_u32_e32 v128, vcc, s26, v148
	s_nop 1
	v_addc_co_u32_e32 v129, vcc, 0, v149, vcc
	s_waitcnt lgkmcnt(1)
	global_store_dwordx4 v[128:129], v[136:139], off nt
	v_add_co_u32_e32 v128, vcc, s27, v148
	ds_read_b128 v[136:139], v132
	s_nop 0
	v_addc_co_u32_e32 v129, vcc, 0, v149, vcc
	s_waitcnt lgkmcnt(1)
	global_store_dwordx4 v[128:129], v[144:147], off nt
	ds_read_b128 v[128:131], v131
	s_nop 0
	v_add_co_u32_e32 v144, vcc, s28, v148
	s_nop 1
	v_addc_co_u32_e32 v145, vcc, 0, v149, vcc
	s_waitcnt lgkmcnt(0)
	global_store_dwordx4 v[144:145], v[128:131], off nt
	s_nop 1
	v_add_co_u32_e32 v128, vcc, s29, v148
	s_nop 1
	v_addc_co_u32_e32 v129, vcc, 0, v149, vcc
	global_store_dwordx4 v[128:129], v[140:143], off nt
	v_add_co_u32_e32 v128, vcc, 0x14000, v148
	s_nop 1
	v_addc_co_u32_e32 v129, vcc, 0, v149, vcc
	global_store_dwordx4 v[128:129], v[136:139], off nt
	ds_read_b128 v[128:131], v133
	ds_read_b128 v[132:135], v134
	v_add_co_u32_e32 v136, vcc, 0x18000, v148
	s_nop 1
	v_addc_co_u32_e32 v137, vcc, 0, v149, vcc
	s_waitcnt lgkmcnt(1)
	global_store_dwordx4 v[136:137], v[128:131], off nt
	s_nop 1
	v_add_co_u32_e32 v128, vcc, 0x1c000, v148
	s_nop 1
	v_addc_co_u32_e32 v129, vcc, 0, v149, vcc
	s_waitcnt lgkmcnt(0)
	global_store_dwordx4 v[128:129], v[132:135], off nt
	s_branch .LBB0_187

.LBB0_199:
	s_add_i32 s30, s8, s18
	s_cmp_lt_i32 s30, 64
	s_cselect_b64 s[2:3], -1, 0
	s_ashr_i32 s4, s18, 31
	s_lshr_b32 s4, s4, 26
	s_add_i32 s4, s18, s4
	s_and_b32 s4, s4, 0xffc0
	s_sub_i32 s4, s18, s4
	s_bfe_i32 s5, s4, 0x80000
	s_bfe_u32 s5, s5, 0x4000b
	s_add_i32 s5, s4, s5
	s_bfe_i32 s14, s5, 0x80000
	s_and_b32 s5, s5, 0xf0
	s_sub_i32 s4, s4, s5
	s_sext_i32_i16 s14, s14
	s_sext_i32_i8 s4, s4
	s_lshl_b32 s16, s4, 6
	s_lshl_b32 s4, s14, 2
	s_and_b32 s14, s4, 0xffffffc0
	v_add_u32_e32 v128, s14, v193
	v_ashrrev_i32_e32 v129, 31, v128
	v_readlane_b32 s40, v252, 36
	v_lshlrev_b64 v[128:129], 12, v[128:129]
	v_readlane_b32 s50, v252, 46
	v_readlane_b32 s51, v252, 47
	s_ashr_i32 s17, s16, 31
	s_cmp_gt_i32 s30, 63
	v_lshl_add_u64 v[128:129], s[50:51], 0, v[128:129]
	v_lshl_add_u64 v[128:129], s[16:17], 2, v[128:129]
	v_lshl_add_u64 v[180:181], v[128:129], 0, v[198:199]
	v_add_co_u32_e32 v128, vcc, s22, v180
	v_readlane_b32 s41, v252, 37
	s_nop 0
	v_addc_co_u32_e32 v129, vcc, 0, v181, vcc
	v_add_co_u32_e32 v136, vcc, s23, v180
	global_load_dwordx4 v[132:135], v[128:129], off offset:-4096 nt
	s_nop 0
	global_load_dwordx4 v[128:131], v[128:129], off nt
	v_addc_co_u32_e32 v137, vcc, 0, v181, vcc
	v_add_co_u32_e32 v140, vcc, s25, v180
	global_load_dwordx4 v[144:147], v[136:137], off offset:-4096 nt
	s_nop 0
	global_load_dwordx4 v[136:139], v[136:137], off nt
	v_addc_co_u32_e32 v141, vcc, 0, v181, vcc
	global_load_dwordx4 v[152:155], v[140:141], off offset:-4096 nt
	global_load_dwordx4 v[148:151], v[140:141], off nt
	v_add_co_u32_e32 v140, vcc, s26, v180
	v_readlane_b32 s42, v252, 38
	s_nop 0
	v_addc_co_u32_e32 v141, vcc, 0, v181, vcc
	v_add_co_u32_e32 v156, vcc, s27, v180
	global_load_dwordx4 v[164:167], v[140:141], off offset:-4096 nt
	s_nop 0
	global_load_dwordx4 v[140:143], v[140:141], off nt
	v_addc_co_u32_e32 v157, vcc, 0, v181, vcc
	v_add_co_u32_e32 v168, vcc, s29, v180
	global_load_dwordx4 v[160:163], v[156:157], off offset:-4096 nt
	s_nop 0
	global_load_dwordx4 v[156:159], v[156:157], off nt
	v_addc_co_u32_e32 v169, vcc, 0, v181, vcc
	v_add_co_u32_e32 v176, vcc, 0xd000, v180
	global_load_dwordx4 v[172:175], v[168:169], off offset:-4096 nt
	s_nop 0
	global_load_dwordx4 v[168:171], v[168:169], off nt
	v_addc_co_u32_e32 v177, vcc, 0, v181, vcc
	v_add_co_u32_e32 v182, vcc, 0xe000, v180
	global_load_dwordx4 v[188:191], v[180:181], off nt
	s_nop 0
	global_load_dwordx4 v[176:179], v[176:177], off nt
	v_addc_co_u32_e32 v183, vcc, 0, v181, vcc
	v_add_co_u32_e32 v184, vcc, 0xf000, v180
	v_readlane_b32 s43, v252, 39
	s_nop 0
	v_addc_co_u32_e32 v185, vcc, 0, v181, vcc
	global_load_dwordx4 v[180:183], v[182:183], off nt
	s_nop 0
	global_load_dwordx4 v[184:187], v[184:185], off nt
	v_readlane_b32 s44, v252, 40
	v_readlane_b32 s45, v252, 41
	v_readlane_b32 s46, v252, 42
	v_readlane_b32 s47, v252, 43
	v_readlane_b32 s48, v252, 44
	v_readlane_b32 s49, v252, 45
	v_readlane_b32 s52, v252, 48
	v_readlane_b32 s53, v252, 49
	v_readlane_b32 s54, v252, 50
	v_readlane_b32 s55, v252, 51
	s_cbranch_scc1 .LBB0_201
	s_ashr_i32 s4, s30, 31
	s_lshr_b32 s4, s4, 26
	s_add_i32 s4, s30, s4
	s_and_b32 s4, s4, 0xffc0
	s_sub_i32 s4, s30, s4
	s_bfe_i32 s5, s4, 0x80000
	s_bfe_u32 s5, s5, 0x4000b
	s_add_i32 s5, s4, s5
	s_bfe_i32 s15, s5, 0x80000
	s_sext_i32_i16 s15, s15
	s_and_b32 s5, s5, 0xf0
	s_sub_i32 s4, s4, s5
	s_lshl_b32 s5, s15, 2
	s_andn2_b32 s5, s5, 63
	v_add_u32_e32 v0, s5, v193
	s_sext_i32_i8 s4, s4
	v_ashrrev_i32_e32 v1, 31, v0
	v_readlane_b32 s40, v252, 36
	s_lshl_b32 s4, s4, 6
	v_lshlrev_b64 v[0:1], 12, v[0:1]
	v_readlane_b32 s50, v252, 46
	v_readlane_b32 s51, v252, 47
	s_ashr_i32 s5, s4, 31
	v_mov_b32_e32 v197, v195
	v_lshl_add_u64 v[0:1], s[50:51], 0, v[0:1]
	v_lshl_add_u64 v[0:1], s[4:5], 2, v[0:1]
	v_lshl_add_u64 v[100:101], v[0:1], 0, v[196:197]
	v_add_co_u32_e32 v0, vcc, s22, v100
	v_readlane_b32 s41, v252, 37
	s_nop 0
	v_addc_co_u32_e32 v1, vcc, 0, v101, vcc
	v_add_co_u32_e32 v8, vcc, s23, v100
	global_load_dwordx4 v[4:7], v[0:1], off offset:-4096 nt
	s_nop 0
	global_load_dwordx4 v[0:3], v[0:1], off nt
	v_addc_co_u32_e32 v9, vcc, 0, v101, vcc
	v_add_co_u32_e32 v16, vcc, s25, v100
	global_load_dwordx4 v[12:15], v[8:9], off offset:-4096 nt
	s_nop 0
	global_load_dwordx4 v[8:11], v[8:9], off nt
	v_addc_co_u32_e32 v17, vcc, 0, v101, vcc
	v_add_co_u32_e32 v24, vcc, s26, v100
	global_load_dwordx4 v[20:23], v[16:17], off offset:-4096 nt
	s_nop 0
	global_load_dwordx4 v[16:19], v[16:17], off nt
	v_addc_co_u32_e32 v25, vcc, 0, v101, vcc
	v_add_co_u32_e32 v40, vcc, s27, v100
	global_load_dwordx4 v[28:31], v[24:25], off offset:-4096 nt
	s_nop 0
	global_load_dwordx4 v[24:27], v[24:25], off nt
	v_addc_co_u32_e32 v41, vcc, 0, v101, vcc
	v_add_co_u32_e32 v56, vcc, s28, v100
	global_load_dwordx4 v[44:47], v[40:41], off offset:-4096 nt
	s_nop 0
	global_load_dwordx4 v[40:43], v[40:41], off nt
	v_addc_co_u32_e32 v57, vcc, 0, v101, vcc
	v_add_co_u32_e32 v80, vcc, 0xc000, v100
	global_load_dwordx4 v[76:79], v[100:101], off nt
	s_nop 0
	global_load_dwordx4 v[56:59], v[56:57], off nt
	v_addc_co_u32_e32 v81, vcc, 0, v101, vcc
	v_add_co_u32_e32 v92, vcc, 0xd000, v100
	v_readlane_b32 s42, v252, 38
	s_nop 0
	v_addc_co_u32_e32 v93, vcc, 0, v101, vcc
	v_add_co_u32_e32 v102, vcc, 0xe000, v100
	global_load_dwordx4 v[80:83], v[80:81], off nt
	s_nop 0
	global_load_dwordx4 v[92:95], v[92:93], off nt
	v_addc_co_u32_e32 v103, vcc, 0, v101, vcc
	v_add_co_u32_e32 v104, vcc, 0xf000, v100
	v_readlane_b32 s43, v252, 39
	s_nop 0
	v_addc_co_u32_e32 v105, vcc, 0, v101, vcc
	global_load_dwordx4 v[100:103], v[102:103], off nt
	s_nop 0
	global_load_dwordx4 v[104:107], v[104:105], off nt
	v_readlane_b32 s44, v252, 40
	v_readlane_b32 s45, v252, 41
	v_readlane_b32 s46, v252, 42
	v_readlane_b32 s47, v252, 43
	v_readlane_b32 s48, v252, 44
	v_readlane_b32 s49, v252, 45
	v_readlane_b32 s52, v252, 48
	v_readlane_b32 s53, v252, 49
	v_readlane_b32 s54, v252, 50
	v_readlane_b32 s55, v252, 51
.LBB0_201:
	s_add_i32 s17, s19, s18
	s_cmp_lt_i32 s17, 64
	s_cselect_b64 s[4:5], -1, 0
	s_cmp_gt_i32 s17, 63
	s_cbranch_scc1 .LBB0_203
	s_ashr_i32 s15, s17, 31
	s_lshr_b32 s15, s15, 26
	s_add_i32 s15, s17, s15
	s_and_b32 s15, s15, 0xffc0
	s_sub_i32 s15, s17, s15
	s_bfe_i32 s31, s15, 0x80000
	s_bfe_u32 s31, s31, 0x4000b
	s_add_i32 s31, s15, s31
	s_bfe_i32 s35, s31, 0x80000
	s_and_b32 s31, s31, 0xf0
	s_sub_i32 s15, s15, s31
	s_sext_i32_i16 s35, s35
	s_sext_i32_i8 s15, s15
	s_lshl_b32 s40, s15, 6
	s_lshl_b32 s15, s35, 2
	s_andn2_b32 s15, s15, 63
	v_add_u32_e32 v32, s15, v193
	v_ashrrev_i32_e32 v33, 31, v32
	v_readlane_b32 s44, v252, 36
	v_lshlrev_b64 v[32:33], 12, v[32:33]
	v_readlane_b32 s54, v252, 46
	v_readlane_b32 s55, v252, 47
	s_ashr_i32 s41, s40, 31
	v_mov_b32_e32 v197, v195
	v_lshl_add_u64 v[32:33], s[54:55], 0, v[32:33]
	v_lshl_add_u64 v[32:33], s[40:41], 2, v[32:33]
	v_lshl_add_u64 v[120:121], v[32:33], 0, v[196:197]
	v_add_co_u32_e32 v32, vcc, s22, v120
	v_readlane_b32 s45, v252, 37
	s_nop 0
	v_addc_co_u32_e32 v33, vcc, 0, v121, vcc
	v_add_co_u32_e32 v48, vcc, s23, v120
	global_load_dwordx4 v[36:39], v[32:33], off offset:-4096 nt
	s_nop 0
	global_load_dwordx4 v[32:35], v[32:33], off nt
	v_addc_co_u32_e32 v49, vcc, 0, v121, vcc
	v_add_co_u32_e32 v60, vcc, s25, v120
	global_load_dwordx4 v[52:55], v[48:49], off offset:-4096 nt
	s_nop 0
	global_load_dwordx4 v[48:51], v[48:49], off nt
	v_addc_co_u32_e32 v61, vcc, 0, v121, vcc
	v_add_co_u32_e32 v68, vcc, s26, v120
	global_load_dwordx4 v[64:67], v[60:61], off offset:-4096 nt
	s_nop 0
	global_load_dwordx4 v[60:63], v[60:61], off nt
	v_addc_co_u32_e32 v69, vcc, 0, v121, vcc
	v_add_co_u32_e32 v84, vcc, s27, v120
	global_load_dwordx4 v[72:75], v[68:69], off offset:-4096 nt
	s_nop 0
	global_load_dwordx4 v[68:71], v[68:69], off nt
	v_addc_co_u32_e32 v85, vcc, 0, v121, vcc
	v_add_co_u32_e32 v96, vcc, s28, v120
	global_load_dwordx4 v[88:91], v[84:85], off offset:-4096 nt
	s_nop 0
	global_load_dwordx4 v[84:87], v[84:85], off nt
	v_addc_co_u32_e32 v97, vcc, 0, v121, vcc
	v_add_co_u32_e32 v112, vcc, 0xc000, v120
	global_load_dwordx4 v[108:111], v[120:121], off nt
	s_nop 0
	global_load_dwordx4 v[96:99], v[96:97], off nt
	v_addc_co_u32_e32 v113, vcc, 0, v121, vcc
	v_add_co_u32_e32 v116, vcc, 0xd000, v120
	v_readlane_b32 s46, v252, 38
	s_nop 0
	v_addc_co_u32_e32 v117, vcc, 0, v121, vcc
	v_add_co_u32_e32 v122, vcc, 0xe000, v120
	global_load_dwordx4 v[112:115], v[112:113], off nt
	s_nop 0
	global_load_dwordx4 v[116:119], v[116:117], off nt
	v_addc_co_u32_e32 v123, vcc, 0, v121, vcc
	v_add_co_u32_e32 v124, vcc, 0xf000, v120
	v_readlane_b32 s47, v252, 39
	s_nop 0
	v_addc_co_u32_e32 v125, vcc, 0, v121, vcc
	global_load_dwordx4 v[120:123], v[122:123], off nt
	s_nop 0
	global_load_dwordx4 v[124:127], v[124:125], off nt
	v_readlane_b32 s48, v252, 40
	v_readlane_b32 s49, v252, 41
	v_readlane_b32 s50, v252, 42
	v_readlane_b32 s51, v252, 43
	v_readlane_b32 s52, v252, 44
	v_readlane_b32 s53, v252, 45
	v_readlane_b32 s56, v252, 48
	v_readlane_b32 s57, v252, 49
	v_readlane_b32 s58, v252, 50
	v_readlane_b32 s59, v252, 51
.LBB0_203:
	s_waitcnt vmcnt(3)
	v_cvt_pk_bf16_f32 v218, v188, v132
	v_cvt_pk_bf16_f32 v219, v128, v144
	v_cvt_pk_bf16_f32 v220, v136, v152
	v_cvt_pk_bf16_f32 v221, v148, v164
	ds_write_b128 v202, v[218:221]
	v_cvt_pk_bf16_f32 v218, v140, v160
	v_cvt_pk_bf16_f32 v219, v156, v172
	s_waitcnt vmcnt(2)
	v_cvt_pk_bf16_f32 v220, v168, v176
	s_waitcnt vmcnt(0)
	v_cvt_pk_bf16_f32 v221, v180, v184
	ds_write_b128 v203, v[218:221]
	v_cvt_pk_bf16_f32 v218, v189, v133
	v_cvt_pk_bf16_f32 v219, v129, v145
	v_cvt_pk_bf16_f32 v220, v137, v153
	v_cvt_pk_bf16_f32 v221, v149, v165
	ds_write_b128 v202, v[218:221] offset:128
	v_cvt_pk_bf16_f32 v218, v141, v161
	v_cvt_pk_bf16_f32 v219, v157, v173
	v_cvt_pk_bf16_f32 v220, v169, v177
	v_cvt_pk_bf16_f32 v221, v181, v185
	ds_write_b128 v203, v[218:221] offset:128
	v_cvt_pk_bf16_f32 v218, v190, v134
	v_cvt_pk_bf16_f32 v219, v130, v146
	v_cvt_pk_bf16_f32 v220, v138, v154
	v_cvt_pk_bf16_f32 v221, v150, v166
	ds_write_b128 v202, v[218:221] offset:256
	v_cvt_pk_bf16_f32 v218, v142, v162
	v_cvt_pk_bf16_f32 v219, v158, v174
	v_cvt_pk_bf16_f32 v220, v170, v178
	v_cvt_pk_bf16_f32 v221, v182, v186
	ds_write_b128 v203, v[218:221] offset:256
	v_cvt_pk_bf16_f32 v128, v191, v135
	v_cvt_pk_bf16_f32 v129, v131, v147
	v_cvt_pk_bf16_f32 v130, v139, v155
	v_cvt_pk_bf16_f32 v131, v151, v167
	ds_write_b128 v202, v[128:131] offset:384
	v_cvt_pk_bf16_f32 v128, v143, v163
	v_cvt_pk_bf16_f32 v129, v159, v175
	v_cvt_pk_bf16_f32 v130, v171, v179
	v_cvt_pk_bf16_f32 v131, v183, v187
	ds_write_b128 v203, v[128:131] offset:384
	v_add_u32_e32 v128, s16, v201
	v_ashrrev_i32_e32 v129, 31, v128
	v_lshlrev_b64 v[128:129], 9, v[128:129]
	v_lshl_add_u64 v[134:135], s[0:1], 0, v[128:129]
	v_add_u32_e32 v128, v204, v205
	ds_read_b128 v[130:133], v128
	s_ashr_i32 s15, s14, 31
	v_lshl_add_u64 v[134:135], s[14:15], 1, v[134:135]
	v_lshl_add_u64 v[146:147], v[134:135], 0, v[194:195]
	ds_read_b128 v[134:137], v128 offset:4096
	s_waitcnt lgkmcnt(1)
	global_store_dwordx4 v[146:147], v[130:133], off nt
	v_add_u32_e32 v129, v206, v207
	s_nop 0
	v_add_u32_e32 v130, v208, v209
	ds_read_b128 v[138:141], v129
	ds_read_b128 v[142:145], v130
	v_add_co_u32_e32 v132, vcc, s22, v146
	v_add_u32_e32 v131, v210, v211
	s_nop 0
	v_addc_co_u32_e32 v133, vcc, 0, v147, vcc
	s_waitcnt lgkmcnt(1)
	global_store_dwordx4 v[132:133], v[138:141], off offset:-4096 nt
	s_waitcnt lgkmcnt(0)
	global_store_dwordx4 v[132:133], v[142:145], off nt
	ds_read_b128 v[138:141], v131
	v_add_u32_e32 v132, v212, v213
	v_add_co_u32_e32 v148, vcc, s23, v146
	ds_read_b128 v[142:145], v132
	s_nop 0
	v_addc_co_u32_e32 v149, vcc, 0, v147, vcc
	s_waitcnt lgkmcnt(1)
	global_store_dwordx4 v[148:149], v[138:141], off offset:-4096 nt
	global_store_dwordx4 v[148:149], v[134:137], off nt
	v_add_u32_e32 v133, v214, v215
	ds_read_b128 v[136:139], v133
	v_add_co_u32_e32 v134, vcc, s24, v146
	s_nop 1
	v_addc_co_u32_e32 v135, vcc, 0, v147, vcc
	s_waitcnt lgkmcnt(1)
	global_store_dwordx4 v[134:135], v[142:145], off nt
	v_add_u32_e32 v134, v216, v217
	ds_read_b128 v[140:143], v134
	v_add_co_u32_e32 v144, vcc, 0x6000, v146
	s_nop 1
	v_addc_co_u32_e32 v145, vcc, 0, v147, vcc
	s_waitcnt lgkmcnt(1)
	global_store_dwordx4 v[144:145], v[136:139], off nt
	s_nop 1
	v_add_co_u32_e32 v136, vcc, 0x7000, v146
	s_nop 1
	v_addc_co_u32_e32 v137, vcc, 0, v147, vcc
	s_andn2_b64 vcc, exec, s[2:3]
	s_waitcnt lgkmcnt(0)
	global_store_dwordx4 v[136:137], v[140:143], off nt
	s_cbranch_vccz .LBB0_205
	s_andn2_b64 vcc, exec, s[4:5]
	s_cbranch_vccnz .LBB0_198
	s_branch .LBB0_206
.LBB0_205:
	s_ashr_i32 s2, s30, 31
	s_lshr_b32 s2, s2, 26
	s_add_i32 s2, s30, s2
	s_and_b32 s2, s2, 0xffc0
	v_cvt_pk_bf16_f32 v136, v76, v4
	s_sub_i32 s2, s30, s2
	v_cvt_pk_bf16_f32 v137, v0, v12
	v_cvt_pk_bf16_f32 v138, v8, v20
	v_cvt_pk_bf16_f32 v139, v16, v28
	ds_write_b128 v202, v[136:139]
	v_cvt_pk_bf16_f32 v136, v24, v44
	s_bfe_i32 s3, s2, 0x80000
	v_cvt_pk_bf16_f32 v137, v40, v56
	v_cvt_pk_bf16_f32 v138, v80, v92
	v_cvt_pk_bf16_f32 v139, v100, v104
	ds_write_b128 v203, v[136:139]
	v_cvt_pk_bf16_f32 v136, v77, v5
	s_bfe_u32 s3, s3, 0x4000b
	v_cvt_pk_bf16_f32 v137, v1, v13
	v_cvt_pk_bf16_f32 v138, v9, v21
	v_cvt_pk_bf16_f32 v139, v17, v29
	ds_write_b128 v202, v[136:139] offset:128
	v_cvt_pk_bf16_f32 v136, v25, v45
	s_add_i32 s3, s2, s3
	v_cvt_pk_bf16_f32 v137, v41, v57
	v_cvt_pk_bf16_f32 v138, v81, v93
	v_cvt_pk_bf16_f32 v139, v101, v105
	ds_write_b128 v203, v[136:139] offset:128
	v_cvt_pk_bf16_f32 v136, v78, v6
	s_bfe_i32 s14, s3, 0x80000
	v_cvt_pk_bf16_f32 v137, v2, v14
	v_cvt_pk_bf16_f32 v138, v10, v22
	v_cvt_pk_bf16_f32 v139, v18, v30
	ds_write_b128 v202, v[136:139] offset:256
	v_cvt_pk_bf16_f32 v136, v26, v46
	s_and_b32 s3, s3, 0xf0
	v_cvt_pk_bf16_f32 v137, v42, v58
	v_cvt_pk_bf16_f32 v138, v82, v94
	v_cvt_pk_bf16_f32 v139, v102, v106
	ds_write_b128 v203, v[136:139] offset:256
	v_cvt_pk_bf16_f32 v136, v79, v7
	s_sub_i32 s2, s2, s3
	v_cvt_pk_bf16_f32 v137, v3, v15
	v_cvt_pk_bf16_f32 v138, v11, v23
	v_cvt_pk_bf16_f32 v139, v19, v31
	ds_write_b128 v202, v[136:139] offset:384
	v_cvt_pk_bf16_f32 v136, v27, v47
	s_sext_i32_i8 s2, s2
	v_cvt_pk_bf16_f32 v137, v43, v59
	v_cvt_pk_bf16_f32 v138, v83, v95
	v_cvt_pk_bf16_f32 v139, v103, v107
	ds_write_b128 v203, v[136:139] offset:384
	v_lshl_add_u32 v136, s2, 6, v201
	v_ashrrev_i32_e32 v137, 31, v136
	s_sext_i32_i16 s14, s14
	v_lshlrev_b64 v[136:137], 9, v[136:137]
	v_lshl_add_u64 v[140:141], s[0:1], 0, v[136:137]
	s_lshl_b32 s2, s14, 2
	ds_read_b128 v[136:139], v128
	s_andn2_b32 s2, s2, 63
	s_ashr_i32 s3, s2, 31
	v_lshl_add_u64 v[140:141], s[2:3], 1, v[140:141]
	v_lshl_add_u64 v[148:149], v[140:141], 0, v[194:195]
	ds_read_b128 v[140:143], v128 offset:4096
	s_waitcnt lgkmcnt(1)
	global_store_dwordx4 v[148:149], v[136:139], off nt
	ds_read_b128 v[136:139], v129
	ds_read_b128 v[144:147], v130
	v_add_co_u32_e32 v150, vcc, s22, v148
	s_nop 1
	v_addc_co_u32_e32 v151, vcc, 0, v149, vcc
	s_waitcnt lgkmcnt(1)
	global_store_dwordx4 v[150:151], v[136:139], off offset:-4096 nt
	s_waitcnt lgkmcnt(0)
	global_store_dwordx4 v[150:151], v[144:147], off nt
	ds_read_b128 v[136:139], v131
	ds_read_b128 v[144:147], v132
	v_add_co_u32_e32 v150, vcc, s23, v148
	s_nop 1
	v_addc_co_u32_e32 v151, vcc, 0, v149, vcc
	s_waitcnt lgkmcnt(1)
	global_store_dwordx4 v[150:151], v[136:139], off offset:-4096 nt
	global_store_dwordx4 v[150:151], v[140:143], off nt
	ds_read_b128 v[140:143], v134
	v_add_co_u32_e32 v136, vcc, 0x5000, v148
	s_nop 1
	v_addc_co_u32_e32 v137, vcc, 0, v149, vcc
	s_waitcnt lgkmcnt(1)
	global_store_dwordx4 v[136:137], v[144:147], off nt
	ds_read_b128 v[136:139], v133
	s_nop 0
	v_add_co_u32_e32 v144, vcc, 0x6000, v148
	s_nop 1
	v_addc_co_u32_e32 v145, vcc, 0, v149, vcc
	s_waitcnt lgkmcnt(0)
	global_store_dwordx4 v[144:145], v[136:139], off nt
	s_nop 1
	v_add_co_u32_e32 v136, vcc, 0x7000, v148
	s_nop 1
	v_addc_co_u32_e32 v137, vcc, 0, v149, vcc
	global_store_dwordx4 v[136:137], v[140:143], off nt
	s_andn2_b64 vcc, exec, s[4:5]
	s_cbranch_vccnz .LBB0_198
.LBB0_206:
	s_ashr_i32 s2, s17, 31
	s_lshr_b32 s2, s2, 26
	s_add_i32 s2, s17, s2
	s_and_b32 s2, s2, 0xffc0
	v_cvt_pk_bf16_f32 v136, v108, v36
	s_sub_i32 s2, s17, s2
	v_cvt_pk_bf16_f32 v137, v32, v52
	v_cvt_pk_bf16_f32 v138, v48, v64
	v_cvt_pk_bf16_f32 v139, v60, v72
	ds_write_b128 v202, v[136:139]
	v_cvt_pk_bf16_f32 v136, v68, v88
	s_bfe_i32 s3, s2, 0x80000
	v_cvt_pk_bf16_f32 v137, v84, v96
	v_cvt_pk_bf16_f32 v138, v112, v116
	v_cvt_pk_bf16_f32 v139, v120, v124
	ds_write_b128 v203, v[136:139]
	v_cvt_pk_bf16_f32 v136, v109, v37
	s_bfe_u32 s3, s3, 0x4000b
	v_cvt_pk_bf16_f32 v137, v33, v53
	v_cvt_pk_bf16_f32 v138, v49, v65
	v_cvt_pk_bf16_f32 v139, v61, v73
	ds_write_b128 v202, v[136:139] offset:128
	v_cvt_pk_bf16_f32 v136, v69, v89
	s_add_i32 s3, s2, s3
	v_cvt_pk_bf16_f32 v137, v85, v97
	v_cvt_pk_bf16_f32 v138, v113, v117
	v_cvt_pk_bf16_f32 v139, v121, v125
	ds_write_b128 v203, v[136:139] offset:128
	v_cvt_pk_bf16_f32 v136, v110, v38
	s_bfe_i32 s4, s3, 0x80000
	v_cvt_pk_bf16_f32 v137, v34, v54
	v_cvt_pk_bf16_f32 v138, v50, v66
	v_cvt_pk_bf16_f32 v139, v62, v74
	ds_write_b128 v202, v[136:139] offset:256
	v_cvt_pk_bf16_f32 v136, v70, v90
	s_and_b32 s3, s3, 0xf0
	v_cvt_pk_bf16_f32 v137, v86, v98
	v_cvt_pk_bf16_f32 v138, v114, v118
	v_cvt_pk_bf16_f32 v139, v122, v126
	ds_write_b128 v203, v[136:139] offset:256
	v_cvt_pk_bf16_f32 v136, v111, v39
	s_sub_i32 s2, s2, s3
	v_cvt_pk_bf16_f32 v137, v35, v55
	v_cvt_pk_bf16_f32 v138, v51, v67
	v_cvt_pk_bf16_f32 v139, v63, v75
	ds_write_b128 v202, v[136:139] offset:384
	v_cvt_pk_bf16_f32 v136, v71, v91
	s_sext_i32_i8 s2, s2
	v_cvt_pk_bf16_f32 v137, v87, v99
	v_cvt_pk_bf16_f32 v138, v115, v119
	v_cvt_pk_bf16_f32 v139, v123, v127
	ds_write_b128 v203, v[136:139] offset:384
	v_lshl_add_u32 v136, s2, 6, v201
	v_ashrrev_i32_e32 v137, 31, v136
	s_sext_i32_i16 s4, s4
	v_lshlrev_b64 v[136:137], 9, v[136:137]
	v_lshl_add_u64 v[140:141], s[0:1], 0, v[136:137]
	s_lshl_b32 s2, s4, 2
	ds_read_b128 v[136:139], v128
	s_andn2_b32 s2, s2, 63
	s_ashr_i32 s3, s2, 31
	v_lshl_add_u64 v[140:141], s[2:3], 1, v[140:141]
	v_lshl_add_u64 v[148:149], v[140:141], 0, v[194:195]
	ds_read_b128 v[140:143], v128 offset:4096
	s_waitcnt lgkmcnt(1)
	global_store_dwordx4 v[148:149], v[136:139], off nt
	ds_read_b128 v[136:139], v129
	ds_read_b128 v[144:147], v130
	v_add_co_u32_e32 v128, vcc, s22, v148
	s_nop 1
	v_addc_co_u32_e32 v129, vcc, 0, v149, vcc
	s_waitcnt lgkmcnt(1)
	global_store_dwordx4 v[128:129], v[136:139], off offset:-4096 nt
	s_waitcnt lgkmcnt(0)
	global_store_dwordx4 v[128:129], v[144:147], off nt
	ds_read_b128 v[128:131], v131
	ds_read_b128 v[136:139], v132
	v_add_co_u32_e32 v144, vcc, s23, v148
	s_nop 1
	v_addc_co_u32_e32 v145, vcc, 0, v149, vcc
	s_waitcnt lgkmcnt(1)
	global_store_dwordx4 v[144:145], v[128:131], off offset:-4096 nt
	global_store_dwordx4 v[144:145], v[140:143], off nt
	s_nop 0
	v_add_co_u32_e32 v128, vcc, 0x5000, v148
	s_nop 1
	v_addc_co_u32_e32 v129, vcc, 0, v149, vcc
	s_waitcnt lgkmcnt(0)
	global_store_dwordx4 v[128:129], v[136:139], off nt
	ds_read_b128 v[128:131], v133
	ds_read_b128 v[132:135], v134
	v_add_co_u32_e32 v136, vcc, 0x6000, v148
	s_nop 1
	v_addc_co_u32_e32 v137, vcc, 0, v149, vcc
	s_waitcnt lgkmcnt(1)
	global_store_dwordx4 v[136:137], v[128:131], off nt
	s_nop 1
	v_add_co_u32_e32 v128, vcc, 0x7000, v148
	s_nop 1
	v_addc_co_u32_e32 v129, vcc, 0, v149, vcc
	s_waitcnt lgkmcnt(0)
	global_store_dwordx4 v[128:129], v[132:135], off nt
	s_branch .LBB0_198
